# P6 V sweep also covers all 8 tokens of a group (accumulators of tokens 4-7 parked in registers the epilogue never touches, two row buffers), epilogue runs twice per group
# speedup vs baseline: 1.0592x; 1.0131x over previous
.Lp6_Adone:
	s_waitcnt vmcnt(0)
	v_mov_b32_e32 v184, 0
	v_mov_b32_e32 v185, 0
	v_mov_b64_e32 v[126:127], v[184:185]
	v_mov_b64_e32 v[128:129], v[184:185]
	v_mov_b64_e32 v[130:131], v[184:185]
	v_mov_b64_e32 v[132:133], v[184:185]
	v_mov_b64_e32 v[134:135], v[184:185]
	v_mov_b64_e32 v[136:137], v[184:185]
	v_mov_b64_e32 v[138:139], v[184:185]
	v_mov_b64_e32 v[140:141], v[184:185]
	v_mov_b64_e32 v[110:111], v[184:185]
	v_mov_b64_e32 v[112:113], v[184:185]
	v_mov_b64_e32 v[114:115], v[184:185]
	v_mov_b64_e32 v[116:117], v[184:185]
	v_mov_b64_e32 v[118:119], v[184:185]
	v_mov_b64_e32 v[120:121], v[184:185]
	v_mov_b64_e32 v[122:123], v[184:185]
	v_mov_b64_e32 v[124:125], v[184:185]
	v_mov_b64_e32 v[94:95], v[184:185]
	v_mov_b64_e32 v[96:97], v[184:185]
	v_mov_b64_e32 v[98:99], v[184:185]
	v_mov_b64_e32 v[100:101], v[184:185]
	v_mov_b64_e32 v[102:103], v[184:185]
	v_mov_b64_e32 v[104:105], v[184:185]
	v_mov_b64_e32 v[106:107], v[184:185]
	v_mov_b64_e32 v[108:109], v[184:185]
	v_mov_b64_e32 v[78:79], v[184:185]
	v_mov_b64_e32 v[80:81], v[184:185]
	v_mov_b64_e32 v[82:83], v[184:185]
	v_mov_b64_e32 v[86:87], v[184:185]
	v_mov_b64_e32 v[88:89], v[184:185]
	v_mov_b64_e32 v[90:91], v[184:185]
	v_mov_b64_e32 v[92:93], v[184:185]
	v_mov_b64_e32 v[84:85], v[184:185]
	v_mov_b64_e32 v[144:145], v[184:185]
	v_mov_b64_e32 v[146:147], v[184:185]
	v_mov_b64_e32 v[148:149], v[184:185]
	v_mov_b64_e32 v[150:151], v[184:185]
	v_mov_b64_e32 v[152:153], v[184:185]
	v_mov_b64_e32 v[154:155], v[184:185]
	v_mov_b64_e32 v[156:157], v[184:185]
	v_mov_b64_e32 v[158:159], v[184:185]
	v_mov_b64_e32 v[160:161], v[184:185]
	v_mov_b64_e32 v[162:163], v[184:185]
	v_mov_b64_e32 v[164:165], v[184:185]
	v_mov_b64_e32 v[166:167], v[184:185]
	v_mov_b64_e32 v[168:169], v[184:185]
	v_mov_b64_e32 v[170:171], v[184:185]
	v_mov_b64_e32 v[172:173], v[184:185]
	v_mov_b64_e32 v[174:175], v[184:185]
	v_mov_b64_e32 v[224:225], v[184:185]
	v_mov_b64_e32 v[226:227], v[184:185]
	v_mov_b64_e32 v[228:229], v[184:185]
	v_mov_b64_e32 v[230:231], v[184:185]
	v_mov_b64_e32 v[232:233], v[184:185]
	v_mov_b64_e32 v[234:235], v[184:185]
	v_mov_b64_e32 v[236:237], v[184:185]
	v_mov_b64_e32 v[238:239], v[184:185]
	v_mov_b64_e32 v[240:241], v[184:185]
	v_mov_b64_e32 v[242:243], v[184:185]
	v_mov_b64_e32 v[244:245], v[184:185]
	v_mov_b64_e32 v[246:247], v[184:185]
	v_mov_b64_e32 v[248:249], v[184:185]
	v_mov_b64_e32 v[250:251], v[184:185]
	v_mov_b64_e32 v[216:217], v[184:185]
	v_mov_b64_e32 v[218:219], v[184:185]
	s_add_i32 s3, s22, -1
	s_min_i32 s2, s3, 0
	s_max_i32 s2, s2, 0
	s_lshl_b32 s2, s2, 2
	s_add_i32 s2, s85, s2
	v_mov_b32_e32 v1, s2
	ds_read_b32 v1, v1 offset:4864
	s_waitcnt lgkmcnt(0)
	v_readfirstlane_b32 s26, v1
	s_and_b32 s2, s26, 0x3ff
	s_bfe_u32 s3, s26, 0x4000a
	v_cmp_gt_u32_e32 vcc, s3, v182
	s_lshl_b32 s2, s2, 2
	s_add_i32 s2, s2, s85
	v_cndmask_b32_e32 v1, 0, v182, vcc
	v_lshl_add_u32 v1, v1, 2, s2
	ds_read_b32 v1, v1 offset:8192
	s_waitcnt lgkmcnt(0)
	v_lshlrev_b32_e32 v1, 10, v1
	v_and_b32_e32 v1, 0x3fffc00, v1
	s_nop 0
	v_readlane_b32 s44, v1, 0
	v_readlane_b32 s45, v1, 1
	v_readlane_b32 s46, v1, 2
	v_readlane_b32 s47, v1, 3
	v_readlane_b32 s48, v1, 4
	v_readlane_b32 s49, v1, 5
	v_readlane_b32 s50, v1, 6
	v_readlane_b32 s51, v1, 7
	s_nop 4
	buffer_load_dwordx4 v[68:71], v181, s[92:95], s44 offen
	buffer_load_dwordx4 v[64:67], v181, s[92:95], s45 offen
	buffer_load_dwordx4 v[60:63], v181, s[92:95], s46 offen
	buffer_load_dwordx4 v[56:59], v181, s[92:95], s47 offen
	buffer_load_dwordx4 v[48:51], v181, s[92:95], s48 offen
	buffer_load_dwordx4 v[32:35], v181, s[92:95], s49 offen
	buffer_load_dwordx4 v[16:19], v181, s[92:95], s50 offen
	buffer_load_dwordx4 v[12:15], v181, s[92:95], s51 offen
	s_add_i32 s3, s22, -1
	s_min_i32 s2, s3, 1
	s_max_i32 s2, s2, 0
	s_lshl_b32 s2, s2, 2
	s_add_i32 s2, s85, s2
	v_mov_b32_e32 v1, s2
	ds_read_b32 v1, v1 offset:4864
	s_waitcnt lgkmcnt(0)
	v_readfirstlane_b32 s86, v1
	s_and_b32 s2, s86, 0x3ff
	s_bfe_u32 s3, s86, 0x4000a
	v_cmp_gt_u32_e32 vcc, s3, v182
	s_lshl_b32 s2, s2, 2
	s_add_i32 s2, s2, s85
	v_cndmask_b32_e32 v1, 0, v182, vcc
	v_lshl_add_u32 v1, v1, 2, s2
	ds_read_b32 v1, v1 offset:8192
	s_waitcnt lgkmcnt(0)
	v_lshlrev_b32_e32 v1, 10, v1
	v_and_b32_e32 v1, 0x3fffc00, v1
	s_nop 0
	v_readlane_b32 s44, v1, 0
	v_readlane_b32 s45, v1, 1
	v_readlane_b32 s46, v1, 2
	v_readlane_b32 s47, v1, 3
	v_readlane_b32 s48, v1, 4
	v_readlane_b32 s49, v1, 5
	v_readlane_b32 s50, v1, 6
	v_readlane_b32 s51, v1, 7
	s_nop 4
	buffer_load_dwordx4 v[72:75], v181, s[92:95], s44 offen
	buffer_load_dwordx4 v[52:55], v181, s[92:95], s45 offen
	buffer_load_dwordx4 v[44:47], v181, s[92:95], s46 offen
	buffer_load_dwordx4 v[40:43], v181, s[92:95], s47 offen
	buffer_load_dwordx4 v[36:39], v181, s[92:95], s48 offen
	buffer_load_dwordx4 v[28:31], v181, s[92:95], s49 offen
	buffer_load_dwordx4 v[24:27], v181, s[92:95], s50 offen
	buffer_load_dwordx4 v[20:23], v181, s[92:95], s51 offen
	s_add_i32 s3, s22, -1
	s_min_i32 s2, s3, 2
	s_max_i32 s2, s2, 0
	s_lshl_b32 s2, s2, 2
	s_add_i32 s2, s85, s2
	v_mov_b32_e32 v1, s2
	ds_read_b32 v1, v1 offset:4864
	s_waitcnt lgkmcnt(0)
	v_readfirstlane_b32 s32, v1
	s_mov_b32 s23, 0
.Lp6c0_top:
	s_add_i32 s23, s23, 1
	s_add_i32 s2, s23, 2
	s_add_i32 s3, s22, -1
	s_min_i32 s2, s2, s3
	s_lshl_b32 s2, s2, 2
	s_add_i32 s2, s85, s2
	v_mov_b32_e32 v1, s2
	ds_read_b32 v252, v1 offset:4864
	s_and_b32 s2, s32, 0x3ff
	s_bfe_u32 s3, s32, 0x4000a
	v_cmp_gt_u32_e32 vcc, s3, v182
	s_lshl_b32 s2, s2, 2
	s_add_i32 s2, s2, s85
	v_cndmask_b32_e32 v1, 0, v182, vcc
	v_lshl_add_u32 v1, v1, 2, s2
	ds_read_b32 v1, v1 offset:8192
	s_bfe_u32 s14, s26, 0x4000a
	v_cmp_gt_u32_e32 vcc, s14, v180
	v_mov_b32_e32 v2, 0
	s_and_b32 s2, s26, 0x3ff
	s_lshr_b32 s66, s26, 14
	s_and_saveexec_b64 s[14:15], vcc
	v_add_u32_e32 v210, s2, v180
	v_lshl_add_u32 v210, v210, 2, s85
	ds_read_b32 v2, v210 offset:12288
	s_or_b64 exec, exec, s[14:15]
	s_waitcnt vmcnt(8)
	s_waitcnt lgkmcnt(0)
	v_readfirstlane_b32 s37, v252
	v_lshlrev_b32_e32 v1, 10, v1
	v_and_b32_e32 v1, 0x3fffc00, v1
	s_nop 0
	v_readlane_b32 s44, v1, 0
	v_readlane_b32 s45, v1, 1
	v_readlane_b32 s46, v1, 2
	v_readlane_b32 s47, v1, 3
	v_readlane_b32 s48, v1, 4
	v_readlane_b32 s49, v1, 5
	v_readlane_b32 s50, v1, 6
	v_readlane_b32 s51, v1, 7
	v_mov_b32_e32 v1, v2
	s_bfe_u32 s36, s26, 0x4000a
	s_cmp_eq_u32 s66, 0
	s_cbranch_scc1 .Lp6c0_t0
	s_cmp_eq_u32 s66, 1
	s_cbranch_scc1 .Lp6c0_t1
	s_cmp_eq_u32 s66, 2
	s_cbranch_scc1 .Lp6c0_t2
	s_cmp_eq_u32 s66, 3
	s_cbranch_scc1 .Lp6c0_t3
	s_cmp_eq_u32 s66, 4
	s_cbranch_scc1 .Lp6c0_t4
	s_cmp_eq_u32 s66, 5
	s_cbranch_scc1 .Lp6c0_t5
	s_cmp_eq_u32 s66, 6
	s_cbranch_scc1 .Lp6c0_t6
	s_branch .Lp6c0_t7
.Lp6c0_t0:
	v_readlane_b32 s14, v1, 0
	v_cvt_pk_f32_fp8_e32 v[184:185], v68
	v_cvt_pk_f32_fp8_sdwa v[186:187], v68 src0_sel:WORD_1
	v_pk_fma_f32 v[126:127], v[184:185], s[14:15], v[126:127] op_sel_hi:[1,0,1]
	v_pk_fma_f32 v[128:129], v[186:187], s[14:15], v[128:129] op_sel_hi:[1,0,1]
	v_cvt_pk_f32_fp8_e32 v[188:189], v69
	v_cvt_pk_f32_fp8_sdwa v[190:191], v69 src0_sel:WORD_1
	v_pk_fma_f32 v[130:131], v[188:189], s[14:15], v[130:131] op_sel_hi:[1,0,1]
	v_pk_fma_f32 v[132:133], v[190:191], s[14:15], v[132:133] op_sel_hi:[1,0,1]
	v_cvt_pk_f32_fp8_e32 v[184:185], v70
	v_cvt_pk_f32_fp8_sdwa v[186:187], v70 src0_sel:WORD_1
	v_pk_fma_f32 v[134:135], v[184:185], s[14:15], v[134:135] op_sel_hi:[1,0,1]
	v_pk_fma_f32 v[136:137], v[186:187], s[14:15], v[136:137] op_sel_hi:[1,0,1]
	v_cvt_pk_f32_fp8_e32 v[188:189], v71
	v_cvt_pk_f32_fp8_sdwa v[190:191], v71 src0_sel:WORD_1
	v_pk_fma_f32 v[138:139], v[188:189], s[14:15], v[138:139] op_sel_hi:[1,0,1]
	v_pk_fma_f32 v[140:141], v[190:191], s[14:15], v[140:141] op_sel_hi:[1,0,1]
	v_readlane_b32 s14, v1, 8
	v_cvt_pk_f32_fp8_e32 v[184:185], v64
	v_cvt_pk_f32_fp8_sdwa v[186:187], v64 src0_sel:WORD_1
	v_pk_fma_f32 v[126:127], v[184:185], s[14:15], v[126:127] op_sel_hi:[1,0,1]
	v_pk_fma_f32 v[128:129], v[186:187], s[14:15], v[128:129] op_sel_hi:[1,0,1]
	v_cvt_pk_f32_fp8_e32 v[188:189], v65
	v_cvt_pk_f32_fp8_sdwa v[190:191], v65 src0_sel:WORD_1
	v_pk_fma_f32 v[130:131], v[188:189], s[14:15], v[130:131] op_sel_hi:[1,0,1]
	v_pk_fma_f32 v[132:133], v[190:191], s[14:15], v[132:133] op_sel_hi:[1,0,1]
	v_cvt_pk_f32_fp8_e32 v[184:185], v66
	v_cvt_pk_f32_fp8_sdwa v[186:187], v66 src0_sel:WORD_1
	v_pk_fma_f32 v[134:135], v[184:185], s[14:15], v[134:135] op_sel_hi:[1,0,1]
	v_pk_fma_f32 v[136:137], v[186:187], s[14:15], v[136:137] op_sel_hi:[1,0,1]
	v_cvt_pk_f32_fp8_e32 v[188:189], v67
	v_cvt_pk_f32_fp8_sdwa v[190:191], v67 src0_sel:WORD_1
	v_pk_fma_f32 v[138:139], v[188:189], s[14:15], v[138:139] op_sel_hi:[1,0,1]
	v_pk_fma_f32 v[140:141], v[190:191], s[14:15], v[140:141] op_sel_hi:[1,0,1]
	s_cmp_le_u32 s36, 2
	s_cbranch_scc1 .Lp6c0_axdone
	v_readlane_b32 s14, v1, 16
	v_cvt_pk_f32_fp8_e32 v[184:185], v60
	v_cvt_pk_f32_fp8_sdwa v[186:187], v60 src0_sel:WORD_1
	v_pk_fma_f32 v[126:127], v[184:185], s[14:15], v[126:127] op_sel_hi:[1,0,1]
	v_pk_fma_f32 v[128:129], v[186:187], s[14:15], v[128:129] op_sel_hi:[1,0,1]
	v_cvt_pk_f32_fp8_e32 v[188:189], v61
	v_cvt_pk_f32_fp8_sdwa v[190:191], v61 src0_sel:WORD_1
	v_pk_fma_f32 v[130:131], v[188:189], s[14:15], v[130:131] op_sel_hi:[1,0,1]
	v_pk_fma_f32 v[132:133], v[190:191], s[14:15], v[132:133] op_sel_hi:[1,0,1]
	v_cvt_pk_f32_fp8_e32 v[184:185], v62
	v_cvt_pk_f32_fp8_sdwa v[186:187], v62 src0_sel:WORD_1
	v_pk_fma_f32 v[134:135], v[184:185], s[14:15], v[134:135] op_sel_hi:[1,0,1]
	v_pk_fma_f32 v[136:137], v[186:187], s[14:15], v[136:137] op_sel_hi:[1,0,1]
	v_cvt_pk_f32_fp8_e32 v[188:189], v63
	v_cvt_pk_f32_fp8_sdwa v[190:191], v63 src0_sel:WORD_1
	v_pk_fma_f32 v[138:139], v[188:189], s[14:15], v[138:139] op_sel_hi:[1,0,1]
	v_pk_fma_f32 v[140:141], v[190:191], s[14:15], v[140:141] op_sel_hi:[1,0,1]
	v_readlane_b32 s14, v1, 24
	v_cvt_pk_f32_fp8_e32 v[184:185], v56
	v_cvt_pk_f32_fp8_sdwa v[186:187], v56 src0_sel:WORD_1
	v_pk_fma_f32 v[126:127], v[184:185], s[14:15], v[126:127] op_sel_hi:[1,0,1]
	v_pk_fma_f32 v[128:129], v[186:187], s[14:15], v[128:129] op_sel_hi:[1,0,1]
	v_cvt_pk_f32_fp8_e32 v[188:189], v57
	v_cvt_pk_f32_fp8_sdwa v[190:191], v57 src0_sel:WORD_1
	v_pk_fma_f32 v[130:131], v[188:189], s[14:15], v[130:131] op_sel_hi:[1,0,1]
	v_pk_fma_f32 v[132:133], v[190:191], s[14:15], v[132:133] op_sel_hi:[1,0,1]
	v_cvt_pk_f32_fp8_e32 v[184:185], v58
	v_cvt_pk_f32_fp8_sdwa v[186:187], v58 src0_sel:WORD_1
	v_pk_fma_f32 v[134:135], v[184:185], s[14:15], v[134:135] op_sel_hi:[1,0,1]
	v_pk_fma_f32 v[136:137], v[186:187], s[14:15], v[136:137] op_sel_hi:[1,0,1]
	v_cvt_pk_f32_fp8_e32 v[188:189], v59
	v_cvt_pk_f32_fp8_sdwa v[190:191], v59 src0_sel:WORD_1
	v_pk_fma_f32 v[138:139], v[188:189], s[14:15], v[138:139] op_sel_hi:[1,0,1]
	v_pk_fma_f32 v[140:141], v[190:191], s[14:15], v[140:141] op_sel_hi:[1,0,1]
	s_cmp_le_u32 s36, 4
	s_cbranch_scc1 .Lp6c0_axdone
	v_readlane_b32 s14, v1, 32
	v_cvt_pk_f32_fp8_e32 v[184:185], v48
	v_cvt_pk_f32_fp8_sdwa v[186:187], v48 src0_sel:WORD_1
	v_pk_fma_f32 v[126:127], v[184:185], s[14:15], v[126:127] op_sel_hi:[1,0,1]
	v_pk_fma_f32 v[128:129], v[186:187], s[14:15], v[128:129] op_sel_hi:[1,0,1]
	v_cvt_pk_f32_fp8_e32 v[188:189], v49
	v_cvt_pk_f32_fp8_sdwa v[190:191], v49 src0_sel:WORD_1
	v_pk_fma_f32 v[130:131], v[188:189], s[14:15], v[130:131] op_sel_hi:[1,0,1]
	v_pk_fma_f32 v[132:133], v[190:191], s[14:15], v[132:133] op_sel_hi:[1,0,1]
	v_cvt_pk_f32_fp8_e32 v[184:185], v50
	v_cvt_pk_f32_fp8_sdwa v[186:187], v50 src0_sel:WORD_1
	v_pk_fma_f32 v[134:135], v[184:185], s[14:15], v[134:135] op_sel_hi:[1,0,1]
	v_pk_fma_f32 v[136:137], v[186:187], s[14:15], v[136:137] op_sel_hi:[1,0,1]
	v_cvt_pk_f32_fp8_e32 v[188:189], v51
	v_cvt_pk_f32_fp8_sdwa v[190:191], v51 src0_sel:WORD_1
	v_pk_fma_f32 v[138:139], v[188:189], s[14:15], v[138:139] op_sel_hi:[1,0,1]
	v_pk_fma_f32 v[140:141], v[190:191], s[14:15], v[140:141] op_sel_hi:[1,0,1]
	v_readlane_b32 s14, v1, 40
	v_cvt_pk_f32_fp8_e32 v[184:185], v32
	v_cvt_pk_f32_fp8_sdwa v[186:187], v32 src0_sel:WORD_1
	v_pk_fma_f32 v[126:127], v[184:185], s[14:15], v[126:127] op_sel_hi:[1,0,1]
	v_pk_fma_f32 v[128:129], v[186:187], s[14:15], v[128:129] op_sel_hi:[1,0,1]
	v_cvt_pk_f32_fp8_e32 v[188:189], v33
	v_cvt_pk_f32_fp8_sdwa v[190:191], v33 src0_sel:WORD_1
	v_pk_fma_f32 v[130:131], v[188:189], s[14:15], v[130:131] op_sel_hi:[1,0,1]
	v_pk_fma_f32 v[132:133], v[190:191], s[14:15], v[132:133] op_sel_hi:[1,0,1]
	v_cvt_pk_f32_fp8_e32 v[184:185], v34
	v_cvt_pk_f32_fp8_sdwa v[186:187], v34 src0_sel:WORD_1
	v_pk_fma_f32 v[134:135], v[184:185], s[14:15], v[134:135] op_sel_hi:[1,0,1]
	v_pk_fma_f32 v[136:137], v[186:187], s[14:15], v[136:137] op_sel_hi:[1,0,1]
	v_cvt_pk_f32_fp8_e32 v[188:189], v35
	v_cvt_pk_f32_fp8_sdwa v[190:191], v35 src0_sel:WORD_1
	v_pk_fma_f32 v[138:139], v[188:189], s[14:15], v[138:139] op_sel_hi:[1,0,1]
	v_pk_fma_f32 v[140:141], v[190:191], s[14:15], v[140:141] op_sel_hi:[1,0,1]
	s_cmp_le_u32 s36, 6
	s_cbranch_scc1 .Lp6c0_axdone
	v_readlane_b32 s14, v1, 48
	v_cvt_pk_f32_fp8_e32 v[184:185], v16
	v_cvt_pk_f32_fp8_sdwa v[186:187], v16 src0_sel:WORD_1
	v_pk_fma_f32 v[126:127], v[184:185], s[14:15], v[126:127] op_sel_hi:[1,0,1]
	v_pk_fma_f32 v[128:129], v[186:187], s[14:15], v[128:129] op_sel_hi:[1,0,1]
	v_cvt_pk_f32_fp8_e32 v[188:189], v17
	v_cvt_pk_f32_fp8_sdwa v[190:191], v17 src0_sel:WORD_1
	v_pk_fma_f32 v[130:131], v[188:189], s[14:15], v[130:131] op_sel_hi:[1,0,1]
	v_pk_fma_f32 v[132:133], v[190:191], s[14:15], v[132:133] op_sel_hi:[1,0,1]
	v_cvt_pk_f32_fp8_e32 v[184:185], v18
	v_cvt_pk_f32_fp8_sdwa v[186:187], v18 src0_sel:WORD_1
	v_pk_fma_f32 v[134:135], v[184:185], s[14:15], v[134:135] op_sel_hi:[1,0,1]
	v_pk_fma_f32 v[136:137], v[186:187], s[14:15], v[136:137] op_sel_hi:[1,0,1]
	v_cvt_pk_f32_fp8_e32 v[188:189], v19
	v_cvt_pk_f32_fp8_sdwa v[190:191], v19 src0_sel:WORD_1
	v_pk_fma_f32 v[138:139], v[188:189], s[14:15], v[138:139] op_sel_hi:[1,0,1]
	v_pk_fma_f32 v[140:141], v[190:191], s[14:15], v[140:141] op_sel_hi:[1,0,1]
	v_readlane_b32 s14, v1, 56
	v_cvt_pk_f32_fp8_e32 v[184:185], v12
	v_cvt_pk_f32_fp8_sdwa v[186:187], v12 src0_sel:WORD_1
	v_pk_fma_f32 v[126:127], v[184:185], s[14:15], v[126:127] op_sel_hi:[1,0,1]
	v_pk_fma_f32 v[128:129], v[186:187], s[14:15], v[128:129] op_sel_hi:[1,0,1]
	v_cvt_pk_f32_fp8_e32 v[188:189], v13
	v_cvt_pk_f32_fp8_sdwa v[190:191], v13 src0_sel:WORD_1
	v_pk_fma_f32 v[130:131], v[188:189], s[14:15], v[130:131] op_sel_hi:[1,0,1]
	v_pk_fma_f32 v[132:133], v[190:191], s[14:15], v[132:133] op_sel_hi:[1,0,1]
	v_cvt_pk_f32_fp8_e32 v[184:185], v14
	v_cvt_pk_f32_fp8_sdwa v[186:187], v14 src0_sel:WORD_1
	v_pk_fma_f32 v[134:135], v[184:185], s[14:15], v[134:135] op_sel_hi:[1,0,1]
	v_pk_fma_f32 v[136:137], v[186:187], s[14:15], v[136:137] op_sel_hi:[1,0,1]
	v_cvt_pk_f32_fp8_e32 v[188:189], v15
	v_cvt_pk_f32_fp8_sdwa v[190:191], v15 src0_sel:WORD_1
	v_pk_fma_f32 v[138:139], v[188:189], s[14:15], v[138:139] op_sel_hi:[1,0,1]
	v_pk_fma_f32 v[140:141], v[190:191], s[14:15], v[140:141] op_sel_hi:[1,0,1]
	s_branch .Lp6c0_axdone
.Lp6c0_t1:
	v_readlane_b32 s14, v1, 0
	v_cvt_pk_f32_fp8_e32 v[184:185], v68
	v_cvt_pk_f32_fp8_sdwa v[186:187], v68 src0_sel:WORD_1
	v_pk_fma_f32 v[110:111], v[184:185], s[14:15], v[110:111] op_sel_hi:[1,0,1]
	v_pk_fma_f32 v[112:113], v[186:187], s[14:15], v[112:113] op_sel_hi:[1,0,1]
	v_cvt_pk_f32_fp8_e32 v[188:189], v69
	v_cvt_pk_f32_fp8_sdwa v[190:191], v69 src0_sel:WORD_1
	v_pk_fma_f32 v[114:115], v[188:189], s[14:15], v[114:115] op_sel_hi:[1,0,1]
	v_pk_fma_f32 v[116:117], v[190:191], s[14:15], v[116:117] op_sel_hi:[1,0,1]
	v_cvt_pk_f32_fp8_e32 v[184:185], v70
	v_cvt_pk_f32_fp8_sdwa v[186:187], v70 src0_sel:WORD_1
	v_pk_fma_f32 v[118:119], v[184:185], s[14:15], v[118:119] op_sel_hi:[1,0,1]
	v_pk_fma_f32 v[120:121], v[186:187], s[14:15], v[120:121] op_sel_hi:[1,0,1]
	v_cvt_pk_f32_fp8_e32 v[188:189], v71
	v_cvt_pk_f32_fp8_sdwa v[190:191], v71 src0_sel:WORD_1
	v_pk_fma_f32 v[122:123], v[188:189], s[14:15], v[122:123] op_sel_hi:[1,0,1]
	v_pk_fma_f32 v[124:125], v[190:191], s[14:15], v[124:125] op_sel_hi:[1,0,1]
	v_readlane_b32 s14, v1, 8
	v_cvt_pk_f32_fp8_e32 v[184:185], v64
	v_cvt_pk_f32_fp8_sdwa v[186:187], v64 src0_sel:WORD_1
	v_pk_fma_f32 v[110:111], v[184:185], s[14:15], v[110:111] op_sel_hi:[1,0,1]
	v_pk_fma_f32 v[112:113], v[186:187], s[14:15], v[112:113] op_sel_hi:[1,0,1]
	v_cvt_pk_f32_fp8_e32 v[188:189], v65
	v_cvt_pk_f32_fp8_sdwa v[190:191], v65 src0_sel:WORD_1
	v_pk_fma_f32 v[114:115], v[188:189], s[14:15], v[114:115] op_sel_hi:[1,0,1]
	v_pk_fma_f32 v[116:117], v[190:191], s[14:15], v[116:117] op_sel_hi:[1,0,1]
	v_cvt_pk_f32_fp8_e32 v[184:185], v66
	v_cvt_pk_f32_fp8_sdwa v[186:187], v66 src0_sel:WORD_1
	v_pk_fma_f32 v[118:119], v[184:185], s[14:15], v[118:119] op_sel_hi:[1,0,1]
	v_pk_fma_f32 v[120:121], v[186:187], s[14:15], v[120:121] op_sel_hi:[1,0,1]
	v_cvt_pk_f32_fp8_e32 v[188:189], v67
	v_cvt_pk_f32_fp8_sdwa v[190:191], v67 src0_sel:WORD_1
	v_pk_fma_f32 v[122:123], v[188:189], s[14:15], v[122:123] op_sel_hi:[1,0,1]
	v_pk_fma_f32 v[124:125], v[190:191], s[14:15], v[124:125] op_sel_hi:[1,0,1]
	s_cmp_le_u32 s36, 2
	s_cbranch_scc1 .Lp6c0_axdone
	v_readlane_b32 s14, v1, 16
	v_cvt_pk_f32_fp8_e32 v[184:185], v60
	v_cvt_pk_f32_fp8_sdwa v[186:187], v60 src0_sel:WORD_1
	v_pk_fma_f32 v[110:111], v[184:185], s[14:15], v[110:111] op_sel_hi:[1,0,1]
	v_pk_fma_f32 v[112:113], v[186:187], s[14:15], v[112:113] op_sel_hi:[1,0,1]
	v_cvt_pk_f32_fp8_e32 v[188:189], v61
	v_cvt_pk_f32_fp8_sdwa v[190:191], v61 src0_sel:WORD_1
	v_pk_fma_f32 v[114:115], v[188:189], s[14:15], v[114:115] op_sel_hi:[1,0,1]
	v_pk_fma_f32 v[116:117], v[190:191], s[14:15], v[116:117] op_sel_hi:[1,0,1]
	v_cvt_pk_f32_fp8_e32 v[184:185], v62
	v_cvt_pk_f32_fp8_sdwa v[186:187], v62 src0_sel:WORD_1
	v_pk_fma_f32 v[118:119], v[184:185], s[14:15], v[118:119] op_sel_hi:[1,0,1]
	v_pk_fma_f32 v[120:121], v[186:187], s[14:15], v[120:121] op_sel_hi:[1,0,1]
	v_cvt_pk_f32_fp8_e32 v[188:189], v63
	v_cvt_pk_f32_fp8_sdwa v[190:191], v63 src0_sel:WORD_1
	v_pk_fma_f32 v[122:123], v[188:189], s[14:15], v[122:123] op_sel_hi:[1,0,1]
	v_pk_fma_f32 v[124:125], v[190:191], s[14:15], v[124:125] op_sel_hi:[1,0,1]
	v_readlane_b32 s14, v1, 24
	v_cvt_pk_f32_fp8_e32 v[184:185], v56
	v_cvt_pk_f32_fp8_sdwa v[186:187], v56 src0_sel:WORD_1
	v_pk_fma_f32 v[110:111], v[184:185], s[14:15], v[110:111] op_sel_hi:[1,0,1]
	v_pk_fma_f32 v[112:113], v[186:187], s[14:15], v[112:113] op_sel_hi:[1,0,1]
	v_cvt_pk_f32_fp8_e32 v[188:189], v57
	v_cvt_pk_f32_fp8_sdwa v[190:191], v57 src0_sel:WORD_1
	v_pk_fma_f32 v[114:115], v[188:189], s[14:15], v[114:115] op_sel_hi:[1,0,1]
	v_pk_fma_f32 v[116:117], v[190:191], s[14:15], v[116:117] op_sel_hi:[1,0,1]
	v_cvt_pk_f32_fp8_e32 v[184:185], v58
	v_cvt_pk_f32_fp8_sdwa v[186:187], v58 src0_sel:WORD_1
	v_pk_fma_f32 v[118:119], v[184:185], s[14:15], v[118:119] op_sel_hi:[1,0,1]
	v_pk_fma_f32 v[120:121], v[186:187], s[14:15], v[120:121] op_sel_hi:[1,0,1]
	v_cvt_pk_f32_fp8_e32 v[188:189], v59
	v_cvt_pk_f32_fp8_sdwa v[190:191], v59 src0_sel:WORD_1
	v_pk_fma_f32 v[122:123], v[188:189], s[14:15], v[122:123] op_sel_hi:[1,0,1]
	v_pk_fma_f32 v[124:125], v[190:191], s[14:15], v[124:125] op_sel_hi:[1,0,1]
	s_cmp_le_u32 s36, 4
	s_cbranch_scc1 .Lp6c0_axdone
	v_readlane_b32 s14, v1, 32
	v_cvt_pk_f32_fp8_e32 v[184:185], v48
	v_cvt_pk_f32_fp8_sdwa v[186:187], v48 src0_sel:WORD_1
	v_pk_fma_f32 v[110:111], v[184:185], s[14:15], v[110:111] op_sel_hi:[1,0,1]
	v_pk_fma_f32 v[112:113], v[186:187], s[14:15], v[112:113] op_sel_hi:[1,0,1]
	v_cvt_pk_f32_fp8_e32 v[188:189], v49
	v_cvt_pk_f32_fp8_sdwa v[190:191], v49 src0_sel:WORD_1
	v_pk_fma_f32 v[114:115], v[188:189], s[14:15], v[114:115] op_sel_hi:[1,0,1]
	v_pk_fma_f32 v[116:117], v[190:191], s[14:15], v[116:117] op_sel_hi:[1,0,1]
	v_cvt_pk_f32_fp8_e32 v[184:185], v50
	v_cvt_pk_f32_fp8_sdwa v[186:187], v50 src0_sel:WORD_1
	v_pk_fma_f32 v[118:119], v[184:185], s[14:15], v[118:119] op_sel_hi:[1,0,1]
	v_pk_fma_f32 v[120:121], v[186:187], s[14:15], v[120:121] op_sel_hi:[1,0,1]
	v_cvt_pk_f32_fp8_e32 v[188:189], v51
	v_cvt_pk_f32_fp8_sdwa v[190:191], v51 src0_sel:WORD_1
	v_pk_fma_f32 v[122:123], v[188:189], s[14:15], v[122:123] op_sel_hi:[1,0,1]
	v_pk_fma_f32 v[124:125], v[190:191], s[14:15], v[124:125] op_sel_hi:[1,0,1]
	v_readlane_b32 s14, v1, 40
	v_cvt_pk_f32_fp8_e32 v[184:185], v32
	v_cvt_pk_f32_fp8_sdwa v[186:187], v32 src0_sel:WORD_1
	v_pk_fma_f32 v[110:111], v[184:185], s[14:15], v[110:111] op_sel_hi:[1,0,1]
	v_pk_fma_f32 v[112:113], v[186:187], s[14:15], v[112:113] op_sel_hi:[1,0,1]
	v_cvt_pk_f32_fp8_e32 v[188:189], v33
	v_cvt_pk_f32_fp8_sdwa v[190:191], v33 src0_sel:WORD_1
	v_pk_fma_f32 v[114:115], v[188:189], s[14:15], v[114:115] op_sel_hi:[1,0,1]
	v_pk_fma_f32 v[116:117], v[190:191], s[14:15], v[116:117] op_sel_hi:[1,0,1]
	v_cvt_pk_f32_fp8_e32 v[184:185], v34
	v_cvt_pk_f32_fp8_sdwa v[186:187], v34 src0_sel:WORD_1
	v_pk_fma_f32 v[118:119], v[184:185], s[14:15], v[118:119] op_sel_hi:[1,0,1]
	v_pk_fma_f32 v[120:121], v[186:187], s[14:15], v[120:121] op_sel_hi:[1,0,1]
	v_cvt_pk_f32_fp8_e32 v[188:189], v35
	v_cvt_pk_f32_fp8_sdwa v[190:191], v35 src0_sel:WORD_1
	v_pk_fma_f32 v[122:123], v[188:189], s[14:15], v[122:123] op_sel_hi:[1,0,1]
	v_pk_fma_f32 v[124:125], v[190:191], s[14:15], v[124:125] op_sel_hi:[1,0,1]
	s_cmp_le_u32 s36, 6
	s_cbranch_scc1 .Lp6c0_axdone
	v_readlane_b32 s14, v1, 48
	v_cvt_pk_f32_fp8_e32 v[184:185], v16
	v_cvt_pk_f32_fp8_sdwa v[186:187], v16 src0_sel:WORD_1
	v_pk_fma_f32 v[110:111], v[184:185], s[14:15], v[110:111] op_sel_hi:[1,0,1]
	v_pk_fma_f32 v[112:113], v[186:187], s[14:15], v[112:113] op_sel_hi:[1,0,1]
	v_cvt_pk_f32_fp8_e32 v[188:189], v17
	v_cvt_pk_f32_fp8_sdwa v[190:191], v17 src0_sel:WORD_1
	v_pk_fma_f32 v[114:115], v[188:189], s[14:15], v[114:115] op_sel_hi:[1,0,1]
	v_pk_fma_f32 v[116:117], v[190:191], s[14:15], v[116:117] op_sel_hi:[1,0,1]
	v_cvt_pk_f32_fp8_e32 v[184:185], v18
	v_cvt_pk_f32_fp8_sdwa v[186:187], v18 src0_sel:WORD_1
	v_pk_fma_f32 v[118:119], v[184:185], s[14:15], v[118:119] op_sel_hi:[1,0,1]
	v_pk_fma_f32 v[120:121], v[186:187], s[14:15], v[120:121] op_sel_hi:[1,0,1]
	v_cvt_pk_f32_fp8_e32 v[188:189], v19
	v_cvt_pk_f32_fp8_sdwa v[190:191], v19 src0_sel:WORD_1
	v_pk_fma_f32 v[122:123], v[188:189], s[14:15], v[122:123] op_sel_hi:[1,0,1]
	v_pk_fma_f32 v[124:125], v[190:191], s[14:15], v[124:125] op_sel_hi:[1,0,1]
	v_readlane_b32 s14, v1, 56
	v_cvt_pk_f32_fp8_e32 v[184:185], v12
	v_cvt_pk_f32_fp8_sdwa v[186:187], v12 src0_sel:WORD_1
	v_pk_fma_f32 v[110:111], v[184:185], s[14:15], v[110:111] op_sel_hi:[1,0,1]
	v_pk_fma_f32 v[112:113], v[186:187], s[14:15], v[112:113] op_sel_hi:[1,0,1]
	v_cvt_pk_f32_fp8_e32 v[188:189], v13
	v_cvt_pk_f32_fp8_sdwa v[190:191], v13 src0_sel:WORD_1
	v_pk_fma_f32 v[114:115], v[188:189], s[14:15], v[114:115] op_sel_hi:[1,0,1]
	v_pk_fma_f32 v[116:117], v[190:191], s[14:15], v[116:117] op_sel_hi:[1,0,1]
	v_cvt_pk_f32_fp8_e32 v[184:185], v14
	v_cvt_pk_f32_fp8_sdwa v[186:187], v14 src0_sel:WORD_1
	v_pk_fma_f32 v[118:119], v[184:185], s[14:15], v[118:119] op_sel_hi:[1,0,1]
	v_pk_fma_f32 v[120:121], v[186:187], s[14:15], v[120:121] op_sel_hi:[1,0,1]
	v_cvt_pk_f32_fp8_e32 v[188:189], v15
	v_cvt_pk_f32_fp8_sdwa v[190:191], v15 src0_sel:WORD_1
	v_pk_fma_f32 v[122:123], v[188:189], s[14:15], v[122:123] op_sel_hi:[1,0,1]
	v_pk_fma_f32 v[124:125], v[190:191], s[14:15], v[124:125] op_sel_hi:[1,0,1]
	s_branch .Lp6c0_axdone
.Lp6c0_t2:
	v_readlane_b32 s14, v1, 0
	v_cvt_pk_f32_fp8_e32 v[184:185], v68
	v_cvt_pk_f32_fp8_sdwa v[186:187], v68 src0_sel:WORD_1
	v_pk_fma_f32 v[94:95], v[184:185], s[14:15], v[94:95] op_sel_hi:[1,0,1]
	v_pk_fma_f32 v[96:97], v[186:187], s[14:15], v[96:97] op_sel_hi:[1,0,1]
	v_cvt_pk_f32_fp8_e32 v[188:189], v69
	v_cvt_pk_f32_fp8_sdwa v[190:191], v69 src0_sel:WORD_1
	v_pk_fma_f32 v[98:99], v[188:189], s[14:15], v[98:99] op_sel_hi:[1,0,1]
	v_pk_fma_f32 v[100:101], v[190:191], s[14:15], v[100:101] op_sel_hi:[1,0,1]
	v_cvt_pk_f32_fp8_e32 v[184:185], v70
	v_cvt_pk_f32_fp8_sdwa v[186:187], v70 src0_sel:WORD_1
	v_pk_fma_f32 v[102:103], v[184:185], s[14:15], v[102:103] op_sel_hi:[1,0,1]
	v_pk_fma_f32 v[104:105], v[186:187], s[14:15], v[104:105] op_sel_hi:[1,0,1]
	v_cvt_pk_f32_fp8_e32 v[188:189], v71
	v_cvt_pk_f32_fp8_sdwa v[190:191], v71 src0_sel:WORD_1
	v_pk_fma_f32 v[106:107], v[188:189], s[14:15], v[106:107] op_sel_hi:[1,0,1]
	v_pk_fma_f32 v[108:109], v[190:191], s[14:15], v[108:109] op_sel_hi:[1,0,1]
	v_readlane_b32 s14, v1, 8
	v_cvt_pk_f32_fp8_e32 v[184:185], v64
	v_cvt_pk_f32_fp8_sdwa v[186:187], v64 src0_sel:WORD_1
	v_pk_fma_f32 v[94:95], v[184:185], s[14:15], v[94:95] op_sel_hi:[1,0,1]
	v_pk_fma_f32 v[96:97], v[186:187], s[14:15], v[96:97] op_sel_hi:[1,0,1]
	v_cvt_pk_f32_fp8_e32 v[188:189], v65
	v_cvt_pk_f32_fp8_sdwa v[190:191], v65 src0_sel:WORD_1
	v_pk_fma_f32 v[98:99], v[188:189], s[14:15], v[98:99] op_sel_hi:[1,0,1]
	v_pk_fma_f32 v[100:101], v[190:191], s[14:15], v[100:101] op_sel_hi:[1,0,1]
	v_cvt_pk_f32_fp8_e32 v[184:185], v66
	v_cvt_pk_f32_fp8_sdwa v[186:187], v66 src0_sel:WORD_1
	v_pk_fma_f32 v[102:103], v[184:185], s[14:15], v[102:103] op_sel_hi:[1,0,1]
	v_pk_fma_f32 v[104:105], v[186:187], s[14:15], v[104:105] op_sel_hi:[1,0,1]
	v_cvt_pk_f32_fp8_e32 v[188:189], v67
	v_cvt_pk_f32_fp8_sdwa v[190:191], v67 src0_sel:WORD_1
	v_pk_fma_f32 v[106:107], v[188:189], s[14:15], v[106:107] op_sel_hi:[1,0,1]
	v_pk_fma_f32 v[108:109], v[190:191], s[14:15], v[108:109] op_sel_hi:[1,0,1]
	s_cmp_le_u32 s36, 2
	s_cbranch_scc1 .Lp6c0_axdone
	v_readlane_b32 s14, v1, 16
	v_cvt_pk_f32_fp8_e32 v[184:185], v60
	v_cvt_pk_f32_fp8_sdwa v[186:187], v60 src0_sel:WORD_1
	v_pk_fma_f32 v[94:95], v[184:185], s[14:15], v[94:95] op_sel_hi:[1,0,1]
	v_pk_fma_f32 v[96:97], v[186:187], s[14:15], v[96:97] op_sel_hi:[1,0,1]
	v_cvt_pk_f32_fp8_e32 v[188:189], v61
	v_cvt_pk_f32_fp8_sdwa v[190:191], v61 src0_sel:WORD_1
	v_pk_fma_f32 v[98:99], v[188:189], s[14:15], v[98:99] op_sel_hi:[1,0,1]
	v_pk_fma_f32 v[100:101], v[190:191], s[14:15], v[100:101] op_sel_hi:[1,0,1]
	v_cvt_pk_f32_fp8_e32 v[184:185], v62
	v_cvt_pk_f32_fp8_sdwa v[186:187], v62 src0_sel:WORD_1
	v_pk_fma_f32 v[102:103], v[184:185], s[14:15], v[102:103] op_sel_hi:[1,0,1]
	v_pk_fma_f32 v[104:105], v[186:187], s[14:15], v[104:105] op_sel_hi:[1,0,1]
	v_cvt_pk_f32_fp8_e32 v[188:189], v63
	v_cvt_pk_f32_fp8_sdwa v[190:191], v63 src0_sel:WORD_1
	v_pk_fma_f32 v[106:107], v[188:189], s[14:15], v[106:107] op_sel_hi:[1,0,1]
	v_pk_fma_f32 v[108:109], v[190:191], s[14:15], v[108:109] op_sel_hi:[1,0,1]
	v_readlane_b32 s14, v1, 24
	v_cvt_pk_f32_fp8_e32 v[184:185], v56
	v_cvt_pk_f32_fp8_sdwa v[186:187], v56 src0_sel:WORD_1
	v_pk_fma_f32 v[94:95], v[184:185], s[14:15], v[94:95] op_sel_hi:[1,0,1]
	v_pk_fma_f32 v[96:97], v[186:187], s[14:15], v[96:97] op_sel_hi:[1,0,1]
	v_cvt_pk_f32_fp8_e32 v[188:189], v57
	v_cvt_pk_f32_fp8_sdwa v[190:191], v57 src0_sel:WORD_1
	v_pk_fma_f32 v[98:99], v[188:189], s[14:15], v[98:99] op_sel_hi:[1,0,1]
	v_pk_fma_f32 v[100:101], v[190:191], s[14:15], v[100:101] op_sel_hi:[1,0,1]
	v_cvt_pk_f32_fp8_e32 v[184:185], v58
	v_cvt_pk_f32_fp8_sdwa v[186:187], v58 src0_sel:WORD_1
	v_pk_fma_f32 v[102:103], v[184:185], s[14:15], v[102:103] op_sel_hi:[1,0,1]
	v_pk_fma_f32 v[104:105], v[186:187], s[14:15], v[104:105] op_sel_hi:[1,0,1]
	v_cvt_pk_f32_fp8_e32 v[188:189], v59
	v_cvt_pk_f32_fp8_sdwa v[190:191], v59 src0_sel:WORD_1
	v_pk_fma_f32 v[106:107], v[188:189], s[14:15], v[106:107] op_sel_hi:[1,0,1]
	v_pk_fma_f32 v[108:109], v[190:191], s[14:15], v[108:109] op_sel_hi:[1,0,1]
	s_cmp_le_u32 s36, 4
	s_cbranch_scc1 .Lp6c0_axdone
	v_readlane_b32 s14, v1, 32
	v_cvt_pk_f32_fp8_e32 v[184:185], v48
	v_cvt_pk_f32_fp8_sdwa v[186:187], v48 src0_sel:WORD_1
	v_pk_fma_f32 v[94:95], v[184:185], s[14:15], v[94:95] op_sel_hi:[1,0,1]
	v_pk_fma_f32 v[96:97], v[186:187], s[14:15], v[96:97] op_sel_hi:[1,0,1]
	v_cvt_pk_f32_fp8_e32 v[188:189], v49
	v_cvt_pk_f32_fp8_sdwa v[190:191], v49 src0_sel:WORD_1
	v_pk_fma_f32 v[98:99], v[188:189], s[14:15], v[98:99] op_sel_hi:[1,0,1]
	v_pk_fma_f32 v[100:101], v[190:191], s[14:15], v[100:101] op_sel_hi:[1,0,1]
	v_cvt_pk_f32_fp8_e32 v[184:185], v50
	v_cvt_pk_f32_fp8_sdwa v[186:187], v50 src0_sel:WORD_1
	v_pk_fma_f32 v[102:103], v[184:185], s[14:15], v[102:103] op_sel_hi:[1,0,1]
	v_pk_fma_f32 v[104:105], v[186:187], s[14:15], v[104:105] op_sel_hi:[1,0,1]
	v_cvt_pk_f32_fp8_e32 v[188:189], v51
	v_cvt_pk_f32_fp8_sdwa v[190:191], v51 src0_sel:WORD_1
	v_pk_fma_f32 v[106:107], v[188:189], s[14:15], v[106:107] op_sel_hi:[1,0,1]
	v_pk_fma_f32 v[108:109], v[190:191], s[14:15], v[108:109] op_sel_hi:[1,0,1]
	v_readlane_b32 s14, v1, 40
	v_cvt_pk_f32_fp8_e32 v[184:185], v32
	v_cvt_pk_f32_fp8_sdwa v[186:187], v32 src0_sel:WORD_1
	v_pk_fma_f32 v[94:95], v[184:185], s[14:15], v[94:95] op_sel_hi:[1,0,1]
	v_pk_fma_f32 v[96:97], v[186:187], s[14:15], v[96:97] op_sel_hi:[1,0,1]
	v_cvt_pk_f32_fp8_e32 v[188:189], v33
	v_cvt_pk_f32_fp8_sdwa v[190:191], v33 src0_sel:WORD_1
	v_pk_fma_f32 v[98:99], v[188:189], s[14:15], v[98:99] op_sel_hi:[1,0,1]
	v_pk_fma_f32 v[100:101], v[190:191], s[14:15], v[100:101] op_sel_hi:[1,0,1]
	v_cvt_pk_f32_fp8_e32 v[184:185], v34
	v_cvt_pk_f32_fp8_sdwa v[186:187], v34 src0_sel:WORD_1
	v_pk_fma_f32 v[102:103], v[184:185], s[14:15], v[102:103] op_sel_hi:[1,0,1]
	v_pk_fma_f32 v[104:105], v[186:187], s[14:15], v[104:105] op_sel_hi:[1,0,1]
	v_cvt_pk_f32_fp8_e32 v[188:189], v35
	v_cvt_pk_f32_fp8_sdwa v[190:191], v35 src0_sel:WORD_1
	v_pk_fma_f32 v[106:107], v[188:189], s[14:15], v[106:107] op_sel_hi:[1,0,1]
	v_pk_fma_f32 v[108:109], v[190:191], s[14:15], v[108:109] op_sel_hi:[1,0,1]
	s_cmp_le_u32 s36, 6
	s_cbranch_scc1 .Lp6c0_axdone
	v_readlane_b32 s14, v1, 48
	v_cvt_pk_f32_fp8_e32 v[184:185], v16
	v_cvt_pk_f32_fp8_sdwa v[186:187], v16 src0_sel:WORD_1
	v_pk_fma_f32 v[94:95], v[184:185], s[14:15], v[94:95] op_sel_hi:[1,0,1]
	v_pk_fma_f32 v[96:97], v[186:187], s[14:15], v[96:97] op_sel_hi:[1,0,1]
	v_cvt_pk_f32_fp8_e32 v[188:189], v17
	v_cvt_pk_f32_fp8_sdwa v[190:191], v17 src0_sel:WORD_1
	v_pk_fma_f32 v[98:99], v[188:189], s[14:15], v[98:99] op_sel_hi:[1,0,1]
	v_pk_fma_f32 v[100:101], v[190:191], s[14:15], v[100:101] op_sel_hi:[1,0,1]
	v_cvt_pk_f32_fp8_e32 v[184:185], v18
	v_cvt_pk_f32_fp8_sdwa v[186:187], v18 src0_sel:WORD_1
	v_pk_fma_f32 v[102:103], v[184:185], s[14:15], v[102:103] op_sel_hi:[1,0,1]
	v_pk_fma_f32 v[104:105], v[186:187], s[14:15], v[104:105] op_sel_hi:[1,0,1]
	v_cvt_pk_f32_fp8_e32 v[188:189], v19
	v_cvt_pk_f32_fp8_sdwa v[190:191], v19 src0_sel:WORD_1
	v_pk_fma_f32 v[106:107], v[188:189], s[14:15], v[106:107] op_sel_hi:[1,0,1]
	v_pk_fma_f32 v[108:109], v[190:191], s[14:15], v[108:109] op_sel_hi:[1,0,1]
	v_readlane_b32 s14, v1, 56
	v_cvt_pk_f32_fp8_e32 v[184:185], v12
	v_cvt_pk_f32_fp8_sdwa v[186:187], v12 src0_sel:WORD_1
	v_pk_fma_f32 v[94:95], v[184:185], s[14:15], v[94:95] op_sel_hi:[1,0,1]
	v_pk_fma_f32 v[96:97], v[186:187], s[14:15], v[96:97] op_sel_hi:[1,0,1]
	v_cvt_pk_f32_fp8_e32 v[188:189], v13
	v_cvt_pk_f32_fp8_sdwa v[190:191], v13 src0_sel:WORD_1
	v_pk_fma_f32 v[98:99], v[188:189], s[14:15], v[98:99] op_sel_hi:[1,0,1]
	v_pk_fma_f32 v[100:101], v[190:191], s[14:15], v[100:101] op_sel_hi:[1,0,1]
	v_cvt_pk_f32_fp8_e32 v[184:185], v14
	v_cvt_pk_f32_fp8_sdwa v[186:187], v14 src0_sel:WORD_1
	v_pk_fma_f32 v[102:103], v[184:185], s[14:15], v[102:103] op_sel_hi:[1,0,1]
	v_pk_fma_f32 v[104:105], v[186:187], s[14:15], v[104:105] op_sel_hi:[1,0,1]
	v_cvt_pk_f32_fp8_e32 v[188:189], v15
	v_cvt_pk_f32_fp8_sdwa v[190:191], v15 src0_sel:WORD_1
	v_pk_fma_f32 v[106:107], v[188:189], s[14:15], v[106:107] op_sel_hi:[1,0,1]
	v_pk_fma_f32 v[108:109], v[190:191], s[14:15], v[108:109] op_sel_hi:[1,0,1]
	s_branch .Lp6c0_axdone
.Lp6c0_t3:
	v_readlane_b32 s14, v1, 0
	v_cvt_pk_f32_fp8_e32 v[184:185], v68
	v_cvt_pk_f32_fp8_sdwa v[186:187], v68 src0_sel:WORD_1
	v_pk_fma_f32 v[78:79], v[184:185], s[14:15], v[78:79] op_sel_hi:[1,0,1]
	v_pk_fma_f32 v[80:81], v[186:187], s[14:15], v[80:81] op_sel_hi:[1,0,1]
	v_cvt_pk_f32_fp8_e32 v[188:189], v69
	v_cvt_pk_f32_fp8_sdwa v[190:191], v69 src0_sel:WORD_1
	v_pk_fma_f32 v[82:83], v[188:189], s[14:15], v[82:83] op_sel_hi:[1,0,1]
	v_pk_fma_f32 v[86:87], v[190:191], s[14:15], v[86:87] op_sel_hi:[1,0,1]
	v_cvt_pk_f32_fp8_e32 v[184:185], v70
	v_cvt_pk_f32_fp8_sdwa v[186:187], v70 src0_sel:WORD_1
	v_pk_fma_f32 v[88:89], v[184:185], s[14:15], v[88:89] op_sel_hi:[1,0,1]
	v_pk_fma_f32 v[90:91], v[186:187], s[14:15], v[90:91] op_sel_hi:[1,0,1]
	v_cvt_pk_f32_fp8_e32 v[188:189], v71
	v_cvt_pk_f32_fp8_sdwa v[190:191], v71 src0_sel:WORD_1
	v_pk_fma_f32 v[92:93], v[188:189], s[14:15], v[92:93] op_sel_hi:[1,0,1]
	v_pk_fma_f32 v[84:85], v[190:191], s[14:15], v[84:85] op_sel_hi:[1,0,1]
	v_readlane_b32 s14, v1, 8
	v_cvt_pk_f32_fp8_e32 v[184:185], v64
	v_cvt_pk_f32_fp8_sdwa v[186:187], v64 src0_sel:WORD_1
	v_pk_fma_f32 v[78:79], v[184:185], s[14:15], v[78:79] op_sel_hi:[1,0,1]
	v_pk_fma_f32 v[80:81], v[186:187], s[14:15], v[80:81] op_sel_hi:[1,0,1]
	v_cvt_pk_f32_fp8_e32 v[188:189], v65
	v_cvt_pk_f32_fp8_sdwa v[190:191], v65 src0_sel:WORD_1
	v_pk_fma_f32 v[82:83], v[188:189], s[14:15], v[82:83] op_sel_hi:[1,0,1]
	v_pk_fma_f32 v[86:87], v[190:191], s[14:15], v[86:87] op_sel_hi:[1,0,1]
	v_cvt_pk_f32_fp8_e32 v[184:185], v66
	v_cvt_pk_f32_fp8_sdwa v[186:187], v66 src0_sel:WORD_1
	v_pk_fma_f32 v[88:89], v[184:185], s[14:15], v[88:89] op_sel_hi:[1,0,1]
	v_pk_fma_f32 v[90:91], v[186:187], s[14:15], v[90:91] op_sel_hi:[1,0,1]
	v_cvt_pk_f32_fp8_e32 v[188:189], v67
	v_cvt_pk_f32_fp8_sdwa v[190:191], v67 src0_sel:WORD_1
	v_pk_fma_f32 v[92:93], v[188:189], s[14:15], v[92:93] op_sel_hi:[1,0,1]
	v_pk_fma_f32 v[84:85], v[190:191], s[14:15], v[84:85] op_sel_hi:[1,0,1]
	s_cmp_le_u32 s36, 2
	s_cbranch_scc1 .Lp6c0_axdone
	v_readlane_b32 s14, v1, 16
	v_cvt_pk_f32_fp8_e32 v[184:185], v60
	v_cvt_pk_f32_fp8_sdwa v[186:187], v60 src0_sel:WORD_1
	v_pk_fma_f32 v[78:79], v[184:185], s[14:15], v[78:79] op_sel_hi:[1,0,1]
	v_pk_fma_f32 v[80:81], v[186:187], s[14:15], v[80:81] op_sel_hi:[1,0,1]
	v_cvt_pk_f32_fp8_e32 v[188:189], v61
	v_cvt_pk_f32_fp8_sdwa v[190:191], v61 src0_sel:WORD_1
	v_pk_fma_f32 v[82:83], v[188:189], s[14:15], v[82:83] op_sel_hi:[1,0,1]
	v_pk_fma_f32 v[86:87], v[190:191], s[14:15], v[86:87] op_sel_hi:[1,0,1]
	v_cvt_pk_f32_fp8_e32 v[184:185], v62
	v_cvt_pk_f32_fp8_sdwa v[186:187], v62 src0_sel:WORD_1
	v_pk_fma_f32 v[88:89], v[184:185], s[14:15], v[88:89] op_sel_hi:[1,0,1]
	v_pk_fma_f32 v[90:91], v[186:187], s[14:15], v[90:91] op_sel_hi:[1,0,1]
	v_cvt_pk_f32_fp8_e32 v[188:189], v63
	v_cvt_pk_f32_fp8_sdwa v[190:191], v63 src0_sel:WORD_1
	v_pk_fma_f32 v[92:93], v[188:189], s[14:15], v[92:93] op_sel_hi:[1,0,1]
	v_pk_fma_f32 v[84:85], v[190:191], s[14:15], v[84:85] op_sel_hi:[1,0,1]
	v_readlane_b32 s14, v1, 24
	v_cvt_pk_f32_fp8_e32 v[184:185], v56
	v_cvt_pk_f32_fp8_sdwa v[186:187], v56 src0_sel:WORD_1
	v_pk_fma_f32 v[78:79], v[184:185], s[14:15], v[78:79] op_sel_hi:[1,0,1]
	v_pk_fma_f32 v[80:81], v[186:187], s[14:15], v[80:81] op_sel_hi:[1,0,1]
	v_cvt_pk_f32_fp8_e32 v[188:189], v57
	v_cvt_pk_f32_fp8_sdwa v[190:191], v57 src0_sel:WORD_1
	v_pk_fma_f32 v[82:83], v[188:189], s[14:15], v[82:83] op_sel_hi:[1,0,1]
	v_pk_fma_f32 v[86:87], v[190:191], s[14:15], v[86:87] op_sel_hi:[1,0,1]
	v_cvt_pk_f32_fp8_e32 v[184:185], v58
	v_cvt_pk_f32_fp8_sdwa v[186:187], v58 src0_sel:WORD_1
	v_pk_fma_f32 v[88:89], v[184:185], s[14:15], v[88:89] op_sel_hi:[1,0,1]
	v_pk_fma_f32 v[90:91], v[186:187], s[14:15], v[90:91] op_sel_hi:[1,0,1]
	v_cvt_pk_f32_fp8_e32 v[188:189], v59
	v_cvt_pk_f32_fp8_sdwa v[190:191], v59 src0_sel:WORD_1
	v_pk_fma_f32 v[92:93], v[188:189], s[14:15], v[92:93] op_sel_hi:[1,0,1]
	v_pk_fma_f32 v[84:85], v[190:191], s[14:15], v[84:85] op_sel_hi:[1,0,1]
	s_cmp_le_u32 s36, 4
	s_cbranch_scc1 .Lp6c0_axdone
	v_readlane_b32 s14, v1, 32
	v_cvt_pk_f32_fp8_e32 v[184:185], v48
	v_cvt_pk_f32_fp8_sdwa v[186:187], v48 src0_sel:WORD_1
	v_pk_fma_f32 v[78:79], v[184:185], s[14:15], v[78:79] op_sel_hi:[1,0,1]
	v_pk_fma_f32 v[80:81], v[186:187], s[14:15], v[80:81] op_sel_hi:[1,0,1]
	v_cvt_pk_f32_fp8_e32 v[188:189], v49
	v_cvt_pk_f32_fp8_sdwa v[190:191], v49 src0_sel:WORD_1
	v_pk_fma_f32 v[82:83], v[188:189], s[14:15], v[82:83] op_sel_hi:[1,0,1]
	v_pk_fma_f32 v[86:87], v[190:191], s[14:15], v[86:87] op_sel_hi:[1,0,1]
	v_cvt_pk_f32_fp8_e32 v[184:185], v50
	v_cvt_pk_f32_fp8_sdwa v[186:187], v50 src0_sel:WORD_1
	v_pk_fma_f32 v[88:89], v[184:185], s[14:15], v[88:89] op_sel_hi:[1,0,1]
	v_pk_fma_f32 v[90:91], v[186:187], s[14:15], v[90:91] op_sel_hi:[1,0,1]
	v_cvt_pk_f32_fp8_e32 v[188:189], v51
	v_cvt_pk_f32_fp8_sdwa v[190:191], v51 src0_sel:WORD_1
	v_pk_fma_f32 v[92:93], v[188:189], s[14:15], v[92:93] op_sel_hi:[1,0,1]
	v_pk_fma_f32 v[84:85], v[190:191], s[14:15], v[84:85] op_sel_hi:[1,0,1]
	v_readlane_b32 s14, v1, 40
	v_cvt_pk_f32_fp8_e32 v[184:185], v32
	v_cvt_pk_f32_fp8_sdwa v[186:187], v32 src0_sel:WORD_1
	v_pk_fma_f32 v[78:79], v[184:185], s[14:15], v[78:79] op_sel_hi:[1,0,1]
	v_pk_fma_f32 v[80:81], v[186:187], s[14:15], v[80:81] op_sel_hi:[1,0,1]
	v_cvt_pk_f32_fp8_e32 v[188:189], v33
	v_cvt_pk_f32_fp8_sdwa v[190:191], v33 src0_sel:WORD_1
	v_pk_fma_f32 v[82:83], v[188:189], s[14:15], v[82:83] op_sel_hi:[1,0,1]
	v_pk_fma_f32 v[86:87], v[190:191], s[14:15], v[86:87] op_sel_hi:[1,0,1]
	v_cvt_pk_f32_fp8_e32 v[184:185], v34
	v_cvt_pk_f32_fp8_sdwa v[186:187], v34 src0_sel:WORD_1
	v_pk_fma_f32 v[88:89], v[184:185], s[14:15], v[88:89] op_sel_hi:[1,0,1]
	v_pk_fma_f32 v[90:91], v[186:187], s[14:15], v[90:91] op_sel_hi:[1,0,1]
	v_cvt_pk_f32_fp8_e32 v[188:189], v35
	v_cvt_pk_f32_fp8_sdwa v[190:191], v35 src0_sel:WORD_1
	v_pk_fma_f32 v[92:93], v[188:189], s[14:15], v[92:93] op_sel_hi:[1,0,1]
	v_pk_fma_f32 v[84:85], v[190:191], s[14:15], v[84:85] op_sel_hi:[1,0,1]
	s_cmp_le_u32 s36, 6
	s_cbranch_scc1 .Lp6c0_axdone
	v_readlane_b32 s14, v1, 48
	v_cvt_pk_f32_fp8_e32 v[184:185], v16
	v_cvt_pk_f32_fp8_sdwa v[186:187], v16 src0_sel:WORD_1
	v_pk_fma_f32 v[78:79], v[184:185], s[14:15], v[78:79] op_sel_hi:[1,0,1]
	v_pk_fma_f32 v[80:81], v[186:187], s[14:15], v[80:81] op_sel_hi:[1,0,1]
	v_cvt_pk_f32_fp8_e32 v[188:189], v17
	v_cvt_pk_f32_fp8_sdwa v[190:191], v17 src0_sel:WORD_1
	v_pk_fma_f32 v[82:83], v[188:189], s[14:15], v[82:83] op_sel_hi:[1,0,1]
	v_pk_fma_f32 v[86:87], v[190:191], s[14:15], v[86:87] op_sel_hi:[1,0,1]
	v_cvt_pk_f32_fp8_e32 v[184:185], v18
	v_cvt_pk_f32_fp8_sdwa v[186:187], v18 src0_sel:WORD_1
	v_pk_fma_f32 v[88:89], v[184:185], s[14:15], v[88:89] op_sel_hi:[1,0,1]
	v_pk_fma_f32 v[90:91], v[186:187], s[14:15], v[90:91] op_sel_hi:[1,0,1]
	v_cvt_pk_f32_fp8_e32 v[188:189], v19
	v_cvt_pk_f32_fp8_sdwa v[190:191], v19 src0_sel:WORD_1
	v_pk_fma_f32 v[92:93], v[188:189], s[14:15], v[92:93] op_sel_hi:[1,0,1]
	v_pk_fma_f32 v[84:85], v[190:191], s[14:15], v[84:85] op_sel_hi:[1,0,1]
	v_readlane_b32 s14, v1, 56
	v_cvt_pk_f32_fp8_e32 v[184:185], v12
	v_cvt_pk_f32_fp8_sdwa v[186:187], v12 src0_sel:WORD_1
	v_pk_fma_f32 v[78:79], v[184:185], s[14:15], v[78:79] op_sel_hi:[1,0,1]
	v_pk_fma_f32 v[80:81], v[186:187], s[14:15], v[80:81] op_sel_hi:[1,0,1]
	v_cvt_pk_f32_fp8_e32 v[188:189], v13
	v_cvt_pk_f32_fp8_sdwa v[190:191], v13 src0_sel:WORD_1
	v_pk_fma_f32 v[82:83], v[188:189], s[14:15], v[82:83] op_sel_hi:[1,0,1]
	v_pk_fma_f32 v[86:87], v[190:191], s[14:15], v[86:87] op_sel_hi:[1,0,1]
	v_cvt_pk_f32_fp8_e32 v[184:185], v14
	v_cvt_pk_f32_fp8_sdwa v[186:187], v14 src0_sel:WORD_1
	v_pk_fma_f32 v[88:89], v[184:185], s[14:15], v[88:89] op_sel_hi:[1,0,1]
	v_pk_fma_f32 v[90:91], v[186:187], s[14:15], v[90:91] op_sel_hi:[1,0,1]
	v_cvt_pk_f32_fp8_e32 v[188:189], v15
	v_cvt_pk_f32_fp8_sdwa v[190:191], v15 src0_sel:WORD_1
	v_pk_fma_f32 v[92:93], v[188:189], s[14:15], v[92:93] op_sel_hi:[1,0,1]
	v_pk_fma_f32 v[84:85], v[190:191], s[14:15], v[84:85] op_sel_hi:[1,0,1]
	s_branch .Lp6c0_axdone
.Lp6c0_t4:
	v_readlane_b32 s14, v1, 0
	v_cvt_pk_f32_fp8_e32 v[184:185], v68
	v_cvt_pk_f32_fp8_sdwa v[186:187], v68 src0_sel:WORD_1
	v_pk_fma_f32 v[144:145], v[184:185], s[14:15], v[144:145] op_sel_hi:[1,0,1]
	v_pk_fma_f32 v[146:147], v[186:187], s[14:15], v[146:147] op_sel_hi:[1,0,1]
	v_cvt_pk_f32_fp8_e32 v[188:189], v69
	v_cvt_pk_f32_fp8_sdwa v[190:191], v69 src0_sel:WORD_1
	v_pk_fma_f32 v[148:149], v[188:189], s[14:15], v[148:149] op_sel_hi:[1,0,1]
	v_pk_fma_f32 v[150:151], v[190:191], s[14:15], v[150:151] op_sel_hi:[1,0,1]
	v_cvt_pk_f32_fp8_e32 v[184:185], v70
	v_cvt_pk_f32_fp8_sdwa v[186:187], v70 src0_sel:WORD_1
	v_pk_fma_f32 v[152:153], v[184:185], s[14:15], v[152:153] op_sel_hi:[1,0,1]
	v_pk_fma_f32 v[154:155], v[186:187], s[14:15], v[154:155] op_sel_hi:[1,0,1]
	v_cvt_pk_f32_fp8_e32 v[188:189], v71
	v_cvt_pk_f32_fp8_sdwa v[190:191], v71 src0_sel:WORD_1
	v_pk_fma_f32 v[156:157], v[188:189], s[14:15], v[156:157] op_sel_hi:[1,0,1]
	v_pk_fma_f32 v[158:159], v[190:191], s[14:15], v[158:159] op_sel_hi:[1,0,1]
	v_readlane_b32 s14, v1, 8
	v_cvt_pk_f32_fp8_e32 v[184:185], v64
	v_cvt_pk_f32_fp8_sdwa v[186:187], v64 src0_sel:WORD_1
	v_pk_fma_f32 v[144:145], v[184:185], s[14:15], v[144:145] op_sel_hi:[1,0,1]
	v_pk_fma_f32 v[146:147], v[186:187], s[14:15], v[146:147] op_sel_hi:[1,0,1]
	v_cvt_pk_f32_fp8_e32 v[188:189], v65
	v_cvt_pk_f32_fp8_sdwa v[190:191], v65 src0_sel:WORD_1
	v_pk_fma_f32 v[148:149], v[188:189], s[14:15], v[148:149] op_sel_hi:[1,0,1]
	v_pk_fma_f32 v[150:151], v[190:191], s[14:15], v[150:151] op_sel_hi:[1,0,1]
	v_cvt_pk_f32_fp8_e32 v[184:185], v66
	v_cvt_pk_f32_fp8_sdwa v[186:187], v66 src0_sel:WORD_1
	v_pk_fma_f32 v[152:153], v[184:185], s[14:15], v[152:153] op_sel_hi:[1,0,1]
	v_pk_fma_f32 v[154:155], v[186:187], s[14:15], v[154:155] op_sel_hi:[1,0,1]
	v_cvt_pk_f32_fp8_e32 v[188:189], v67
	v_cvt_pk_f32_fp8_sdwa v[190:191], v67 src0_sel:WORD_1
	v_pk_fma_f32 v[156:157], v[188:189], s[14:15], v[156:157] op_sel_hi:[1,0,1]
	v_pk_fma_f32 v[158:159], v[190:191], s[14:15], v[158:159] op_sel_hi:[1,0,1]
	s_cmp_le_u32 s36, 2
	s_cbranch_scc1 .Lp6c0_axdone
	v_readlane_b32 s14, v1, 16
	v_cvt_pk_f32_fp8_e32 v[184:185], v60
	v_cvt_pk_f32_fp8_sdwa v[186:187], v60 src0_sel:WORD_1
	v_pk_fma_f32 v[144:145], v[184:185], s[14:15], v[144:145] op_sel_hi:[1,0,1]
	v_pk_fma_f32 v[146:147], v[186:187], s[14:15], v[146:147] op_sel_hi:[1,0,1]
	v_cvt_pk_f32_fp8_e32 v[188:189], v61
	v_cvt_pk_f32_fp8_sdwa v[190:191], v61 src0_sel:WORD_1
	v_pk_fma_f32 v[148:149], v[188:189], s[14:15], v[148:149] op_sel_hi:[1,0,1]
	v_pk_fma_f32 v[150:151], v[190:191], s[14:15], v[150:151] op_sel_hi:[1,0,1]
	v_cvt_pk_f32_fp8_e32 v[184:185], v62
	v_cvt_pk_f32_fp8_sdwa v[186:187], v62 src0_sel:WORD_1
	v_pk_fma_f32 v[152:153], v[184:185], s[14:15], v[152:153] op_sel_hi:[1,0,1]
	v_pk_fma_f32 v[154:155], v[186:187], s[14:15], v[154:155] op_sel_hi:[1,0,1]
	v_cvt_pk_f32_fp8_e32 v[188:189], v63
	v_cvt_pk_f32_fp8_sdwa v[190:191], v63 src0_sel:WORD_1
	v_pk_fma_f32 v[156:157], v[188:189], s[14:15], v[156:157] op_sel_hi:[1,0,1]
	v_pk_fma_f32 v[158:159], v[190:191], s[14:15], v[158:159] op_sel_hi:[1,0,1]
	v_readlane_b32 s14, v1, 24
	v_cvt_pk_f32_fp8_e32 v[184:185], v56
	v_cvt_pk_f32_fp8_sdwa v[186:187], v56 src0_sel:WORD_1
	v_pk_fma_f32 v[144:145], v[184:185], s[14:15], v[144:145] op_sel_hi:[1,0,1]
	v_pk_fma_f32 v[146:147], v[186:187], s[14:15], v[146:147] op_sel_hi:[1,0,1]
	v_cvt_pk_f32_fp8_e32 v[188:189], v57
	v_cvt_pk_f32_fp8_sdwa v[190:191], v57 src0_sel:WORD_1
	v_pk_fma_f32 v[148:149], v[188:189], s[14:15], v[148:149] op_sel_hi:[1,0,1]
	v_pk_fma_f32 v[150:151], v[190:191], s[14:15], v[150:151] op_sel_hi:[1,0,1]
	v_cvt_pk_f32_fp8_e32 v[184:185], v58
	v_cvt_pk_f32_fp8_sdwa v[186:187], v58 src0_sel:WORD_1
	v_pk_fma_f32 v[152:153], v[184:185], s[14:15], v[152:153] op_sel_hi:[1,0,1]
	v_pk_fma_f32 v[154:155], v[186:187], s[14:15], v[154:155] op_sel_hi:[1,0,1]
	v_cvt_pk_f32_fp8_e32 v[188:189], v59
	v_cvt_pk_f32_fp8_sdwa v[190:191], v59 src0_sel:WORD_1
	v_pk_fma_f32 v[156:157], v[188:189], s[14:15], v[156:157] op_sel_hi:[1,0,1]
	v_pk_fma_f32 v[158:159], v[190:191], s[14:15], v[158:159] op_sel_hi:[1,0,1]
	s_cmp_le_u32 s36, 4
	s_cbranch_scc1 .Lp6c0_axdone
	v_readlane_b32 s14, v1, 32
	v_cvt_pk_f32_fp8_e32 v[184:185], v48
	v_cvt_pk_f32_fp8_sdwa v[186:187], v48 src0_sel:WORD_1
	v_pk_fma_f32 v[144:145], v[184:185], s[14:15], v[144:145] op_sel_hi:[1,0,1]
	v_pk_fma_f32 v[146:147], v[186:187], s[14:15], v[146:147] op_sel_hi:[1,0,1]
	v_cvt_pk_f32_fp8_e32 v[188:189], v49
	v_cvt_pk_f32_fp8_sdwa v[190:191], v49 src0_sel:WORD_1
	v_pk_fma_f32 v[148:149], v[188:189], s[14:15], v[148:149] op_sel_hi:[1,0,1]
	v_pk_fma_f32 v[150:151], v[190:191], s[14:15], v[150:151] op_sel_hi:[1,0,1]
	v_cvt_pk_f32_fp8_e32 v[184:185], v50
	v_cvt_pk_f32_fp8_sdwa v[186:187], v50 src0_sel:WORD_1
	v_pk_fma_f32 v[152:153], v[184:185], s[14:15], v[152:153] op_sel_hi:[1,0,1]
	v_pk_fma_f32 v[154:155], v[186:187], s[14:15], v[154:155] op_sel_hi:[1,0,1]
	v_cvt_pk_f32_fp8_e32 v[188:189], v51
	v_cvt_pk_f32_fp8_sdwa v[190:191], v51 src0_sel:WORD_1
	v_pk_fma_f32 v[156:157], v[188:189], s[14:15], v[156:157] op_sel_hi:[1,0,1]
	v_pk_fma_f32 v[158:159], v[190:191], s[14:15], v[158:159] op_sel_hi:[1,0,1]
	v_readlane_b32 s14, v1, 40
	v_cvt_pk_f32_fp8_e32 v[184:185], v32
	v_cvt_pk_f32_fp8_sdwa v[186:187], v32 src0_sel:WORD_1
	v_pk_fma_f32 v[144:145], v[184:185], s[14:15], v[144:145] op_sel_hi:[1,0,1]
	v_pk_fma_f32 v[146:147], v[186:187], s[14:15], v[146:147] op_sel_hi:[1,0,1]
	v_cvt_pk_f32_fp8_e32 v[188:189], v33
	v_cvt_pk_f32_fp8_sdwa v[190:191], v33 src0_sel:WORD_1
	v_pk_fma_f32 v[148:149], v[188:189], s[14:15], v[148:149] op_sel_hi:[1,0,1]
	v_pk_fma_f32 v[150:151], v[190:191], s[14:15], v[150:151] op_sel_hi:[1,0,1]
	v_cvt_pk_f32_fp8_e32 v[184:185], v34
	v_cvt_pk_f32_fp8_sdwa v[186:187], v34 src0_sel:WORD_1
	v_pk_fma_f32 v[152:153], v[184:185], s[14:15], v[152:153] op_sel_hi:[1,0,1]
	v_pk_fma_f32 v[154:155], v[186:187], s[14:15], v[154:155] op_sel_hi:[1,0,1]
	v_cvt_pk_f32_fp8_e32 v[188:189], v35
	v_cvt_pk_f32_fp8_sdwa v[190:191], v35 src0_sel:WORD_1
	v_pk_fma_f32 v[156:157], v[188:189], s[14:15], v[156:157] op_sel_hi:[1,0,1]
	v_pk_fma_f32 v[158:159], v[190:191], s[14:15], v[158:159] op_sel_hi:[1,0,1]
	s_cmp_le_u32 s36, 6
	s_cbranch_scc1 .Lp6c0_axdone
	v_readlane_b32 s14, v1, 48
	v_cvt_pk_f32_fp8_e32 v[184:185], v16
	v_cvt_pk_f32_fp8_sdwa v[186:187], v16 src0_sel:WORD_1
	v_pk_fma_f32 v[144:145], v[184:185], s[14:15], v[144:145] op_sel_hi:[1,0,1]
	v_pk_fma_f32 v[146:147], v[186:187], s[14:15], v[146:147] op_sel_hi:[1,0,1]
	v_cvt_pk_f32_fp8_e32 v[188:189], v17
	v_cvt_pk_f32_fp8_sdwa v[190:191], v17 src0_sel:WORD_1
	v_pk_fma_f32 v[148:149], v[188:189], s[14:15], v[148:149] op_sel_hi:[1,0,1]
	v_pk_fma_f32 v[150:151], v[190:191], s[14:15], v[150:151] op_sel_hi:[1,0,1]
	v_cvt_pk_f32_fp8_e32 v[184:185], v18
	v_cvt_pk_f32_fp8_sdwa v[186:187], v18 src0_sel:WORD_1
	v_pk_fma_f32 v[152:153], v[184:185], s[14:15], v[152:153] op_sel_hi:[1,0,1]
	v_pk_fma_f32 v[154:155], v[186:187], s[14:15], v[154:155] op_sel_hi:[1,0,1]
	v_cvt_pk_f32_fp8_e32 v[188:189], v19
	v_cvt_pk_f32_fp8_sdwa v[190:191], v19 src0_sel:WORD_1
	v_pk_fma_f32 v[156:157], v[188:189], s[14:15], v[156:157] op_sel_hi:[1,0,1]
	v_pk_fma_f32 v[158:159], v[190:191], s[14:15], v[158:159] op_sel_hi:[1,0,1]
	v_readlane_b32 s14, v1, 56
	v_cvt_pk_f32_fp8_e32 v[184:185], v12
	v_cvt_pk_f32_fp8_sdwa v[186:187], v12 src0_sel:WORD_1
	v_pk_fma_f32 v[144:145], v[184:185], s[14:15], v[144:145] op_sel_hi:[1,0,1]
	v_pk_fma_f32 v[146:147], v[186:187], s[14:15], v[146:147] op_sel_hi:[1,0,1]
	v_cvt_pk_f32_fp8_e32 v[188:189], v13
	v_cvt_pk_f32_fp8_sdwa v[190:191], v13 src0_sel:WORD_1
	v_pk_fma_f32 v[148:149], v[188:189], s[14:15], v[148:149] op_sel_hi:[1,0,1]
	v_pk_fma_f32 v[150:151], v[190:191], s[14:15], v[150:151] op_sel_hi:[1,0,1]
	v_cvt_pk_f32_fp8_e32 v[184:185], v14
	v_cvt_pk_f32_fp8_sdwa v[186:187], v14 src0_sel:WORD_1
	v_pk_fma_f32 v[152:153], v[184:185], s[14:15], v[152:153] op_sel_hi:[1,0,1]
	v_pk_fma_f32 v[154:155], v[186:187], s[14:15], v[154:155] op_sel_hi:[1,0,1]
	v_cvt_pk_f32_fp8_e32 v[188:189], v15
	v_cvt_pk_f32_fp8_sdwa v[190:191], v15 src0_sel:WORD_1
	v_pk_fma_f32 v[156:157], v[188:189], s[14:15], v[156:157] op_sel_hi:[1,0,1]
	v_pk_fma_f32 v[158:159], v[190:191], s[14:15], v[158:159] op_sel_hi:[1,0,1]
	s_branch .Lp6c0_axdone
.Lp6c0_t5:
	v_readlane_b32 s14, v1, 0
	v_cvt_pk_f32_fp8_e32 v[184:185], v68
	v_cvt_pk_f32_fp8_sdwa v[186:187], v68 src0_sel:WORD_1
	v_pk_fma_f32 v[160:161], v[184:185], s[14:15], v[160:161] op_sel_hi:[1,0,1]
	v_pk_fma_f32 v[162:163], v[186:187], s[14:15], v[162:163] op_sel_hi:[1,0,1]
	v_cvt_pk_f32_fp8_e32 v[188:189], v69
	v_cvt_pk_f32_fp8_sdwa v[190:191], v69 src0_sel:WORD_1
	v_pk_fma_f32 v[164:165], v[188:189], s[14:15], v[164:165] op_sel_hi:[1,0,1]
	v_pk_fma_f32 v[166:167], v[190:191], s[14:15], v[166:167] op_sel_hi:[1,0,1]
	v_cvt_pk_f32_fp8_e32 v[184:185], v70
	v_cvt_pk_f32_fp8_sdwa v[186:187], v70 src0_sel:WORD_1
	v_pk_fma_f32 v[168:169], v[184:185], s[14:15], v[168:169] op_sel_hi:[1,0,1]
	v_pk_fma_f32 v[170:171], v[186:187], s[14:15], v[170:171] op_sel_hi:[1,0,1]
	v_cvt_pk_f32_fp8_e32 v[188:189], v71
	v_cvt_pk_f32_fp8_sdwa v[190:191], v71 src0_sel:WORD_1
	v_pk_fma_f32 v[172:173], v[188:189], s[14:15], v[172:173] op_sel_hi:[1,0,1]
	v_pk_fma_f32 v[174:175], v[190:191], s[14:15], v[174:175] op_sel_hi:[1,0,1]
	v_readlane_b32 s14, v1, 8
	v_cvt_pk_f32_fp8_e32 v[184:185], v64
	v_cvt_pk_f32_fp8_sdwa v[186:187], v64 src0_sel:WORD_1
	v_pk_fma_f32 v[160:161], v[184:185], s[14:15], v[160:161] op_sel_hi:[1,0,1]
	v_pk_fma_f32 v[162:163], v[186:187], s[14:15], v[162:163] op_sel_hi:[1,0,1]
	v_cvt_pk_f32_fp8_e32 v[188:189], v65
	v_cvt_pk_f32_fp8_sdwa v[190:191], v65 src0_sel:WORD_1
	v_pk_fma_f32 v[164:165], v[188:189], s[14:15], v[164:165] op_sel_hi:[1,0,1]
	v_pk_fma_f32 v[166:167], v[190:191], s[14:15], v[166:167] op_sel_hi:[1,0,1]
	v_cvt_pk_f32_fp8_e32 v[184:185], v66
	v_cvt_pk_f32_fp8_sdwa v[186:187], v66 src0_sel:WORD_1
	v_pk_fma_f32 v[168:169], v[184:185], s[14:15], v[168:169] op_sel_hi:[1,0,1]
	v_pk_fma_f32 v[170:171], v[186:187], s[14:15], v[170:171] op_sel_hi:[1,0,1]
	v_cvt_pk_f32_fp8_e32 v[188:189], v67
	v_cvt_pk_f32_fp8_sdwa v[190:191], v67 src0_sel:WORD_1
	v_pk_fma_f32 v[172:173], v[188:189], s[14:15], v[172:173] op_sel_hi:[1,0,1]
	v_pk_fma_f32 v[174:175], v[190:191], s[14:15], v[174:175] op_sel_hi:[1,0,1]
	s_cmp_le_u32 s36, 2
	s_cbranch_scc1 .Lp6c0_axdone
	v_readlane_b32 s14, v1, 16
	v_cvt_pk_f32_fp8_e32 v[184:185], v60
	v_cvt_pk_f32_fp8_sdwa v[186:187], v60 src0_sel:WORD_1
	v_pk_fma_f32 v[160:161], v[184:185], s[14:15], v[160:161] op_sel_hi:[1,0,1]
	v_pk_fma_f32 v[162:163], v[186:187], s[14:15], v[162:163] op_sel_hi:[1,0,1]
	v_cvt_pk_f32_fp8_e32 v[188:189], v61
	v_cvt_pk_f32_fp8_sdwa v[190:191], v61 src0_sel:WORD_1
	v_pk_fma_f32 v[164:165], v[188:189], s[14:15], v[164:165] op_sel_hi:[1,0,1]
	v_pk_fma_f32 v[166:167], v[190:191], s[14:15], v[166:167] op_sel_hi:[1,0,1]
	v_cvt_pk_f32_fp8_e32 v[184:185], v62
	v_cvt_pk_f32_fp8_sdwa v[186:187], v62 src0_sel:WORD_1
	v_pk_fma_f32 v[168:169], v[184:185], s[14:15], v[168:169] op_sel_hi:[1,0,1]
	v_pk_fma_f32 v[170:171], v[186:187], s[14:15], v[170:171] op_sel_hi:[1,0,1]
	v_cvt_pk_f32_fp8_e32 v[188:189], v63
	v_cvt_pk_f32_fp8_sdwa v[190:191], v63 src0_sel:WORD_1
	v_pk_fma_f32 v[172:173], v[188:189], s[14:15], v[172:173] op_sel_hi:[1,0,1]
	v_pk_fma_f32 v[174:175], v[190:191], s[14:15], v[174:175] op_sel_hi:[1,0,1]
	v_readlane_b32 s14, v1, 24
	v_cvt_pk_f32_fp8_e32 v[184:185], v56
	v_cvt_pk_f32_fp8_sdwa v[186:187], v56 src0_sel:WORD_1
	v_pk_fma_f32 v[160:161], v[184:185], s[14:15], v[160:161] op_sel_hi:[1,0,1]
	v_pk_fma_f32 v[162:163], v[186:187], s[14:15], v[162:163] op_sel_hi:[1,0,1]
	v_cvt_pk_f32_fp8_e32 v[188:189], v57
	v_cvt_pk_f32_fp8_sdwa v[190:191], v57 src0_sel:WORD_1
	v_pk_fma_f32 v[164:165], v[188:189], s[14:15], v[164:165] op_sel_hi:[1,0,1]
	v_pk_fma_f32 v[166:167], v[190:191], s[14:15], v[166:167] op_sel_hi:[1,0,1]
	v_cvt_pk_f32_fp8_e32 v[184:185], v58
	v_cvt_pk_f32_fp8_sdwa v[186:187], v58 src0_sel:WORD_1
	v_pk_fma_f32 v[168:169], v[184:185], s[14:15], v[168:169] op_sel_hi:[1,0,1]
	v_pk_fma_f32 v[170:171], v[186:187], s[14:15], v[170:171] op_sel_hi:[1,0,1]
	v_cvt_pk_f32_fp8_e32 v[188:189], v59
	v_cvt_pk_f32_fp8_sdwa v[190:191], v59 src0_sel:WORD_1
	v_pk_fma_f32 v[172:173], v[188:189], s[14:15], v[172:173] op_sel_hi:[1,0,1]
	v_pk_fma_f32 v[174:175], v[190:191], s[14:15], v[174:175] op_sel_hi:[1,0,1]
	s_cmp_le_u32 s36, 4
	s_cbranch_scc1 .Lp6c0_axdone
	v_readlane_b32 s14, v1, 32
	v_cvt_pk_f32_fp8_e32 v[184:185], v48
	v_cvt_pk_f32_fp8_sdwa v[186:187], v48 src0_sel:WORD_1
	v_pk_fma_f32 v[160:161], v[184:185], s[14:15], v[160:161] op_sel_hi:[1,0,1]
	v_pk_fma_f32 v[162:163], v[186:187], s[14:15], v[162:163] op_sel_hi:[1,0,1]
	v_cvt_pk_f32_fp8_e32 v[188:189], v49
	v_cvt_pk_f32_fp8_sdwa v[190:191], v49 src0_sel:WORD_1
	v_pk_fma_f32 v[164:165], v[188:189], s[14:15], v[164:165] op_sel_hi:[1,0,1]
	v_pk_fma_f32 v[166:167], v[190:191], s[14:15], v[166:167] op_sel_hi:[1,0,1]
	v_cvt_pk_f32_fp8_e32 v[184:185], v50
	v_cvt_pk_f32_fp8_sdwa v[186:187], v50 src0_sel:WORD_1
	v_pk_fma_f32 v[168:169], v[184:185], s[14:15], v[168:169] op_sel_hi:[1,0,1]
	v_pk_fma_f32 v[170:171], v[186:187], s[14:15], v[170:171] op_sel_hi:[1,0,1]
	v_cvt_pk_f32_fp8_e32 v[188:189], v51
	v_cvt_pk_f32_fp8_sdwa v[190:191], v51 src0_sel:WORD_1
	v_pk_fma_f32 v[172:173], v[188:189], s[14:15], v[172:173] op_sel_hi:[1,0,1]
	v_pk_fma_f32 v[174:175], v[190:191], s[14:15], v[174:175] op_sel_hi:[1,0,1]
	v_readlane_b32 s14, v1, 40
	v_cvt_pk_f32_fp8_e32 v[184:185], v32
	v_cvt_pk_f32_fp8_sdwa v[186:187], v32 src0_sel:WORD_1
	v_pk_fma_f32 v[160:161], v[184:185], s[14:15], v[160:161] op_sel_hi:[1,0,1]
	v_pk_fma_f32 v[162:163], v[186:187], s[14:15], v[162:163] op_sel_hi:[1,0,1]
	v_cvt_pk_f32_fp8_e32 v[188:189], v33
	v_cvt_pk_f32_fp8_sdwa v[190:191], v33 src0_sel:WORD_1
	v_pk_fma_f32 v[164:165], v[188:189], s[14:15], v[164:165] op_sel_hi:[1,0,1]
	v_pk_fma_f32 v[166:167], v[190:191], s[14:15], v[166:167] op_sel_hi:[1,0,1]
	v_cvt_pk_f32_fp8_e32 v[184:185], v34
	v_cvt_pk_f32_fp8_sdwa v[186:187], v34 src0_sel:WORD_1
	v_pk_fma_f32 v[168:169], v[184:185], s[14:15], v[168:169] op_sel_hi:[1,0,1]
	v_pk_fma_f32 v[170:171], v[186:187], s[14:15], v[170:171] op_sel_hi:[1,0,1]
	v_cvt_pk_f32_fp8_e32 v[188:189], v35
	v_cvt_pk_f32_fp8_sdwa v[190:191], v35 src0_sel:WORD_1
	v_pk_fma_f32 v[172:173], v[188:189], s[14:15], v[172:173] op_sel_hi:[1,0,1]
	v_pk_fma_f32 v[174:175], v[190:191], s[14:15], v[174:175] op_sel_hi:[1,0,1]
	s_cmp_le_u32 s36, 6
	s_cbranch_scc1 .Lp6c0_axdone
	v_readlane_b32 s14, v1, 48
	v_cvt_pk_f32_fp8_e32 v[184:185], v16
	v_cvt_pk_f32_fp8_sdwa v[186:187], v16 src0_sel:WORD_1
	v_pk_fma_f32 v[160:161], v[184:185], s[14:15], v[160:161] op_sel_hi:[1,0,1]
	v_pk_fma_f32 v[162:163], v[186:187], s[14:15], v[162:163] op_sel_hi:[1,0,1]
	v_cvt_pk_f32_fp8_e32 v[188:189], v17
	v_cvt_pk_f32_fp8_sdwa v[190:191], v17 src0_sel:WORD_1
	v_pk_fma_f32 v[164:165], v[188:189], s[14:15], v[164:165] op_sel_hi:[1,0,1]
	v_pk_fma_f32 v[166:167], v[190:191], s[14:15], v[166:167] op_sel_hi:[1,0,1]
	v_cvt_pk_f32_fp8_e32 v[184:185], v18
	v_cvt_pk_f32_fp8_sdwa v[186:187], v18 src0_sel:WORD_1
	v_pk_fma_f32 v[168:169], v[184:185], s[14:15], v[168:169] op_sel_hi:[1,0,1]
	v_pk_fma_f32 v[170:171], v[186:187], s[14:15], v[170:171] op_sel_hi:[1,0,1]
	v_cvt_pk_f32_fp8_e32 v[188:189], v19
	v_cvt_pk_f32_fp8_sdwa v[190:191], v19 src0_sel:WORD_1
	v_pk_fma_f32 v[172:173], v[188:189], s[14:15], v[172:173] op_sel_hi:[1,0,1]
	v_pk_fma_f32 v[174:175], v[190:191], s[14:15], v[174:175] op_sel_hi:[1,0,1]
	v_readlane_b32 s14, v1, 56
	v_cvt_pk_f32_fp8_e32 v[184:185], v12
	v_cvt_pk_f32_fp8_sdwa v[186:187], v12 src0_sel:WORD_1
	v_pk_fma_f32 v[160:161], v[184:185], s[14:15], v[160:161] op_sel_hi:[1,0,1]
	v_pk_fma_f32 v[162:163], v[186:187], s[14:15], v[162:163] op_sel_hi:[1,0,1]
	v_cvt_pk_f32_fp8_e32 v[188:189], v13
	v_cvt_pk_f32_fp8_sdwa v[190:191], v13 src0_sel:WORD_1
	v_pk_fma_f32 v[164:165], v[188:189], s[14:15], v[164:165] op_sel_hi:[1,0,1]
	v_pk_fma_f32 v[166:167], v[190:191], s[14:15], v[166:167] op_sel_hi:[1,0,1]
	v_cvt_pk_f32_fp8_e32 v[184:185], v14
	v_cvt_pk_f32_fp8_sdwa v[186:187], v14 src0_sel:WORD_1
	v_pk_fma_f32 v[168:169], v[184:185], s[14:15], v[168:169] op_sel_hi:[1,0,1]
	v_pk_fma_f32 v[170:171], v[186:187], s[14:15], v[170:171] op_sel_hi:[1,0,1]
	v_cvt_pk_f32_fp8_e32 v[188:189], v15
	v_cvt_pk_f32_fp8_sdwa v[190:191], v15 src0_sel:WORD_1
	v_pk_fma_f32 v[172:173], v[188:189], s[14:15], v[172:173] op_sel_hi:[1,0,1]
	v_pk_fma_f32 v[174:175], v[190:191], s[14:15], v[174:175] op_sel_hi:[1,0,1]
	s_branch .Lp6c0_axdone
.Lp6c0_t6:
	v_readlane_b32 s14, v1, 0
	v_cvt_pk_f32_fp8_e32 v[184:185], v68
	v_cvt_pk_f32_fp8_sdwa v[186:187], v68 src0_sel:WORD_1
	v_pk_fma_f32 v[224:225], v[184:185], s[14:15], v[224:225] op_sel_hi:[1,0,1]
	v_pk_fma_f32 v[226:227], v[186:187], s[14:15], v[226:227] op_sel_hi:[1,0,1]
	v_cvt_pk_f32_fp8_e32 v[188:189], v69
	v_cvt_pk_f32_fp8_sdwa v[190:191], v69 src0_sel:WORD_1
	v_pk_fma_f32 v[228:229], v[188:189], s[14:15], v[228:229] op_sel_hi:[1,0,1]
	v_pk_fma_f32 v[230:231], v[190:191], s[14:15], v[230:231] op_sel_hi:[1,0,1]
	v_cvt_pk_f32_fp8_e32 v[184:185], v70
	v_cvt_pk_f32_fp8_sdwa v[186:187], v70 src0_sel:WORD_1
	v_pk_fma_f32 v[232:233], v[184:185], s[14:15], v[232:233] op_sel_hi:[1,0,1]
	v_pk_fma_f32 v[234:235], v[186:187], s[14:15], v[234:235] op_sel_hi:[1,0,1]
	v_cvt_pk_f32_fp8_e32 v[188:189], v71
	v_cvt_pk_f32_fp8_sdwa v[190:191], v71 src0_sel:WORD_1
	v_pk_fma_f32 v[236:237], v[188:189], s[14:15], v[236:237] op_sel_hi:[1,0,1]
	v_pk_fma_f32 v[238:239], v[190:191], s[14:15], v[238:239] op_sel_hi:[1,0,1]
	v_readlane_b32 s14, v1, 8
	v_cvt_pk_f32_fp8_e32 v[184:185], v64
	v_cvt_pk_f32_fp8_sdwa v[186:187], v64 src0_sel:WORD_1
	v_pk_fma_f32 v[224:225], v[184:185], s[14:15], v[224:225] op_sel_hi:[1,0,1]
	v_pk_fma_f32 v[226:227], v[186:187], s[14:15], v[226:227] op_sel_hi:[1,0,1]
	v_cvt_pk_f32_fp8_e32 v[188:189], v65
	v_cvt_pk_f32_fp8_sdwa v[190:191], v65 src0_sel:WORD_1
	v_pk_fma_f32 v[228:229], v[188:189], s[14:15], v[228:229] op_sel_hi:[1,0,1]
	v_pk_fma_f32 v[230:231], v[190:191], s[14:15], v[230:231] op_sel_hi:[1,0,1]
	v_cvt_pk_f32_fp8_e32 v[184:185], v66
	v_cvt_pk_f32_fp8_sdwa v[186:187], v66 src0_sel:WORD_1
	v_pk_fma_f32 v[232:233], v[184:185], s[14:15], v[232:233] op_sel_hi:[1,0,1]
	v_pk_fma_f32 v[234:235], v[186:187], s[14:15], v[234:235] op_sel_hi:[1,0,1]
	v_cvt_pk_f32_fp8_e32 v[188:189], v67
	v_cvt_pk_f32_fp8_sdwa v[190:191], v67 src0_sel:WORD_1
	v_pk_fma_f32 v[236:237], v[188:189], s[14:15], v[236:237] op_sel_hi:[1,0,1]
	v_pk_fma_f32 v[238:239], v[190:191], s[14:15], v[238:239] op_sel_hi:[1,0,1]
	s_cmp_le_u32 s36, 2
	s_cbranch_scc1 .Lp6c0_axdone
	v_readlane_b32 s14, v1, 16
	v_cvt_pk_f32_fp8_e32 v[184:185], v60
	v_cvt_pk_f32_fp8_sdwa v[186:187], v60 src0_sel:WORD_1
	v_pk_fma_f32 v[224:225], v[184:185], s[14:15], v[224:225] op_sel_hi:[1,0,1]
	v_pk_fma_f32 v[226:227], v[186:187], s[14:15], v[226:227] op_sel_hi:[1,0,1]
	v_cvt_pk_f32_fp8_e32 v[188:189], v61
	v_cvt_pk_f32_fp8_sdwa v[190:191], v61 src0_sel:WORD_1
	v_pk_fma_f32 v[228:229], v[188:189], s[14:15], v[228:229] op_sel_hi:[1,0,1]
	v_pk_fma_f32 v[230:231], v[190:191], s[14:15], v[230:231] op_sel_hi:[1,0,1]
	v_cvt_pk_f32_fp8_e32 v[184:185], v62
	v_cvt_pk_f32_fp8_sdwa v[186:187], v62 src0_sel:WORD_1
	v_pk_fma_f32 v[232:233], v[184:185], s[14:15], v[232:233] op_sel_hi:[1,0,1]
	v_pk_fma_f32 v[234:235], v[186:187], s[14:15], v[234:235] op_sel_hi:[1,0,1]
	v_cvt_pk_f32_fp8_e32 v[188:189], v63
	v_cvt_pk_f32_fp8_sdwa v[190:191], v63 src0_sel:WORD_1
	v_pk_fma_f32 v[236:237], v[188:189], s[14:15], v[236:237] op_sel_hi:[1,0,1]
	v_pk_fma_f32 v[238:239], v[190:191], s[14:15], v[238:239] op_sel_hi:[1,0,1]
	v_readlane_b32 s14, v1, 24
	v_cvt_pk_f32_fp8_e32 v[184:185], v56
	v_cvt_pk_f32_fp8_sdwa v[186:187], v56 src0_sel:WORD_1
	v_pk_fma_f32 v[224:225], v[184:185], s[14:15], v[224:225] op_sel_hi:[1,0,1]
	v_pk_fma_f32 v[226:227], v[186:187], s[14:15], v[226:227] op_sel_hi:[1,0,1]
	v_cvt_pk_f32_fp8_e32 v[188:189], v57
	v_cvt_pk_f32_fp8_sdwa v[190:191], v57 src0_sel:WORD_1
	v_pk_fma_f32 v[228:229], v[188:189], s[14:15], v[228:229] op_sel_hi:[1,0,1]
	v_pk_fma_f32 v[230:231], v[190:191], s[14:15], v[230:231] op_sel_hi:[1,0,1]
	v_cvt_pk_f32_fp8_e32 v[184:185], v58
	v_cvt_pk_f32_fp8_sdwa v[186:187], v58 src0_sel:WORD_1
	v_pk_fma_f32 v[232:233], v[184:185], s[14:15], v[232:233] op_sel_hi:[1,0,1]
	v_pk_fma_f32 v[234:235], v[186:187], s[14:15], v[234:235] op_sel_hi:[1,0,1]
	v_cvt_pk_f32_fp8_e32 v[188:189], v59
	v_cvt_pk_f32_fp8_sdwa v[190:191], v59 src0_sel:WORD_1
	v_pk_fma_f32 v[236:237], v[188:189], s[14:15], v[236:237] op_sel_hi:[1,0,1]
	v_pk_fma_f32 v[238:239], v[190:191], s[14:15], v[238:239] op_sel_hi:[1,0,1]
	s_cmp_le_u32 s36, 4
	s_cbranch_scc1 .Lp6c0_axdone
	v_readlane_b32 s14, v1, 32
	v_cvt_pk_f32_fp8_e32 v[184:185], v48
	v_cvt_pk_f32_fp8_sdwa v[186:187], v48 src0_sel:WORD_1
	v_pk_fma_f32 v[224:225], v[184:185], s[14:15], v[224:225] op_sel_hi:[1,0,1]
	v_pk_fma_f32 v[226:227], v[186:187], s[14:15], v[226:227] op_sel_hi:[1,0,1]
	v_cvt_pk_f32_fp8_e32 v[188:189], v49
	v_cvt_pk_f32_fp8_sdwa v[190:191], v49 src0_sel:WORD_1
	v_pk_fma_f32 v[228:229], v[188:189], s[14:15], v[228:229] op_sel_hi:[1,0,1]
	v_pk_fma_f32 v[230:231], v[190:191], s[14:15], v[230:231] op_sel_hi:[1,0,1]
	v_cvt_pk_f32_fp8_e32 v[184:185], v50
	v_cvt_pk_f32_fp8_sdwa v[186:187], v50 src0_sel:WORD_1
	v_pk_fma_f32 v[232:233], v[184:185], s[14:15], v[232:233] op_sel_hi:[1,0,1]
	v_pk_fma_f32 v[234:235], v[186:187], s[14:15], v[234:235] op_sel_hi:[1,0,1]
	v_cvt_pk_f32_fp8_e32 v[188:189], v51
	v_cvt_pk_f32_fp8_sdwa v[190:191], v51 src0_sel:WORD_1
	v_pk_fma_f32 v[236:237], v[188:189], s[14:15], v[236:237] op_sel_hi:[1,0,1]
	v_pk_fma_f32 v[238:239], v[190:191], s[14:15], v[238:239] op_sel_hi:[1,0,1]
	v_readlane_b32 s14, v1, 40
	v_cvt_pk_f32_fp8_e32 v[184:185], v32
	v_cvt_pk_f32_fp8_sdwa v[186:187], v32 src0_sel:WORD_1
	v_pk_fma_f32 v[224:225], v[184:185], s[14:15], v[224:225] op_sel_hi:[1,0,1]
	v_pk_fma_f32 v[226:227], v[186:187], s[14:15], v[226:227] op_sel_hi:[1,0,1]
	v_cvt_pk_f32_fp8_e32 v[188:189], v33
	v_cvt_pk_f32_fp8_sdwa v[190:191], v33 src0_sel:WORD_1
	v_pk_fma_f32 v[228:229], v[188:189], s[14:15], v[228:229] op_sel_hi:[1,0,1]
	v_pk_fma_f32 v[230:231], v[190:191], s[14:15], v[230:231] op_sel_hi:[1,0,1]
	v_cvt_pk_f32_fp8_e32 v[184:185], v34
	v_cvt_pk_f32_fp8_sdwa v[186:187], v34 src0_sel:WORD_1
	v_pk_fma_f32 v[232:233], v[184:185], s[14:15], v[232:233] op_sel_hi:[1,0,1]
	v_pk_fma_f32 v[234:235], v[186:187], s[14:15], v[234:235] op_sel_hi:[1,0,1]
	v_cvt_pk_f32_fp8_e32 v[188:189], v35
	v_cvt_pk_f32_fp8_sdwa v[190:191], v35 src0_sel:WORD_1
	v_pk_fma_f32 v[236:237], v[188:189], s[14:15], v[236:237] op_sel_hi:[1,0,1]
	v_pk_fma_f32 v[238:239], v[190:191], s[14:15], v[238:239] op_sel_hi:[1,0,1]
	s_cmp_le_u32 s36, 6
	s_cbranch_scc1 .Lp6c0_axdone
	v_readlane_b32 s14, v1, 48
	v_cvt_pk_f32_fp8_e32 v[184:185], v16
	v_cvt_pk_f32_fp8_sdwa v[186:187], v16 src0_sel:WORD_1
	v_pk_fma_f32 v[224:225], v[184:185], s[14:15], v[224:225] op_sel_hi:[1,0,1]
	v_pk_fma_f32 v[226:227], v[186:187], s[14:15], v[226:227] op_sel_hi:[1,0,1]
	v_cvt_pk_f32_fp8_e32 v[188:189], v17
	v_cvt_pk_f32_fp8_sdwa v[190:191], v17 src0_sel:WORD_1
	v_pk_fma_f32 v[228:229], v[188:189], s[14:15], v[228:229] op_sel_hi:[1,0,1]
	v_pk_fma_f32 v[230:231], v[190:191], s[14:15], v[230:231] op_sel_hi:[1,0,1]
	v_cvt_pk_f32_fp8_e32 v[184:185], v18
	v_cvt_pk_f32_fp8_sdwa v[186:187], v18 src0_sel:WORD_1
	v_pk_fma_f32 v[232:233], v[184:185], s[14:15], v[232:233] op_sel_hi:[1,0,1]
	v_pk_fma_f32 v[234:235], v[186:187], s[14:15], v[234:235] op_sel_hi:[1,0,1]
	v_cvt_pk_f32_fp8_e32 v[188:189], v19
	v_cvt_pk_f32_fp8_sdwa v[190:191], v19 src0_sel:WORD_1
	v_pk_fma_f32 v[236:237], v[188:189], s[14:15], v[236:237] op_sel_hi:[1,0,1]
	v_pk_fma_f32 v[238:239], v[190:191], s[14:15], v[238:239] op_sel_hi:[1,0,1]
	v_readlane_b32 s14, v1, 56
	v_cvt_pk_f32_fp8_e32 v[184:185], v12
	v_cvt_pk_f32_fp8_sdwa v[186:187], v12 src0_sel:WORD_1
	v_pk_fma_f32 v[224:225], v[184:185], s[14:15], v[224:225] op_sel_hi:[1,0,1]
	v_pk_fma_f32 v[226:227], v[186:187], s[14:15], v[226:227] op_sel_hi:[1,0,1]
	v_cvt_pk_f32_fp8_e32 v[188:189], v13
	v_cvt_pk_f32_fp8_sdwa v[190:191], v13 src0_sel:WORD_1
	v_pk_fma_f32 v[228:229], v[188:189], s[14:15], v[228:229] op_sel_hi:[1,0,1]
	v_pk_fma_f32 v[230:231], v[190:191], s[14:15], v[230:231] op_sel_hi:[1,0,1]
	v_cvt_pk_f32_fp8_e32 v[184:185], v14
	v_cvt_pk_f32_fp8_sdwa v[186:187], v14 src0_sel:WORD_1
	v_pk_fma_f32 v[232:233], v[184:185], s[14:15], v[232:233] op_sel_hi:[1,0,1]
	v_pk_fma_f32 v[234:235], v[186:187], s[14:15], v[234:235] op_sel_hi:[1,0,1]
	v_cvt_pk_f32_fp8_e32 v[188:189], v15
	v_cvt_pk_f32_fp8_sdwa v[190:191], v15 src0_sel:WORD_1
	v_pk_fma_f32 v[236:237], v[188:189], s[14:15], v[236:237] op_sel_hi:[1,0,1]
	v_pk_fma_f32 v[238:239], v[190:191], s[14:15], v[238:239] op_sel_hi:[1,0,1]
	s_branch .Lp6c0_axdone
.Lp6c0_t7:
	v_readlane_b32 s14, v1, 0
	v_cvt_pk_f32_fp8_e32 v[184:185], v68
	v_cvt_pk_f32_fp8_sdwa v[186:187], v68 src0_sel:WORD_1
	v_pk_fma_f32 v[240:241], v[184:185], s[14:15], v[240:241] op_sel_hi:[1,0,1]
	v_pk_fma_f32 v[242:243], v[186:187], s[14:15], v[242:243] op_sel_hi:[1,0,1]
	v_cvt_pk_f32_fp8_e32 v[188:189], v69
	v_cvt_pk_f32_fp8_sdwa v[190:191], v69 src0_sel:WORD_1
	v_pk_fma_f32 v[244:245], v[188:189], s[14:15], v[244:245] op_sel_hi:[1,0,1]
	v_pk_fma_f32 v[246:247], v[190:191], s[14:15], v[246:247] op_sel_hi:[1,0,1]
	v_cvt_pk_f32_fp8_e32 v[184:185], v70
	v_cvt_pk_f32_fp8_sdwa v[186:187], v70 src0_sel:WORD_1
	v_pk_fma_f32 v[248:249], v[184:185], s[14:15], v[248:249] op_sel_hi:[1,0,1]
	v_pk_fma_f32 v[250:251], v[186:187], s[14:15], v[250:251] op_sel_hi:[1,0,1]
	v_cvt_pk_f32_fp8_e32 v[188:189], v71
	v_cvt_pk_f32_fp8_sdwa v[190:191], v71 src0_sel:WORD_1
	v_pk_fma_f32 v[216:217], v[188:189], s[14:15], v[216:217] op_sel_hi:[1,0,1]
	v_pk_fma_f32 v[218:219], v[190:191], s[14:15], v[218:219] op_sel_hi:[1,0,1]
	v_readlane_b32 s14, v1, 8
	v_cvt_pk_f32_fp8_e32 v[184:185], v64
	v_cvt_pk_f32_fp8_sdwa v[186:187], v64 src0_sel:WORD_1
	v_pk_fma_f32 v[240:241], v[184:185], s[14:15], v[240:241] op_sel_hi:[1,0,1]
	v_pk_fma_f32 v[242:243], v[186:187], s[14:15], v[242:243] op_sel_hi:[1,0,1]
	v_cvt_pk_f32_fp8_e32 v[188:189], v65
	v_cvt_pk_f32_fp8_sdwa v[190:191], v65 src0_sel:WORD_1
	v_pk_fma_f32 v[244:245], v[188:189], s[14:15], v[244:245] op_sel_hi:[1,0,1]
	v_pk_fma_f32 v[246:247], v[190:191], s[14:15], v[246:247] op_sel_hi:[1,0,1]
	v_cvt_pk_f32_fp8_e32 v[184:185], v66
	v_cvt_pk_f32_fp8_sdwa v[186:187], v66 src0_sel:WORD_1
	v_pk_fma_f32 v[248:249], v[184:185], s[14:15], v[248:249] op_sel_hi:[1,0,1]
	v_pk_fma_f32 v[250:251], v[186:187], s[14:15], v[250:251] op_sel_hi:[1,0,1]
	v_cvt_pk_f32_fp8_e32 v[188:189], v67
	v_cvt_pk_f32_fp8_sdwa v[190:191], v67 src0_sel:WORD_1
	v_pk_fma_f32 v[216:217], v[188:189], s[14:15], v[216:217] op_sel_hi:[1,0,1]
	v_pk_fma_f32 v[218:219], v[190:191], s[14:15], v[218:219] op_sel_hi:[1,0,1]
	s_cmp_le_u32 s36, 2
	s_cbranch_scc1 .Lp6c0_axdone
	v_readlane_b32 s14, v1, 16
	v_cvt_pk_f32_fp8_e32 v[184:185], v60
	v_cvt_pk_f32_fp8_sdwa v[186:187], v60 src0_sel:WORD_1
	v_pk_fma_f32 v[240:241], v[184:185], s[14:15], v[240:241] op_sel_hi:[1,0,1]
	v_pk_fma_f32 v[242:243], v[186:187], s[14:15], v[242:243] op_sel_hi:[1,0,1]
	v_cvt_pk_f32_fp8_e32 v[188:189], v61
	v_cvt_pk_f32_fp8_sdwa v[190:191], v61 src0_sel:WORD_1
	v_pk_fma_f32 v[244:245], v[188:189], s[14:15], v[244:245] op_sel_hi:[1,0,1]
	v_pk_fma_f32 v[246:247], v[190:191], s[14:15], v[246:247] op_sel_hi:[1,0,1]
	v_cvt_pk_f32_fp8_e32 v[184:185], v62
	v_cvt_pk_f32_fp8_sdwa v[186:187], v62 src0_sel:WORD_1
	v_pk_fma_f32 v[248:249], v[184:185], s[14:15], v[248:249] op_sel_hi:[1,0,1]
	v_pk_fma_f32 v[250:251], v[186:187], s[14:15], v[250:251] op_sel_hi:[1,0,1]
	v_cvt_pk_f32_fp8_e32 v[188:189], v63
	v_cvt_pk_f32_fp8_sdwa v[190:191], v63 src0_sel:WORD_1
	v_pk_fma_f32 v[216:217], v[188:189], s[14:15], v[216:217] op_sel_hi:[1,0,1]
	v_pk_fma_f32 v[218:219], v[190:191], s[14:15], v[218:219] op_sel_hi:[1,0,1]
	v_readlane_b32 s14, v1, 24
	v_cvt_pk_f32_fp8_e32 v[184:185], v56
	v_cvt_pk_f32_fp8_sdwa v[186:187], v56 src0_sel:WORD_1
	v_pk_fma_f32 v[240:241], v[184:185], s[14:15], v[240:241] op_sel_hi:[1,0,1]
	v_pk_fma_f32 v[242:243], v[186:187], s[14:15], v[242:243] op_sel_hi:[1,0,1]
	v_cvt_pk_f32_fp8_e32 v[188:189], v57
	v_cvt_pk_f32_fp8_sdwa v[190:191], v57 src0_sel:WORD_1
	v_pk_fma_f32 v[244:245], v[188:189], s[14:15], v[244:245] op_sel_hi:[1,0,1]
	v_pk_fma_f32 v[246:247], v[190:191], s[14:15], v[246:247] op_sel_hi:[1,0,1]
	v_cvt_pk_f32_fp8_e32 v[184:185], v58
	v_cvt_pk_f32_fp8_sdwa v[186:187], v58 src0_sel:WORD_1
	v_pk_fma_f32 v[248:249], v[184:185], s[14:15], v[248:249] op_sel_hi:[1,0,1]
	v_pk_fma_f32 v[250:251], v[186:187], s[14:15], v[250:251] op_sel_hi:[1,0,1]
	v_cvt_pk_f32_fp8_e32 v[188:189], v59
	v_cvt_pk_f32_fp8_sdwa v[190:191], v59 src0_sel:WORD_1
	v_pk_fma_f32 v[216:217], v[188:189], s[14:15], v[216:217] op_sel_hi:[1,0,1]
	v_pk_fma_f32 v[218:219], v[190:191], s[14:15], v[218:219] op_sel_hi:[1,0,1]
	s_cmp_le_u32 s36, 4
	s_cbranch_scc1 .Lp6c0_axdone
	v_readlane_b32 s14, v1, 32
	v_cvt_pk_f32_fp8_e32 v[184:185], v48
	v_cvt_pk_f32_fp8_sdwa v[186:187], v48 src0_sel:WORD_1
	v_pk_fma_f32 v[240:241], v[184:185], s[14:15], v[240:241] op_sel_hi:[1,0,1]
	v_pk_fma_f32 v[242:243], v[186:187], s[14:15], v[242:243] op_sel_hi:[1,0,1]
	v_cvt_pk_f32_fp8_e32 v[188:189], v49
	v_cvt_pk_f32_fp8_sdwa v[190:191], v49 src0_sel:WORD_1
	v_pk_fma_f32 v[244:245], v[188:189], s[14:15], v[244:245] op_sel_hi:[1,0,1]
	v_pk_fma_f32 v[246:247], v[190:191], s[14:15], v[246:247] op_sel_hi:[1,0,1]
	v_cvt_pk_f32_fp8_e32 v[184:185], v50
	v_cvt_pk_f32_fp8_sdwa v[186:187], v50 src0_sel:WORD_1
	v_pk_fma_f32 v[248:249], v[184:185], s[14:15], v[248:249] op_sel_hi:[1,0,1]
	v_pk_fma_f32 v[250:251], v[186:187], s[14:15], v[250:251] op_sel_hi:[1,0,1]
	v_cvt_pk_f32_fp8_e32 v[188:189], v51
	v_cvt_pk_f32_fp8_sdwa v[190:191], v51 src0_sel:WORD_1
	v_pk_fma_f32 v[216:217], v[188:189], s[14:15], v[216:217] op_sel_hi:[1,0,1]
	v_pk_fma_f32 v[218:219], v[190:191], s[14:15], v[218:219] op_sel_hi:[1,0,1]
	v_readlane_b32 s14, v1, 40
	v_cvt_pk_f32_fp8_e32 v[184:185], v32
	v_cvt_pk_f32_fp8_sdwa v[186:187], v32 src0_sel:WORD_1
	v_pk_fma_f32 v[240:241], v[184:185], s[14:15], v[240:241] op_sel_hi:[1,0,1]
	v_pk_fma_f32 v[242:243], v[186:187], s[14:15], v[242:243] op_sel_hi:[1,0,1]
	v_cvt_pk_f32_fp8_e32 v[188:189], v33
	v_cvt_pk_f32_fp8_sdwa v[190:191], v33 src0_sel:WORD_1
	v_pk_fma_f32 v[244:245], v[188:189], s[14:15], v[244:245] op_sel_hi:[1,0,1]
	v_pk_fma_f32 v[246:247], v[190:191], s[14:15], v[246:247] op_sel_hi:[1,0,1]
	v_cvt_pk_f32_fp8_e32 v[184:185], v34
	v_cvt_pk_f32_fp8_sdwa v[186:187], v34 src0_sel:WORD_1
	v_pk_fma_f32 v[248:249], v[184:185], s[14:15], v[248:249] op_sel_hi:[1,0,1]
	v_pk_fma_f32 v[250:251], v[186:187], s[14:15], v[250:251] op_sel_hi:[1,0,1]
	v_cvt_pk_f32_fp8_e32 v[188:189], v35
	v_cvt_pk_f32_fp8_sdwa v[190:191], v35 src0_sel:WORD_1
	v_pk_fma_f32 v[216:217], v[188:189], s[14:15], v[216:217] op_sel_hi:[1,0,1]
	v_pk_fma_f32 v[218:219], v[190:191], s[14:15], v[218:219] op_sel_hi:[1,0,1]
	s_cmp_le_u32 s36, 6
	s_cbranch_scc1 .Lp6c0_axdone
	v_readlane_b32 s14, v1, 48
	v_cvt_pk_f32_fp8_e32 v[184:185], v16
	v_cvt_pk_f32_fp8_sdwa v[186:187], v16 src0_sel:WORD_1
	v_pk_fma_f32 v[240:241], v[184:185], s[14:15], v[240:241] op_sel_hi:[1,0,1]
	v_pk_fma_f32 v[242:243], v[186:187], s[14:15], v[242:243] op_sel_hi:[1,0,1]
	v_cvt_pk_f32_fp8_e32 v[188:189], v17
	v_cvt_pk_f32_fp8_sdwa v[190:191], v17 src0_sel:WORD_1
	v_pk_fma_f32 v[244:245], v[188:189], s[14:15], v[244:245] op_sel_hi:[1,0,1]
	v_pk_fma_f32 v[246:247], v[190:191], s[14:15], v[246:247] op_sel_hi:[1,0,1]
	v_cvt_pk_f32_fp8_e32 v[184:185], v18
	v_cvt_pk_f32_fp8_sdwa v[186:187], v18 src0_sel:WORD_1
	v_pk_fma_f32 v[248:249], v[184:185], s[14:15], v[248:249] op_sel_hi:[1,0,1]
	v_pk_fma_f32 v[250:251], v[186:187], s[14:15], v[250:251] op_sel_hi:[1,0,1]
	v_cvt_pk_f32_fp8_e32 v[188:189], v19
	v_cvt_pk_f32_fp8_sdwa v[190:191], v19 src0_sel:WORD_1
	v_pk_fma_f32 v[216:217], v[188:189], s[14:15], v[216:217] op_sel_hi:[1,0,1]
	v_pk_fma_f32 v[218:219], v[190:191], s[14:15], v[218:219] op_sel_hi:[1,0,1]
	v_readlane_b32 s14, v1, 56
	v_cvt_pk_f32_fp8_e32 v[184:185], v12
	v_cvt_pk_f32_fp8_sdwa v[186:187], v12 src0_sel:WORD_1
	v_pk_fma_f32 v[240:241], v[184:185], s[14:15], v[240:241] op_sel_hi:[1,0,1]
	v_pk_fma_f32 v[242:243], v[186:187], s[14:15], v[242:243] op_sel_hi:[1,0,1]
	v_cvt_pk_f32_fp8_e32 v[188:189], v13
	v_cvt_pk_f32_fp8_sdwa v[190:191], v13 src0_sel:WORD_1
	v_pk_fma_f32 v[244:245], v[188:189], s[14:15], v[244:245] op_sel_hi:[1,0,1]
	v_pk_fma_f32 v[246:247], v[190:191], s[14:15], v[246:247] op_sel_hi:[1,0,1]
	v_cvt_pk_f32_fp8_e32 v[184:185], v14
	v_cvt_pk_f32_fp8_sdwa v[186:187], v14 src0_sel:WORD_1
	v_pk_fma_f32 v[248:249], v[184:185], s[14:15], v[248:249] op_sel_hi:[1,0,1]
	v_pk_fma_f32 v[250:251], v[186:187], s[14:15], v[250:251] op_sel_hi:[1,0,1]
	v_cvt_pk_f32_fp8_e32 v[188:189], v15
	v_cvt_pk_f32_fp8_sdwa v[190:191], v15 src0_sel:WORD_1
	v_pk_fma_f32 v[216:217], v[188:189], s[14:15], v[216:217] op_sel_hi:[1,0,1]
	v_pk_fma_f32 v[218:219], v[190:191], s[14:15], v[218:219] op_sel_hi:[1,0,1]
	s_branch .Lp6c0_axdone
.Lp6c0_axdone:
	s_nop 4
	buffer_load_dwordx4 v[68:71], v181, s[92:95], s44 offen
	buffer_load_dwordx4 v[64:67], v181, s[92:95], s45 offen
	buffer_load_dwordx4 v[60:63], v181, s[92:95], s46 offen
	buffer_load_dwordx4 v[56:59], v181, s[92:95], s47 offen
	buffer_load_dwordx4 v[48:51], v181, s[92:95], s48 offen
	buffer_load_dwordx4 v[32:35], v181, s[92:95], s49 offen
	buffer_load_dwordx4 v[16:19], v181, s[92:95], s50 offen
	buffer_load_dwordx4 v[12:15], v181, s[92:95], s51 offen
	s_mov_b32 s26, s86
	s_mov_b32 s86, s32
	s_mov_b32 s32, s37
	s_cmp_eq_u32 s22, s23
	s_cbranch_scc1 .Lp6_B8done

.Lp6c1_t0:
	v_readlane_b32 s14, v1, 0
	v_cvt_pk_f32_fp8_e32 v[184:185], v72
	v_cvt_pk_f32_fp8_sdwa v[186:187], v72 src0_sel:WORD_1
	v_pk_fma_f32 v[126:127], v[184:185], s[14:15], v[126:127] op_sel_hi:[1,0,1]
	v_pk_fma_f32 v[128:129], v[186:187], s[14:15], v[128:129] op_sel_hi:[1,0,1]
	v_cvt_pk_f32_fp8_e32 v[188:189], v73
	v_cvt_pk_f32_fp8_sdwa v[190:191], v73 src0_sel:WORD_1
	v_pk_fma_f32 v[130:131], v[188:189], s[14:15], v[130:131] op_sel_hi:[1,0,1]
	v_pk_fma_f32 v[132:133], v[190:191], s[14:15], v[132:133] op_sel_hi:[1,0,1]
	v_cvt_pk_f32_fp8_e32 v[184:185], v74
	v_cvt_pk_f32_fp8_sdwa v[186:187], v74 src0_sel:WORD_1
	v_pk_fma_f32 v[134:135], v[184:185], s[14:15], v[134:135] op_sel_hi:[1,0,1]
	v_pk_fma_f32 v[136:137], v[186:187], s[14:15], v[136:137] op_sel_hi:[1,0,1]
	v_cvt_pk_f32_fp8_e32 v[188:189], v75
	v_cvt_pk_f32_fp8_sdwa v[190:191], v75 src0_sel:WORD_1
	v_pk_fma_f32 v[138:139], v[188:189], s[14:15], v[138:139] op_sel_hi:[1,0,1]
	v_pk_fma_f32 v[140:141], v[190:191], s[14:15], v[140:141] op_sel_hi:[1,0,1]
	v_readlane_b32 s14, v1, 8
	v_cvt_pk_f32_fp8_e32 v[184:185], v52
	v_cvt_pk_f32_fp8_sdwa v[186:187], v52 src0_sel:WORD_1
	v_pk_fma_f32 v[126:127], v[184:185], s[14:15], v[126:127] op_sel_hi:[1,0,1]
	v_pk_fma_f32 v[128:129], v[186:187], s[14:15], v[128:129] op_sel_hi:[1,0,1]
	v_cvt_pk_f32_fp8_e32 v[188:189], v53
	v_cvt_pk_f32_fp8_sdwa v[190:191], v53 src0_sel:WORD_1
	v_pk_fma_f32 v[130:131], v[188:189], s[14:15], v[130:131] op_sel_hi:[1,0,1]
	v_pk_fma_f32 v[132:133], v[190:191], s[14:15], v[132:133] op_sel_hi:[1,0,1]
	v_cvt_pk_f32_fp8_e32 v[184:185], v54
	v_cvt_pk_f32_fp8_sdwa v[186:187], v54 src0_sel:WORD_1
	v_pk_fma_f32 v[134:135], v[184:185], s[14:15], v[134:135] op_sel_hi:[1,0,1]
	v_pk_fma_f32 v[136:137], v[186:187], s[14:15], v[136:137] op_sel_hi:[1,0,1]
	v_cvt_pk_f32_fp8_e32 v[188:189], v55
	v_cvt_pk_f32_fp8_sdwa v[190:191], v55 src0_sel:WORD_1
	v_pk_fma_f32 v[138:139], v[188:189], s[14:15], v[138:139] op_sel_hi:[1,0,1]
	v_pk_fma_f32 v[140:141], v[190:191], s[14:15], v[140:141] op_sel_hi:[1,0,1]
	s_cmp_le_u32 s36, 2
	s_cbranch_scc1 .Lp6c1_axdone
	v_readlane_b32 s14, v1, 16
	v_cvt_pk_f32_fp8_e32 v[184:185], v44
	v_cvt_pk_f32_fp8_sdwa v[186:187], v44 src0_sel:WORD_1
	v_pk_fma_f32 v[126:127], v[184:185], s[14:15], v[126:127] op_sel_hi:[1,0,1]
	v_pk_fma_f32 v[128:129], v[186:187], s[14:15], v[128:129] op_sel_hi:[1,0,1]
	v_cvt_pk_f32_fp8_e32 v[188:189], v45
	v_cvt_pk_f32_fp8_sdwa v[190:191], v45 src0_sel:WORD_1
	v_pk_fma_f32 v[130:131], v[188:189], s[14:15], v[130:131] op_sel_hi:[1,0,1]
	v_pk_fma_f32 v[132:133], v[190:191], s[14:15], v[132:133] op_sel_hi:[1,0,1]
	v_cvt_pk_f32_fp8_e32 v[184:185], v46
	v_cvt_pk_f32_fp8_sdwa v[186:187], v46 src0_sel:WORD_1
	v_pk_fma_f32 v[134:135], v[184:185], s[14:15], v[134:135] op_sel_hi:[1,0,1]
	v_pk_fma_f32 v[136:137], v[186:187], s[14:15], v[136:137] op_sel_hi:[1,0,1]
	v_cvt_pk_f32_fp8_e32 v[188:189], v47
	v_cvt_pk_f32_fp8_sdwa v[190:191], v47 src0_sel:WORD_1
	v_pk_fma_f32 v[138:139], v[188:189], s[14:15], v[138:139] op_sel_hi:[1,0,1]
	v_pk_fma_f32 v[140:141], v[190:191], s[14:15], v[140:141] op_sel_hi:[1,0,1]
	v_readlane_b32 s14, v1, 24
	v_cvt_pk_f32_fp8_e32 v[184:185], v40
	v_cvt_pk_f32_fp8_sdwa v[186:187], v40 src0_sel:WORD_1
	v_pk_fma_f32 v[126:127], v[184:185], s[14:15], v[126:127] op_sel_hi:[1,0,1]
	v_pk_fma_f32 v[128:129], v[186:187], s[14:15], v[128:129] op_sel_hi:[1,0,1]
	v_cvt_pk_f32_fp8_e32 v[188:189], v41
	v_cvt_pk_f32_fp8_sdwa v[190:191], v41 src0_sel:WORD_1
	v_pk_fma_f32 v[130:131], v[188:189], s[14:15], v[130:131] op_sel_hi:[1,0,1]
	v_pk_fma_f32 v[132:133], v[190:191], s[14:15], v[132:133] op_sel_hi:[1,0,1]
	v_cvt_pk_f32_fp8_e32 v[184:185], v42
	v_cvt_pk_f32_fp8_sdwa v[186:187], v42 src0_sel:WORD_1
	v_pk_fma_f32 v[134:135], v[184:185], s[14:15], v[134:135] op_sel_hi:[1,0,1]
	v_pk_fma_f32 v[136:137], v[186:187], s[14:15], v[136:137] op_sel_hi:[1,0,1]
	v_cvt_pk_f32_fp8_e32 v[188:189], v43
	v_cvt_pk_f32_fp8_sdwa v[190:191], v43 src0_sel:WORD_1
	v_pk_fma_f32 v[138:139], v[188:189], s[14:15], v[138:139] op_sel_hi:[1,0,1]
	v_pk_fma_f32 v[140:141], v[190:191], s[14:15], v[140:141] op_sel_hi:[1,0,1]
	s_cmp_le_u32 s36, 4
	s_cbranch_scc1 .Lp6c1_axdone
	v_readlane_b32 s14, v1, 32
	v_cvt_pk_f32_fp8_e32 v[184:185], v36
	v_cvt_pk_f32_fp8_sdwa v[186:187], v36 src0_sel:WORD_1
	v_pk_fma_f32 v[126:127], v[184:185], s[14:15], v[126:127] op_sel_hi:[1,0,1]
	v_pk_fma_f32 v[128:129], v[186:187], s[14:15], v[128:129] op_sel_hi:[1,0,1]
	v_cvt_pk_f32_fp8_e32 v[188:189], v37
	v_cvt_pk_f32_fp8_sdwa v[190:191], v37 src0_sel:WORD_1
	v_pk_fma_f32 v[130:131], v[188:189], s[14:15], v[130:131] op_sel_hi:[1,0,1]
	v_pk_fma_f32 v[132:133], v[190:191], s[14:15], v[132:133] op_sel_hi:[1,0,1]
	v_cvt_pk_f32_fp8_e32 v[184:185], v38
	v_cvt_pk_f32_fp8_sdwa v[186:187], v38 src0_sel:WORD_1
	v_pk_fma_f32 v[134:135], v[184:185], s[14:15], v[134:135] op_sel_hi:[1,0,1]
	v_pk_fma_f32 v[136:137], v[186:187], s[14:15], v[136:137] op_sel_hi:[1,0,1]
	v_cvt_pk_f32_fp8_e32 v[188:189], v39
	v_cvt_pk_f32_fp8_sdwa v[190:191], v39 src0_sel:WORD_1
	v_pk_fma_f32 v[138:139], v[188:189], s[14:15], v[138:139] op_sel_hi:[1,0,1]
	v_pk_fma_f32 v[140:141], v[190:191], s[14:15], v[140:141] op_sel_hi:[1,0,1]
	v_readlane_b32 s14, v1, 40
	v_cvt_pk_f32_fp8_e32 v[184:185], v28
	v_cvt_pk_f32_fp8_sdwa v[186:187], v28 src0_sel:WORD_1
	v_pk_fma_f32 v[126:127], v[184:185], s[14:15], v[126:127] op_sel_hi:[1,0,1]
	v_pk_fma_f32 v[128:129], v[186:187], s[14:15], v[128:129] op_sel_hi:[1,0,1]
	v_cvt_pk_f32_fp8_e32 v[188:189], v29
	v_cvt_pk_f32_fp8_sdwa v[190:191], v29 src0_sel:WORD_1
	v_pk_fma_f32 v[130:131], v[188:189], s[14:15], v[130:131] op_sel_hi:[1,0,1]
	v_pk_fma_f32 v[132:133], v[190:191], s[14:15], v[132:133] op_sel_hi:[1,0,1]
	v_cvt_pk_f32_fp8_e32 v[184:185], v30
	v_cvt_pk_f32_fp8_sdwa v[186:187], v30 src0_sel:WORD_1
	v_pk_fma_f32 v[134:135], v[184:185], s[14:15], v[134:135] op_sel_hi:[1,0,1]
	v_pk_fma_f32 v[136:137], v[186:187], s[14:15], v[136:137] op_sel_hi:[1,0,1]
	v_cvt_pk_f32_fp8_e32 v[188:189], v31
	v_cvt_pk_f32_fp8_sdwa v[190:191], v31 src0_sel:WORD_1
	v_pk_fma_f32 v[138:139], v[188:189], s[14:15], v[138:139] op_sel_hi:[1,0,1]
	v_pk_fma_f32 v[140:141], v[190:191], s[14:15], v[140:141] op_sel_hi:[1,0,1]
	s_cmp_le_u32 s36, 6
	s_cbranch_scc1 .Lp6c1_axdone
	v_readlane_b32 s14, v1, 48
	v_cvt_pk_f32_fp8_e32 v[184:185], v24
	v_cvt_pk_f32_fp8_sdwa v[186:187], v24 src0_sel:WORD_1
	v_pk_fma_f32 v[126:127], v[184:185], s[14:15], v[126:127] op_sel_hi:[1,0,1]
	v_pk_fma_f32 v[128:129], v[186:187], s[14:15], v[128:129] op_sel_hi:[1,0,1]
	v_cvt_pk_f32_fp8_e32 v[188:189], v25
	v_cvt_pk_f32_fp8_sdwa v[190:191], v25 src0_sel:WORD_1
	v_pk_fma_f32 v[130:131], v[188:189], s[14:15], v[130:131] op_sel_hi:[1,0,1]
	v_pk_fma_f32 v[132:133], v[190:191], s[14:15], v[132:133] op_sel_hi:[1,0,1]
	v_cvt_pk_f32_fp8_e32 v[184:185], v26
	v_cvt_pk_f32_fp8_sdwa v[186:187], v26 src0_sel:WORD_1
	v_pk_fma_f32 v[134:135], v[184:185], s[14:15], v[134:135] op_sel_hi:[1,0,1]
	v_pk_fma_f32 v[136:137], v[186:187], s[14:15], v[136:137] op_sel_hi:[1,0,1]
	v_cvt_pk_f32_fp8_e32 v[188:189], v27
	v_cvt_pk_f32_fp8_sdwa v[190:191], v27 src0_sel:WORD_1
	v_pk_fma_f32 v[138:139], v[188:189], s[14:15], v[138:139] op_sel_hi:[1,0,1]
	v_pk_fma_f32 v[140:141], v[190:191], s[14:15], v[140:141] op_sel_hi:[1,0,1]
	v_readlane_b32 s14, v1, 56
	v_cvt_pk_f32_fp8_e32 v[184:185], v20
	v_cvt_pk_f32_fp8_sdwa v[186:187], v20 src0_sel:WORD_1
	v_pk_fma_f32 v[126:127], v[184:185], s[14:15], v[126:127] op_sel_hi:[1,0,1]
	v_pk_fma_f32 v[128:129], v[186:187], s[14:15], v[128:129] op_sel_hi:[1,0,1]
	v_cvt_pk_f32_fp8_e32 v[188:189], v21
	v_cvt_pk_f32_fp8_sdwa v[190:191], v21 src0_sel:WORD_1
	v_pk_fma_f32 v[130:131], v[188:189], s[14:15], v[130:131] op_sel_hi:[1,0,1]
	v_pk_fma_f32 v[132:133], v[190:191], s[14:15], v[132:133] op_sel_hi:[1,0,1]
	v_cvt_pk_f32_fp8_e32 v[184:185], v22
	v_cvt_pk_f32_fp8_sdwa v[186:187], v22 src0_sel:WORD_1
	v_pk_fma_f32 v[134:135], v[184:185], s[14:15], v[134:135] op_sel_hi:[1,0,1]
	v_pk_fma_f32 v[136:137], v[186:187], s[14:15], v[136:137] op_sel_hi:[1,0,1]
	v_cvt_pk_f32_fp8_e32 v[188:189], v23
	v_cvt_pk_f32_fp8_sdwa v[190:191], v23 src0_sel:WORD_1
	v_pk_fma_f32 v[138:139], v[188:189], s[14:15], v[138:139] op_sel_hi:[1,0,1]
	v_pk_fma_f32 v[140:141], v[190:191], s[14:15], v[140:141] op_sel_hi:[1,0,1]
	s_branch .Lp6c1_axdone
.Lp6c1_t1:
	v_readlane_b32 s14, v1, 0
	v_cvt_pk_f32_fp8_e32 v[184:185], v72
	v_cvt_pk_f32_fp8_sdwa v[186:187], v72 src0_sel:WORD_1
	v_pk_fma_f32 v[110:111], v[184:185], s[14:15], v[110:111] op_sel_hi:[1,0,1]
	v_pk_fma_f32 v[112:113], v[186:187], s[14:15], v[112:113] op_sel_hi:[1,0,1]
	v_cvt_pk_f32_fp8_e32 v[188:189], v73
	v_cvt_pk_f32_fp8_sdwa v[190:191], v73 src0_sel:WORD_1
	v_pk_fma_f32 v[114:115], v[188:189], s[14:15], v[114:115] op_sel_hi:[1,0,1]
	v_pk_fma_f32 v[116:117], v[190:191], s[14:15], v[116:117] op_sel_hi:[1,0,1]
	v_cvt_pk_f32_fp8_e32 v[184:185], v74
	v_cvt_pk_f32_fp8_sdwa v[186:187], v74 src0_sel:WORD_1
	v_pk_fma_f32 v[118:119], v[184:185], s[14:15], v[118:119] op_sel_hi:[1,0,1]
	v_pk_fma_f32 v[120:121], v[186:187], s[14:15], v[120:121] op_sel_hi:[1,0,1]
	v_cvt_pk_f32_fp8_e32 v[188:189], v75
	v_cvt_pk_f32_fp8_sdwa v[190:191], v75 src0_sel:WORD_1
	v_pk_fma_f32 v[122:123], v[188:189], s[14:15], v[122:123] op_sel_hi:[1,0,1]
	v_pk_fma_f32 v[124:125], v[190:191], s[14:15], v[124:125] op_sel_hi:[1,0,1]
	v_readlane_b32 s14, v1, 8
	v_cvt_pk_f32_fp8_e32 v[184:185], v52
	v_cvt_pk_f32_fp8_sdwa v[186:187], v52 src0_sel:WORD_1
	v_pk_fma_f32 v[110:111], v[184:185], s[14:15], v[110:111] op_sel_hi:[1,0,1]
	v_pk_fma_f32 v[112:113], v[186:187], s[14:15], v[112:113] op_sel_hi:[1,0,1]
	v_cvt_pk_f32_fp8_e32 v[188:189], v53
	v_cvt_pk_f32_fp8_sdwa v[190:191], v53 src0_sel:WORD_1
	v_pk_fma_f32 v[114:115], v[188:189], s[14:15], v[114:115] op_sel_hi:[1,0,1]
	v_pk_fma_f32 v[116:117], v[190:191], s[14:15], v[116:117] op_sel_hi:[1,0,1]
	v_cvt_pk_f32_fp8_e32 v[184:185], v54
	v_cvt_pk_f32_fp8_sdwa v[186:187], v54 src0_sel:WORD_1
	v_pk_fma_f32 v[118:119], v[184:185], s[14:15], v[118:119] op_sel_hi:[1,0,1]
	v_pk_fma_f32 v[120:121], v[186:187], s[14:15], v[120:121] op_sel_hi:[1,0,1]
	v_cvt_pk_f32_fp8_e32 v[188:189], v55
	v_cvt_pk_f32_fp8_sdwa v[190:191], v55 src0_sel:WORD_1
	v_pk_fma_f32 v[122:123], v[188:189], s[14:15], v[122:123] op_sel_hi:[1,0,1]
	v_pk_fma_f32 v[124:125], v[190:191], s[14:15], v[124:125] op_sel_hi:[1,0,1]
	s_cmp_le_u32 s36, 2
	s_cbranch_scc1 .Lp6c1_axdone
	v_readlane_b32 s14, v1, 16
	v_cvt_pk_f32_fp8_e32 v[184:185], v44
	v_cvt_pk_f32_fp8_sdwa v[186:187], v44 src0_sel:WORD_1
	v_pk_fma_f32 v[110:111], v[184:185], s[14:15], v[110:111] op_sel_hi:[1,0,1]
	v_pk_fma_f32 v[112:113], v[186:187], s[14:15], v[112:113] op_sel_hi:[1,0,1]
	v_cvt_pk_f32_fp8_e32 v[188:189], v45
	v_cvt_pk_f32_fp8_sdwa v[190:191], v45 src0_sel:WORD_1
	v_pk_fma_f32 v[114:115], v[188:189], s[14:15], v[114:115] op_sel_hi:[1,0,1]
	v_pk_fma_f32 v[116:117], v[190:191], s[14:15], v[116:117] op_sel_hi:[1,0,1]
	v_cvt_pk_f32_fp8_e32 v[184:185], v46
	v_cvt_pk_f32_fp8_sdwa v[186:187], v46 src0_sel:WORD_1
	v_pk_fma_f32 v[118:119], v[184:185], s[14:15], v[118:119] op_sel_hi:[1,0,1]
	v_pk_fma_f32 v[120:121], v[186:187], s[14:15], v[120:121] op_sel_hi:[1,0,1]
	v_cvt_pk_f32_fp8_e32 v[188:189], v47
	v_cvt_pk_f32_fp8_sdwa v[190:191], v47 src0_sel:WORD_1
	v_pk_fma_f32 v[122:123], v[188:189], s[14:15], v[122:123] op_sel_hi:[1,0,1]
	v_pk_fma_f32 v[124:125], v[190:191], s[14:15], v[124:125] op_sel_hi:[1,0,1]
	v_readlane_b32 s14, v1, 24
	v_cvt_pk_f32_fp8_e32 v[184:185], v40
	v_cvt_pk_f32_fp8_sdwa v[186:187], v40 src0_sel:WORD_1
	v_pk_fma_f32 v[110:111], v[184:185], s[14:15], v[110:111] op_sel_hi:[1,0,1]
	v_pk_fma_f32 v[112:113], v[186:187], s[14:15], v[112:113] op_sel_hi:[1,0,1]
	v_cvt_pk_f32_fp8_e32 v[188:189], v41
	v_cvt_pk_f32_fp8_sdwa v[190:191], v41 src0_sel:WORD_1
	v_pk_fma_f32 v[114:115], v[188:189], s[14:15], v[114:115] op_sel_hi:[1,0,1]
	v_pk_fma_f32 v[116:117], v[190:191], s[14:15], v[116:117] op_sel_hi:[1,0,1]
	v_cvt_pk_f32_fp8_e32 v[184:185], v42
	v_cvt_pk_f32_fp8_sdwa v[186:187], v42 src0_sel:WORD_1
	v_pk_fma_f32 v[118:119], v[184:185], s[14:15], v[118:119] op_sel_hi:[1,0,1]
	v_pk_fma_f32 v[120:121], v[186:187], s[14:15], v[120:121] op_sel_hi:[1,0,1]
	v_cvt_pk_f32_fp8_e32 v[188:189], v43
	v_cvt_pk_f32_fp8_sdwa v[190:191], v43 src0_sel:WORD_1
	v_pk_fma_f32 v[122:123], v[188:189], s[14:15], v[122:123] op_sel_hi:[1,0,1]
	v_pk_fma_f32 v[124:125], v[190:191], s[14:15], v[124:125] op_sel_hi:[1,0,1]
	s_cmp_le_u32 s36, 4
	s_cbranch_scc1 .Lp6c1_axdone
	v_readlane_b32 s14, v1, 32
	v_cvt_pk_f32_fp8_e32 v[184:185], v36
	v_cvt_pk_f32_fp8_sdwa v[186:187], v36 src0_sel:WORD_1
	v_pk_fma_f32 v[110:111], v[184:185], s[14:15], v[110:111] op_sel_hi:[1,0,1]
	v_pk_fma_f32 v[112:113], v[186:187], s[14:15], v[112:113] op_sel_hi:[1,0,1]
	v_cvt_pk_f32_fp8_e32 v[188:189], v37
	v_cvt_pk_f32_fp8_sdwa v[190:191], v37 src0_sel:WORD_1
	v_pk_fma_f32 v[114:115], v[188:189], s[14:15], v[114:115] op_sel_hi:[1,0,1]
	v_pk_fma_f32 v[116:117], v[190:191], s[14:15], v[116:117] op_sel_hi:[1,0,1]
	v_cvt_pk_f32_fp8_e32 v[184:185], v38
	v_cvt_pk_f32_fp8_sdwa v[186:187], v38 src0_sel:WORD_1
	v_pk_fma_f32 v[118:119], v[184:185], s[14:15], v[118:119] op_sel_hi:[1,0,1]
	v_pk_fma_f32 v[120:121], v[186:187], s[14:15], v[120:121] op_sel_hi:[1,0,1]
	v_cvt_pk_f32_fp8_e32 v[188:189], v39
	v_cvt_pk_f32_fp8_sdwa v[190:191], v39 src0_sel:WORD_1
	v_pk_fma_f32 v[122:123], v[188:189], s[14:15], v[122:123] op_sel_hi:[1,0,1]
	v_pk_fma_f32 v[124:125], v[190:191], s[14:15], v[124:125] op_sel_hi:[1,0,1]
	v_readlane_b32 s14, v1, 40
	v_cvt_pk_f32_fp8_e32 v[184:185], v28
	v_cvt_pk_f32_fp8_sdwa v[186:187], v28 src0_sel:WORD_1
	v_pk_fma_f32 v[110:111], v[184:185], s[14:15], v[110:111] op_sel_hi:[1,0,1]
	v_pk_fma_f32 v[112:113], v[186:187], s[14:15], v[112:113] op_sel_hi:[1,0,1]
	v_cvt_pk_f32_fp8_e32 v[188:189], v29
	v_cvt_pk_f32_fp8_sdwa v[190:191], v29 src0_sel:WORD_1
	v_pk_fma_f32 v[114:115], v[188:189], s[14:15], v[114:115] op_sel_hi:[1,0,1]
	v_pk_fma_f32 v[116:117], v[190:191], s[14:15], v[116:117] op_sel_hi:[1,0,1]
	v_cvt_pk_f32_fp8_e32 v[184:185], v30
	v_cvt_pk_f32_fp8_sdwa v[186:187], v30 src0_sel:WORD_1
	v_pk_fma_f32 v[118:119], v[184:185], s[14:15], v[118:119] op_sel_hi:[1,0,1]
	v_pk_fma_f32 v[120:121], v[186:187], s[14:15], v[120:121] op_sel_hi:[1,0,1]
	v_cvt_pk_f32_fp8_e32 v[188:189], v31
	v_cvt_pk_f32_fp8_sdwa v[190:191], v31 src0_sel:WORD_1
	v_pk_fma_f32 v[122:123], v[188:189], s[14:15], v[122:123] op_sel_hi:[1,0,1]
	v_pk_fma_f32 v[124:125], v[190:191], s[14:15], v[124:125] op_sel_hi:[1,0,1]
	s_cmp_le_u32 s36, 6
	s_cbranch_scc1 .Lp6c1_axdone
	v_readlane_b32 s14, v1, 48
	v_cvt_pk_f32_fp8_e32 v[184:185], v24
	v_cvt_pk_f32_fp8_sdwa v[186:187], v24 src0_sel:WORD_1
	v_pk_fma_f32 v[110:111], v[184:185], s[14:15], v[110:111] op_sel_hi:[1,0,1]
	v_pk_fma_f32 v[112:113], v[186:187], s[14:15], v[112:113] op_sel_hi:[1,0,1]
	v_cvt_pk_f32_fp8_e32 v[188:189], v25
	v_cvt_pk_f32_fp8_sdwa v[190:191], v25 src0_sel:WORD_1
	v_pk_fma_f32 v[114:115], v[188:189], s[14:15], v[114:115] op_sel_hi:[1,0,1]
	v_pk_fma_f32 v[116:117], v[190:191], s[14:15], v[116:117] op_sel_hi:[1,0,1]
	v_cvt_pk_f32_fp8_e32 v[184:185], v26
	v_cvt_pk_f32_fp8_sdwa v[186:187], v26 src0_sel:WORD_1
	v_pk_fma_f32 v[118:119], v[184:185], s[14:15], v[118:119] op_sel_hi:[1,0,1]
	v_pk_fma_f32 v[120:121], v[186:187], s[14:15], v[120:121] op_sel_hi:[1,0,1]
	v_cvt_pk_f32_fp8_e32 v[188:189], v27
	v_cvt_pk_f32_fp8_sdwa v[190:191], v27 src0_sel:WORD_1
	v_pk_fma_f32 v[122:123], v[188:189], s[14:15], v[122:123] op_sel_hi:[1,0,1]
	v_pk_fma_f32 v[124:125], v[190:191], s[14:15], v[124:125] op_sel_hi:[1,0,1]
	v_readlane_b32 s14, v1, 56
	v_cvt_pk_f32_fp8_e32 v[184:185], v20
	v_cvt_pk_f32_fp8_sdwa v[186:187], v20 src0_sel:WORD_1
	v_pk_fma_f32 v[110:111], v[184:185], s[14:15], v[110:111] op_sel_hi:[1,0,1]
	v_pk_fma_f32 v[112:113], v[186:187], s[14:15], v[112:113] op_sel_hi:[1,0,1]
	v_cvt_pk_f32_fp8_e32 v[188:189], v21
	v_cvt_pk_f32_fp8_sdwa v[190:191], v21 src0_sel:WORD_1
	v_pk_fma_f32 v[114:115], v[188:189], s[14:15], v[114:115] op_sel_hi:[1,0,1]
	v_pk_fma_f32 v[116:117], v[190:191], s[14:15], v[116:117] op_sel_hi:[1,0,1]
	v_cvt_pk_f32_fp8_e32 v[184:185], v22
	v_cvt_pk_f32_fp8_sdwa v[186:187], v22 src0_sel:WORD_1
	v_pk_fma_f32 v[118:119], v[184:185], s[14:15], v[118:119] op_sel_hi:[1,0,1]
	v_pk_fma_f32 v[120:121], v[186:187], s[14:15], v[120:121] op_sel_hi:[1,0,1]
	v_cvt_pk_f32_fp8_e32 v[188:189], v23
	v_cvt_pk_f32_fp8_sdwa v[190:191], v23 src0_sel:WORD_1
	v_pk_fma_f32 v[122:123], v[188:189], s[14:15], v[122:123] op_sel_hi:[1,0,1]
	v_pk_fma_f32 v[124:125], v[190:191], s[14:15], v[124:125] op_sel_hi:[1,0,1]
	s_branch .Lp6c1_axdone
.Lp6c1_t2:
	v_readlane_b32 s14, v1, 0
	v_cvt_pk_f32_fp8_e32 v[184:185], v72
	v_cvt_pk_f32_fp8_sdwa v[186:187], v72 src0_sel:WORD_1
	v_pk_fma_f32 v[94:95], v[184:185], s[14:15], v[94:95] op_sel_hi:[1,0,1]
	v_pk_fma_f32 v[96:97], v[186:187], s[14:15], v[96:97] op_sel_hi:[1,0,1]
	v_cvt_pk_f32_fp8_e32 v[188:189], v73
	v_cvt_pk_f32_fp8_sdwa v[190:191], v73 src0_sel:WORD_1
	v_pk_fma_f32 v[98:99], v[188:189], s[14:15], v[98:99] op_sel_hi:[1,0,1]
	v_pk_fma_f32 v[100:101], v[190:191], s[14:15], v[100:101] op_sel_hi:[1,0,1]
	v_cvt_pk_f32_fp8_e32 v[184:185], v74
	v_cvt_pk_f32_fp8_sdwa v[186:187], v74 src0_sel:WORD_1
	v_pk_fma_f32 v[102:103], v[184:185], s[14:15], v[102:103] op_sel_hi:[1,0,1]
	v_pk_fma_f32 v[104:105], v[186:187], s[14:15], v[104:105] op_sel_hi:[1,0,1]
	v_cvt_pk_f32_fp8_e32 v[188:189], v75
	v_cvt_pk_f32_fp8_sdwa v[190:191], v75 src0_sel:WORD_1
	v_pk_fma_f32 v[106:107], v[188:189], s[14:15], v[106:107] op_sel_hi:[1,0,1]
	v_pk_fma_f32 v[108:109], v[190:191], s[14:15], v[108:109] op_sel_hi:[1,0,1]
	v_readlane_b32 s14, v1, 8
	v_cvt_pk_f32_fp8_e32 v[184:185], v52
	v_cvt_pk_f32_fp8_sdwa v[186:187], v52 src0_sel:WORD_1
	v_pk_fma_f32 v[94:95], v[184:185], s[14:15], v[94:95] op_sel_hi:[1,0,1]
	v_pk_fma_f32 v[96:97], v[186:187], s[14:15], v[96:97] op_sel_hi:[1,0,1]
	v_cvt_pk_f32_fp8_e32 v[188:189], v53
	v_cvt_pk_f32_fp8_sdwa v[190:191], v53 src0_sel:WORD_1
	v_pk_fma_f32 v[98:99], v[188:189], s[14:15], v[98:99] op_sel_hi:[1,0,1]
	v_pk_fma_f32 v[100:101], v[190:191], s[14:15], v[100:101] op_sel_hi:[1,0,1]
	v_cvt_pk_f32_fp8_e32 v[184:185], v54
	v_cvt_pk_f32_fp8_sdwa v[186:187], v54 src0_sel:WORD_1
	v_pk_fma_f32 v[102:103], v[184:185], s[14:15], v[102:103] op_sel_hi:[1,0,1]
	v_pk_fma_f32 v[104:105], v[186:187], s[14:15], v[104:105] op_sel_hi:[1,0,1]
	v_cvt_pk_f32_fp8_e32 v[188:189], v55
	v_cvt_pk_f32_fp8_sdwa v[190:191], v55 src0_sel:WORD_1
	v_pk_fma_f32 v[106:107], v[188:189], s[14:15], v[106:107] op_sel_hi:[1,0,1]
	v_pk_fma_f32 v[108:109], v[190:191], s[14:15], v[108:109] op_sel_hi:[1,0,1]
	s_cmp_le_u32 s36, 2
	s_cbranch_scc1 .Lp6c1_axdone
	v_readlane_b32 s14, v1, 16
	v_cvt_pk_f32_fp8_e32 v[184:185], v44
	v_cvt_pk_f32_fp8_sdwa v[186:187], v44 src0_sel:WORD_1
	v_pk_fma_f32 v[94:95], v[184:185], s[14:15], v[94:95] op_sel_hi:[1,0,1]
	v_pk_fma_f32 v[96:97], v[186:187], s[14:15], v[96:97] op_sel_hi:[1,0,1]
	v_cvt_pk_f32_fp8_e32 v[188:189], v45
	v_cvt_pk_f32_fp8_sdwa v[190:191], v45 src0_sel:WORD_1
	v_pk_fma_f32 v[98:99], v[188:189], s[14:15], v[98:99] op_sel_hi:[1,0,1]
	v_pk_fma_f32 v[100:101], v[190:191], s[14:15], v[100:101] op_sel_hi:[1,0,1]
	v_cvt_pk_f32_fp8_e32 v[184:185], v46
	v_cvt_pk_f32_fp8_sdwa v[186:187], v46 src0_sel:WORD_1
	v_pk_fma_f32 v[102:103], v[184:185], s[14:15], v[102:103] op_sel_hi:[1,0,1]
	v_pk_fma_f32 v[104:105], v[186:187], s[14:15], v[104:105] op_sel_hi:[1,0,1]
	v_cvt_pk_f32_fp8_e32 v[188:189], v47
	v_cvt_pk_f32_fp8_sdwa v[190:191], v47 src0_sel:WORD_1
	v_pk_fma_f32 v[106:107], v[188:189], s[14:15], v[106:107] op_sel_hi:[1,0,1]
	v_pk_fma_f32 v[108:109], v[190:191], s[14:15], v[108:109] op_sel_hi:[1,0,1]
	v_readlane_b32 s14, v1, 24
	v_cvt_pk_f32_fp8_e32 v[184:185], v40
	v_cvt_pk_f32_fp8_sdwa v[186:187], v40 src0_sel:WORD_1
	v_pk_fma_f32 v[94:95], v[184:185], s[14:15], v[94:95] op_sel_hi:[1,0,1]
	v_pk_fma_f32 v[96:97], v[186:187], s[14:15], v[96:97] op_sel_hi:[1,0,1]
	v_cvt_pk_f32_fp8_e32 v[188:189], v41
	v_cvt_pk_f32_fp8_sdwa v[190:191], v41 src0_sel:WORD_1
	v_pk_fma_f32 v[98:99], v[188:189], s[14:15], v[98:99] op_sel_hi:[1,0,1]
	v_pk_fma_f32 v[100:101], v[190:191], s[14:15], v[100:101] op_sel_hi:[1,0,1]
	v_cvt_pk_f32_fp8_e32 v[184:185], v42
	v_cvt_pk_f32_fp8_sdwa v[186:187], v42 src0_sel:WORD_1
	v_pk_fma_f32 v[102:103], v[184:185], s[14:15], v[102:103] op_sel_hi:[1,0,1]
	v_pk_fma_f32 v[104:105], v[186:187], s[14:15], v[104:105] op_sel_hi:[1,0,1]
	v_cvt_pk_f32_fp8_e32 v[188:189], v43
	v_cvt_pk_f32_fp8_sdwa v[190:191], v43 src0_sel:WORD_1
	v_pk_fma_f32 v[106:107], v[188:189], s[14:15], v[106:107] op_sel_hi:[1,0,1]
	v_pk_fma_f32 v[108:109], v[190:191], s[14:15], v[108:109] op_sel_hi:[1,0,1]
	s_cmp_le_u32 s36, 4
	s_cbranch_scc1 .Lp6c1_axdone
	v_readlane_b32 s14, v1, 32
	v_cvt_pk_f32_fp8_e32 v[184:185], v36
	v_cvt_pk_f32_fp8_sdwa v[186:187], v36 src0_sel:WORD_1
	v_pk_fma_f32 v[94:95], v[184:185], s[14:15], v[94:95] op_sel_hi:[1,0,1]
	v_pk_fma_f32 v[96:97], v[186:187], s[14:15], v[96:97] op_sel_hi:[1,0,1]
	v_cvt_pk_f32_fp8_e32 v[188:189], v37
	v_cvt_pk_f32_fp8_sdwa v[190:191], v37 src0_sel:WORD_1
	v_pk_fma_f32 v[98:99], v[188:189], s[14:15], v[98:99] op_sel_hi:[1,0,1]
	v_pk_fma_f32 v[100:101], v[190:191], s[14:15], v[100:101] op_sel_hi:[1,0,1]
	v_cvt_pk_f32_fp8_e32 v[184:185], v38
	v_cvt_pk_f32_fp8_sdwa v[186:187], v38 src0_sel:WORD_1
	v_pk_fma_f32 v[102:103], v[184:185], s[14:15], v[102:103] op_sel_hi:[1,0,1]
	v_pk_fma_f32 v[104:105], v[186:187], s[14:15], v[104:105] op_sel_hi:[1,0,1]
	v_cvt_pk_f32_fp8_e32 v[188:189], v39
	v_cvt_pk_f32_fp8_sdwa v[190:191], v39 src0_sel:WORD_1
	v_pk_fma_f32 v[106:107], v[188:189], s[14:15], v[106:107] op_sel_hi:[1,0,1]
	v_pk_fma_f32 v[108:109], v[190:191], s[14:15], v[108:109] op_sel_hi:[1,0,1]
	v_readlane_b32 s14, v1, 40
	v_cvt_pk_f32_fp8_e32 v[184:185], v28
	v_cvt_pk_f32_fp8_sdwa v[186:187], v28 src0_sel:WORD_1
	v_pk_fma_f32 v[94:95], v[184:185], s[14:15], v[94:95] op_sel_hi:[1,0,1]
	v_pk_fma_f32 v[96:97], v[186:187], s[14:15], v[96:97] op_sel_hi:[1,0,1]
	v_cvt_pk_f32_fp8_e32 v[188:189], v29
	v_cvt_pk_f32_fp8_sdwa v[190:191], v29 src0_sel:WORD_1
	v_pk_fma_f32 v[98:99], v[188:189], s[14:15], v[98:99] op_sel_hi:[1,0,1]
	v_pk_fma_f32 v[100:101], v[190:191], s[14:15], v[100:101] op_sel_hi:[1,0,1]
	v_cvt_pk_f32_fp8_e32 v[184:185], v30
	v_cvt_pk_f32_fp8_sdwa v[186:187], v30 src0_sel:WORD_1
	v_pk_fma_f32 v[102:103], v[184:185], s[14:15], v[102:103] op_sel_hi:[1,0,1]
	v_pk_fma_f32 v[104:105], v[186:187], s[14:15], v[104:105] op_sel_hi:[1,0,1]
	v_cvt_pk_f32_fp8_e32 v[188:189], v31
	v_cvt_pk_f32_fp8_sdwa v[190:191], v31 src0_sel:WORD_1
	v_pk_fma_f32 v[106:107], v[188:189], s[14:15], v[106:107] op_sel_hi:[1,0,1]
	v_pk_fma_f32 v[108:109], v[190:191], s[14:15], v[108:109] op_sel_hi:[1,0,1]
	s_cmp_le_u32 s36, 6
	s_cbranch_scc1 .Lp6c1_axdone
	v_readlane_b32 s14, v1, 48
	v_cvt_pk_f32_fp8_e32 v[184:185], v24
	v_cvt_pk_f32_fp8_sdwa v[186:187], v24 src0_sel:WORD_1
	v_pk_fma_f32 v[94:95], v[184:185], s[14:15], v[94:95] op_sel_hi:[1,0,1]
	v_pk_fma_f32 v[96:97], v[186:187], s[14:15], v[96:97] op_sel_hi:[1,0,1]
	v_cvt_pk_f32_fp8_e32 v[188:189], v25
	v_cvt_pk_f32_fp8_sdwa v[190:191], v25 src0_sel:WORD_1
	v_pk_fma_f32 v[98:99], v[188:189], s[14:15], v[98:99] op_sel_hi:[1,0,1]
	v_pk_fma_f32 v[100:101], v[190:191], s[14:15], v[100:101] op_sel_hi:[1,0,1]
	v_cvt_pk_f32_fp8_e32 v[184:185], v26
	v_cvt_pk_f32_fp8_sdwa v[186:187], v26 src0_sel:WORD_1
	v_pk_fma_f32 v[102:103], v[184:185], s[14:15], v[102:103] op_sel_hi:[1,0,1]
	v_pk_fma_f32 v[104:105], v[186:187], s[14:15], v[104:105] op_sel_hi:[1,0,1]
	v_cvt_pk_f32_fp8_e32 v[188:189], v27
	v_cvt_pk_f32_fp8_sdwa v[190:191], v27 src0_sel:WORD_1
	v_pk_fma_f32 v[106:107], v[188:189], s[14:15], v[106:107] op_sel_hi:[1,0,1]
	v_pk_fma_f32 v[108:109], v[190:191], s[14:15], v[108:109] op_sel_hi:[1,0,1]
	v_readlane_b32 s14, v1, 56
	v_cvt_pk_f32_fp8_e32 v[184:185], v20
	v_cvt_pk_f32_fp8_sdwa v[186:187], v20 src0_sel:WORD_1
	v_pk_fma_f32 v[94:95], v[184:185], s[14:15], v[94:95] op_sel_hi:[1,0,1]
	v_pk_fma_f32 v[96:97], v[186:187], s[14:15], v[96:97] op_sel_hi:[1,0,1]
	v_cvt_pk_f32_fp8_e32 v[188:189], v21
	v_cvt_pk_f32_fp8_sdwa v[190:191], v21 src0_sel:WORD_1
	v_pk_fma_f32 v[98:99], v[188:189], s[14:15], v[98:99] op_sel_hi:[1,0,1]
	v_pk_fma_f32 v[100:101], v[190:191], s[14:15], v[100:101] op_sel_hi:[1,0,1]
	v_cvt_pk_f32_fp8_e32 v[184:185], v22
	v_cvt_pk_f32_fp8_sdwa v[186:187], v22 src0_sel:WORD_1
	v_pk_fma_f32 v[102:103], v[184:185], s[14:15], v[102:103] op_sel_hi:[1,0,1]
	v_pk_fma_f32 v[104:105], v[186:187], s[14:15], v[104:105] op_sel_hi:[1,0,1]
	v_cvt_pk_f32_fp8_e32 v[188:189], v23
	v_cvt_pk_f32_fp8_sdwa v[190:191], v23 src0_sel:WORD_1
	v_pk_fma_f32 v[106:107], v[188:189], s[14:15], v[106:107] op_sel_hi:[1,0,1]
	v_pk_fma_f32 v[108:109], v[190:191], s[14:15], v[108:109] op_sel_hi:[1,0,1]
	s_branch .Lp6c1_axdone
.Lp6c1_t3:
	v_readlane_b32 s14, v1, 0
	v_cvt_pk_f32_fp8_e32 v[184:185], v72
	v_cvt_pk_f32_fp8_sdwa v[186:187], v72 src0_sel:WORD_1
	v_pk_fma_f32 v[78:79], v[184:185], s[14:15], v[78:79] op_sel_hi:[1,0,1]
	v_pk_fma_f32 v[80:81], v[186:187], s[14:15], v[80:81] op_sel_hi:[1,0,1]
	v_cvt_pk_f32_fp8_e32 v[188:189], v73
	v_cvt_pk_f32_fp8_sdwa v[190:191], v73 src0_sel:WORD_1
	v_pk_fma_f32 v[82:83], v[188:189], s[14:15], v[82:83] op_sel_hi:[1,0,1]
	v_pk_fma_f32 v[86:87], v[190:191], s[14:15], v[86:87] op_sel_hi:[1,0,1]
	v_cvt_pk_f32_fp8_e32 v[184:185], v74
	v_cvt_pk_f32_fp8_sdwa v[186:187], v74 src0_sel:WORD_1
	v_pk_fma_f32 v[88:89], v[184:185], s[14:15], v[88:89] op_sel_hi:[1,0,1]
	v_pk_fma_f32 v[90:91], v[186:187], s[14:15], v[90:91] op_sel_hi:[1,0,1]
	v_cvt_pk_f32_fp8_e32 v[188:189], v75
	v_cvt_pk_f32_fp8_sdwa v[190:191], v75 src0_sel:WORD_1
	v_pk_fma_f32 v[92:93], v[188:189], s[14:15], v[92:93] op_sel_hi:[1,0,1]
	v_pk_fma_f32 v[84:85], v[190:191], s[14:15], v[84:85] op_sel_hi:[1,0,1]
	v_readlane_b32 s14, v1, 8
	v_cvt_pk_f32_fp8_e32 v[184:185], v52
	v_cvt_pk_f32_fp8_sdwa v[186:187], v52 src0_sel:WORD_1
	v_pk_fma_f32 v[78:79], v[184:185], s[14:15], v[78:79] op_sel_hi:[1,0,1]
	v_pk_fma_f32 v[80:81], v[186:187], s[14:15], v[80:81] op_sel_hi:[1,0,1]
	v_cvt_pk_f32_fp8_e32 v[188:189], v53
	v_cvt_pk_f32_fp8_sdwa v[190:191], v53 src0_sel:WORD_1
	v_pk_fma_f32 v[82:83], v[188:189], s[14:15], v[82:83] op_sel_hi:[1,0,1]
	v_pk_fma_f32 v[86:87], v[190:191], s[14:15], v[86:87] op_sel_hi:[1,0,1]
	v_cvt_pk_f32_fp8_e32 v[184:185], v54
	v_cvt_pk_f32_fp8_sdwa v[186:187], v54 src0_sel:WORD_1
	v_pk_fma_f32 v[88:89], v[184:185], s[14:15], v[88:89] op_sel_hi:[1,0,1]
	v_pk_fma_f32 v[90:91], v[186:187], s[14:15], v[90:91] op_sel_hi:[1,0,1]
	v_cvt_pk_f32_fp8_e32 v[188:189], v55
	v_cvt_pk_f32_fp8_sdwa v[190:191], v55 src0_sel:WORD_1
	v_pk_fma_f32 v[92:93], v[188:189], s[14:15], v[92:93] op_sel_hi:[1,0,1]
	v_pk_fma_f32 v[84:85], v[190:191], s[14:15], v[84:85] op_sel_hi:[1,0,1]
	s_cmp_le_u32 s36, 2
	s_cbranch_scc1 .Lp6c1_axdone
	v_readlane_b32 s14, v1, 16
	v_cvt_pk_f32_fp8_e32 v[184:185], v44
	v_cvt_pk_f32_fp8_sdwa v[186:187], v44 src0_sel:WORD_1
	v_pk_fma_f32 v[78:79], v[184:185], s[14:15], v[78:79] op_sel_hi:[1,0,1]
	v_pk_fma_f32 v[80:81], v[186:187], s[14:15], v[80:81] op_sel_hi:[1,0,1]
	v_cvt_pk_f32_fp8_e32 v[188:189], v45
	v_cvt_pk_f32_fp8_sdwa v[190:191], v45 src0_sel:WORD_1
	v_pk_fma_f32 v[82:83], v[188:189], s[14:15], v[82:83] op_sel_hi:[1,0,1]
	v_pk_fma_f32 v[86:87], v[190:191], s[14:15], v[86:87] op_sel_hi:[1,0,1]
	v_cvt_pk_f32_fp8_e32 v[184:185], v46
	v_cvt_pk_f32_fp8_sdwa v[186:187], v46 src0_sel:WORD_1
	v_pk_fma_f32 v[88:89], v[184:185], s[14:15], v[88:89] op_sel_hi:[1,0,1]
	v_pk_fma_f32 v[90:91], v[186:187], s[14:15], v[90:91] op_sel_hi:[1,0,1]
	v_cvt_pk_f32_fp8_e32 v[188:189], v47
	v_cvt_pk_f32_fp8_sdwa v[190:191], v47 src0_sel:WORD_1
	v_pk_fma_f32 v[92:93], v[188:189], s[14:15], v[92:93] op_sel_hi:[1,0,1]
	v_pk_fma_f32 v[84:85], v[190:191], s[14:15], v[84:85] op_sel_hi:[1,0,1]
	v_readlane_b32 s14, v1, 24
	v_cvt_pk_f32_fp8_e32 v[184:185], v40
	v_cvt_pk_f32_fp8_sdwa v[186:187], v40 src0_sel:WORD_1
	v_pk_fma_f32 v[78:79], v[184:185], s[14:15], v[78:79] op_sel_hi:[1,0,1]
	v_pk_fma_f32 v[80:81], v[186:187], s[14:15], v[80:81] op_sel_hi:[1,0,1]
	v_cvt_pk_f32_fp8_e32 v[188:189], v41
	v_cvt_pk_f32_fp8_sdwa v[190:191], v41 src0_sel:WORD_1
	v_pk_fma_f32 v[82:83], v[188:189], s[14:15], v[82:83] op_sel_hi:[1,0,1]
	v_pk_fma_f32 v[86:87], v[190:191], s[14:15], v[86:87] op_sel_hi:[1,0,1]
	v_cvt_pk_f32_fp8_e32 v[184:185], v42
	v_cvt_pk_f32_fp8_sdwa v[186:187], v42 src0_sel:WORD_1
	v_pk_fma_f32 v[88:89], v[184:185], s[14:15], v[88:89] op_sel_hi:[1,0,1]
	v_pk_fma_f32 v[90:91], v[186:187], s[14:15], v[90:91] op_sel_hi:[1,0,1]
	v_cvt_pk_f32_fp8_e32 v[188:189], v43
	v_cvt_pk_f32_fp8_sdwa v[190:191], v43 src0_sel:WORD_1
	v_pk_fma_f32 v[92:93], v[188:189], s[14:15], v[92:93] op_sel_hi:[1,0,1]
	v_pk_fma_f32 v[84:85], v[190:191], s[14:15], v[84:85] op_sel_hi:[1,0,1]
	s_cmp_le_u32 s36, 4
	s_cbranch_scc1 .Lp6c1_axdone
	v_readlane_b32 s14, v1, 32
	v_cvt_pk_f32_fp8_e32 v[184:185], v36
	v_cvt_pk_f32_fp8_sdwa v[186:187], v36 src0_sel:WORD_1
	v_pk_fma_f32 v[78:79], v[184:185], s[14:15], v[78:79] op_sel_hi:[1,0,1]
	v_pk_fma_f32 v[80:81], v[186:187], s[14:15], v[80:81] op_sel_hi:[1,0,1]
	v_cvt_pk_f32_fp8_e32 v[188:189], v37
	v_cvt_pk_f32_fp8_sdwa v[190:191], v37 src0_sel:WORD_1
	v_pk_fma_f32 v[82:83], v[188:189], s[14:15], v[82:83] op_sel_hi:[1,0,1]
	v_pk_fma_f32 v[86:87], v[190:191], s[14:15], v[86:87] op_sel_hi:[1,0,1]
	v_cvt_pk_f32_fp8_e32 v[184:185], v38
	v_cvt_pk_f32_fp8_sdwa v[186:187], v38 src0_sel:WORD_1
	v_pk_fma_f32 v[88:89], v[184:185], s[14:15], v[88:89] op_sel_hi:[1,0,1]
	v_pk_fma_f32 v[90:91], v[186:187], s[14:15], v[90:91] op_sel_hi:[1,0,1]
	v_cvt_pk_f32_fp8_e32 v[188:189], v39
	v_cvt_pk_f32_fp8_sdwa v[190:191], v39 src0_sel:WORD_1
	v_pk_fma_f32 v[92:93], v[188:189], s[14:15], v[92:93] op_sel_hi:[1,0,1]
	v_pk_fma_f32 v[84:85], v[190:191], s[14:15], v[84:85] op_sel_hi:[1,0,1]
	v_readlane_b32 s14, v1, 40
	v_cvt_pk_f32_fp8_e32 v[184:185], v28
	v_cvt_pk_f32_fp8_sdwa v[186:187], v28 src0_sel:WORD_1
	v_pk_fma_f32 v[78:79], v[184:185], s[14:15], v[78:79] op_sel_hi:[1,0,1]
	v_pk_fma_f32 v[80:81], v[186:187], s[14:15], v[80:81] op_sel_hi:[1,0,1]
	v_cvt_pk_f32_fp8_e32 v[188:189], v29
	v_cvt_pk_f32_fp8_sdwa v[190:191], v29 src0_sel:WORD_1
	v_pk_fma_f32 v[82:83], v[188:189], s[14:15], v[82:83] op_sel_hi:[1,0,1]
	v_pk_fma_f32 v[86:87], v[190:191], s[14:15], v[86:87] op_sel_hi:[1,0,1]
	v_cvt_pk_f32_fp8_e32 v[184:185], v30
	v_cvt_pk_f32_fp8_sdwa v[186:187], v30 src0_sel:WORD_1
	v_pk_fma_f32 v[88:89], v[184:185], s[14:15], v[88:89] op_sel_hi:[1,0,1]
	v_pk_fma_f32 v[90:91], v[186:187], s[14:15], v[90:91] op_sel_hi:[1,0,1]
	v_cvt_pk_f32_fp8_e32 v[188:189], v31
	v_cvt_pk_f32_fp8_sdwa v[190:191], v31 src0_sel:WORD_1
	v_pk_fma_f32 v[92:93], v[188:189], s[14:15], v[92:93] op_sel_hi:[1,0,1]
	v_pk_fma_f32 v[84:85], v[190:191], s[14:15], v[84:85] op_sel_hi:[1,0,1]
	s_cmp_le_u32 s36, 6
	s_cbranch_scc1 .Lp6c1_axdone
	v_readlane_b32 s14, v1, 48
	v_cvt_pk_f32_fp8_e32 v[184:185], v24
	v_cvt_pk_f32_fp8_sdwa v[186:187], v24 src0_sel:WORD_1
	v_pk_fma_f32 v[78:79], v[184:185], s[14:15], v[78:79] op_sel_hi:[1,0,1]
	v_pk_fma_f32 v[80:81], v[186:187], s[14:15], v[80:81] op_sel_hi:[1,0,1]
	v_cvt_pk_f32_fp8_e32 v[188:189], v25
	v_cvt_pk_f32_fp8_sdwa v[190:191], v25 src0_sel:WORD_1
	v_pk_fma_f32 v[82:83], v[188:189], s[14:15], v[82:83] op_sel_hi:[1,0,1]
	v_pk_fma_f32 v[86:87], v[190:191], s[14:15], v[86:87] op_sel_hi:[1,0,1]
	v_cvt_pk_f32_fp8_e32 v[184:185], v26
	v_cvt_pk_f32_fp8_sdwa v[186:187], v26 src0_sel:WORD_1
	v_pk_fma_f32 v[88:89], v[184:185], s[14:15], v[88:89] op_sel_hi:[1,0,1]
	v_pk_fma_f32 v[90:91], v[186:187], s[14:15], v[90:91] op_sel_hi:[1,0,1]
	v_cvt_pk_f32_fp8_e32 v[188:189], v27
	v_cvt_pk_f32_fp8_sdwa v[190:191], v27 src0_sel:WORD_1
	v_pk_fma_f32 v[92:93], v[188:189], s[14:15], v[92:93] op_sel_hi:[1,0,1]
	v_pk_fma_f32 v[84:85], v[190:191], s[14:15], v[84:85] op_sel_hi:[1,0,1]
	v_readlane_b32 s14, v1, 56
	v_cvt_pk_f32_fp8_e32 v[184:185], v20
	v_cvt_pk_f32_fp8_sdwa v[186:187], v20 src0_sel:WORD_1
	v_pk_fma_f32 v[78:79], v[184:185], s[14:15], v[78:79] op_sel_hi:[1,0,1]
	v_pk_fma_f32 v[80:81], v[186:187], s[14:15], v[80:81] op_sel_hi:[1,0,1]
	v_cvt_pk_f32_fp8_e32 v[188:189], v21
	v_cvt_pk_f32_fp8_sdwa v[190:191], v21 src0_sel:WORD_1
	v_pk_fma_f32 v[82:83], v[188:189], s[14:15], v[82:83] op_sel_hi:[1,0,1]
	v_pk_fma_f32 v[86:87], v[190:191], s[14:15], v[86:87] op_sel_hi:[1,0,1]
	v_cvt_pk_f32_fp8_e32 v[184:185], v22
	v_cvt_pk_f32_fp8_sdwa v[186:187], v22 src0_sel:WORD_1
	v_pk_fma_f32 v[88:89], v[184:185], s[14:15], v[88:89] op_sel_hi:[1,0,1]
	v_pk_fma_f32 v[90:91], v[186:187], s[14:15], v[90:91] op_sel_hi:[1,0,1]
	v_cvt_pk_f32_fp8_e32 v[188:189], v23
	v_cvt_pk_f32_fp8_sdwa v[190:191], v23 src0_sel:WORD_1
	v_pk_fma_f32 v[92:93], v[188:189], s[14:15], v[92:93] op_sel_hi:[1,0,1]
	v_pk_fma_f32 v[84:85], v[190:191], s[14:15], v[84:85] op_sel_hi:[1,0,1]
	s_branch .Lp6c1_axdone
.Lp6c1_t4:
	v_readlane_b32 s14, v1, 0
	v_cvt_pk_f32_fp8_e32 v[184:185], v72
	v_cvt_pk_f32_fp8_sdwa v[186:187], v72 src0_sel:WORD_1
	v_pk_fma_f32 v[144:145], v[184:185], s[14:15], v[144:145] op_sel_hi:[1,0,1]
	v_pk_fma_f32 v[146:147], v[186:187], s[14:15], v[146:147] op_sel_hi:[1,0,1]
	v_cvt_pk_f32_fp8_e32 v[188:189], v73
	v_cvt_pk_f32_fp8_sdwa v[190:191], v73 src0_sel:WORD_1
	v_pk_fma_f32 v[148:149], v[188:189], s[14:15], v[148:149] op_sel_hi:[1,0,1]
	v_pk_fma_f32 v[150:151], v[190:191], s[14:15], v[150:151] op_sel_hi:[1,0,1]
	v_cvt_pk_f32_fp8_e32 v[184:185], v74
	v_cvt_pk_f32_fp8_sdwa v[186:187], v74 src0_sel:WORD_1
	v_pk_fma_f32 v[152:153], v[184:185], s[14:15], v[152:153] op_sel_hi:[1,0,1]
	v_pk_fma_f32 v[154:155], v[186:187], s[14:15], v[154:155] op_sel_hi:[1,0,1]
	v_cvt_pk_f32_fp8_e32 v[188:189], v75
	v_cvt_pk_f32_fp8_sdwa v[190:191], v75 src0_sel:WORD_1
	v_pk_fma_f32 v[156:157], v[188:189], s[14:15], v[156:157] op_sel_hi:[1,0,1]
	v_pk_fma_f32 v[158:159], v[190:191], s[14:15], v[158:159] op_sel_hi:[1,0,1]
	v_readlane_b32 s14, v1, 8
	v_cvt_pk_f32_fp8_e32 v[184:185], v52
	v_cvt_pk_f32_fp8_sdwa v[186:187], v52 src0_sel:WORD_1
	v_pk_fma_f32 v[144:145], v[184:185], s[14:15], v[144:145] op_sel_hi:[1,0,1]
	v_pk_fma_f32 v[146:147], v[186:187], s[14:15], v[146:147] op_sel_hi:[1,0,1]
	v_cvt_pk_f32_fp8_e32 v[188:189], v53
	v_cvt_pk_f32_fp8_sdwa v[190:191], v53 src0_sel:WORD_1
	v_pk_fma_f32 v[148:149], v[188:189], s[14:15], v[148:149] op_sel_hi:[1,0,1]
	v_pk_fma_f32 v[150:151], v[190:191], s[14:15], v[150:151] op_sel_hi:[1,0,1]
	v_cvt_pk_f32_fp8_e32 v[184:185], v54
	v_cvt_pk_f32_fp8_sdwa v[186:187], v54 src0_sel:WORD_1
	v_pk_fma_f32 v[152:153], v[184:185], s[14:15], v[152:153] op_sel_hi:[1,0,1]
	v_pk_fma_f32 v[154:155], v[186:187], s[14:15], v[154:155] op_sel_hi:[1,0,1]
	v_cvt_pk_f32_fp8_e32 v[188:189], v55
	v_cvt_pk_f32_fp8_sdwa v[190:191], v55 src0_sel:WORD_1
	v_pk_fma_f32 v[156:157], v[188:189], s[14:15], v[156:157] op_sel_hi:[1,0,1]
	v_pk_fma_f32 v[158:159], v[190:191], s[14:15], v[158:159] op_sel_hi:[1,0,1]
	s_cmp_le_u32 s36, 2
	s_cbranch_scc1 .Lp6c1_axdone
	v_readlane_b32 s14, v1, 16
	v_cvt_pk_f32_fp8_e32 v[184:185], v44
	v_cvt_pk_f32_fp8_sdwa v[186:187], v44 src0_sel:WORD_1
	v_pk_fma_f32 v[144:145], v[184:185], s[14:15], v[144:145] op_sel_hi:[1,0,1]
	v_pk_fma_f32 v[146:147], v[186:187], s[14:15], v[146:147] op_sel_hi:[1,0,1]
	v_cvt_pk_f32_fp8_e32 v[188:189], v45
	v_cvt_pk_f32_fp8_sdwa v[190:191], v45 src0_sel:WORD_1
	v_pk_fma_f32 v[148:149], v[188:189], s[14:15], v[148:149] op_sel_hi:[1,0,1]
	v_pk_fma_f32 v[150:151], v[190:191], s[14:15], v[150:151] op_sel_hi:[1,0,1]
	v_cvt_pk_f32_fp8_e32 v[184:185], v46
	v_cvt_pk_f32_fp8_sdwa v[186:187], v46 src0_sel:WORD_1
	v_pk_fma_f32 v[152:153], v[184:185], s[14:15], v[152:153] op_sel_hi:[1,0,1]
	v_pk_fma_f32 v[154:155], v[186:187], s[14:15], v[154:155] op_sel_hi:[1,0,1]
	v_cvt_pk_f32_fp8_e32 v[188:189], v47
	v_cvt_pk_f32_fp8_sdwa v[190:191], v47 src0_sel:WORD_1
	v_pk_fma_f32 v[156:157], v[188:189], s[14:15], v[156:157] op_sel_hi:[1,0,1]
	v_pk_fma_f32 v[158:159], v[190:191], s[14:15], v[158:159] op_sel_hi:[1,0,1]
	v_readlane_b32 s14, v1, 24
	v_cvt_pk_f32_fp8_e32 v[184:185], v40
	v_cvt_pk_f32_fp8_sdwa v[186:187], v40 src0_sel:WORD_1
	v_pk_fma_f32 v[144:145], v[184:185], s[14:15], v[144:145] op_sel_hi:[1,0,1]
	v_pk_fma_f32 v[146:147], v[186:187], s[14:15], v[146:147] op_sel_hi:[1,0,1]
	v_cvt_pk_f32_fp8_e32 v[188:189], v41
	v_cvt_pk_f32_fp8_sdwa v[190:191], v41 src0_sel:WORD_1
	v_pk_fma_f32 v[148:149], v[188:189], s[14:15], v[148:149] op_sel_hi:[1,0,1]
	v_pk_fma_f32 v[150:151], v[190:191], s[14:15], v[150:151] op_sel_hi:[1,0,1]
	v_cvt_pk_f32_fp8_e32 v[184:185], v42
	v_cvt_pk_f32_fp8_sdwa v[186:187], v42 src0_sel:WORD_1
	v_pk_fma_f32 v[152:153], v[184:185], s[14:15], v[152:153] op_sel_hi:[1,0,1]
	v_pk_fma_f32 v[154:155], v[186:187], s[14:15], v[154:155] op_sel_hi:[1,0,1]
	v_cvt_pk_f32_fp8_e32 v[188:189], v43
	v_cvt_pk_f32_fp8_sdwa v[190:191], v43 src0_sel:WORD_1
	v_pk_fma_f32 v[156:157], v[188:189], s[14:15], v[156:157] op_sel_hi:[1,0,1]
	v_pk_fma_f32 v[158:159], v[190:191], s[14:15], v[158:159] op_sel_hi:[1,0,1]
	s_cmp_le_u32 s36, 4
	s_cbranch_scc1 .Lp6c1_axdone
	v_readlane_b32 s14, v1, 32
	v_cvt_pk_f32_fp8_e32 v[184:185], v36
	v_cvt_pk_f32_fp8_sdwa v[186:187], v36 src0_sel:WORD_1
	v_pk_fma_f32 v[144:145], v[184:185], s[14:15], v[144:145] op_sel_hi:[1,0,1]
	v_pk_fma_f32 v[146:147], v[186:187], s[14:15], v[146:147] op_sel_hi:[1,0,1]
	v_cvt_pk_f32_fp8_e32 v[188:189], v37
	v_cvt_pk_f32_fp8_sdwa v[190:191], v37 src0_sel:WORD_1
	v_pk_fma_f32 v[148:149], v[188:189], s[14:15], v[148:149] op_sel_hi:[1,0,1]
	v_pk_fma_f32 v[150:151], v[190:191], s[14:15], v[150:151] op_sel_hi:[1,0,1]
	v_cvt_pk_f32_fp8_e32 v[184:185], v38
	v_cvt_pk_f32_fp8_sdwa v[186:187], v38 src0_sel:WORD_1
	v_pk_fma_f32 v[152:153], v[184:185], s[14:15], v[152:153] op_sel_hi:[1,0,1]
	v_pk_fma_f32 v[154:155], v[186:187], s[14:15], v[154:155] op_sel_hi:[1,0,1]
	v_cvt_pk_f32_fp8_e32 v[188:189], v39
	v_cvt_pk_f32_fp8_sdwa v[190:191], v39 src0_sel:WORD_1
	v_pk_fma_f32 v[156:157], v[188:189], s[14:15], v[156:157] op_sel_hi:[1,0,1]
	v_pk_fma_f32 v[158:159], v[190:191], s[14:15], v[158:159] op_sel_hi:[1,0,1]
	v_readlane_b32 s14, v1, 40
	v_cvt_pk_f32_fp8_e32 v[184:185], v28
	v_cvt_pk_f32_fp8_sdwa v[186:187], v28 src0_sel:WORD_1
	v_pk_fma_f32 v[144:145], v[184:185], s[14:15], v[144:145] op_sel_hi:[1,0,1]
	v_pk_fma_f32 v[146:147], v[186:187], s[14:15], v[146:147] op_sel_hi:[1,0,1]
	v_cvt_pk_f32_fp8_e32 v[188:189], v29
	v_cvt_pk_f32_fp8_sdwa v[190:191], v29 src0_sel:WORD_1
	v_pk_fma_f32 v[148:149], v[188:189], s[14:15], v[148:149] op_sel_hi:[1,0,1]
	v_pk_fma_f32 v[150:151], v[190:191], s[14:15], v[150:151] op_sel_hi:[1,0,1]
	v_cvt_pk_f32_fp8_e32 v[184:185], v30
	v_cvt_pk_f32_fp8_sdwa v[186:187], v30 src0_sel:WORD_1
	v_pk_fma_f32 v[152:153], v[184:185], s[14:15], v[152:153] op_sel_hi:[1,0,1]
	v_pk_fma_f32 v[154:155], v[186:187], s[14:15], v[154:155] op_sel_hi:[1,0,1]
	v_cvt_pk_f32_fp8_e32 v[188:189], v31
	v_cvt_pk_f32_fp8_sdwa v[190:191], v31 src0_sel:WORD_1
	v_pk_fma_f32 v[156:157], v[188:189], s[14:15], v[156:157] op_sel_hi:[1,0,1]
	v_pk_fma_f32 v[158:159], v[190:191], s[14:15], v[158:159] op_sel_hi:[1,0,1]
	s_cmp_le_u32 s36, 6
	s_cbranch_scc1 .Lp6c1_axdone
	v_readlane_b32 s14, v1, 48
	v_cvt_pk_f32_fp8_e32 v[184:185], v24
	v_cvt_pk_f32_fp8_sdwa v[186:187], v24 src0_sel:WORD_1
	v_pk_fma_f32 v[144:145], v[184:185], s[14:15], v[144:145] op_sel_hi:[1,0,1]
	v_pk_fma_f32 v[146:147], v[186:187], s[14:15], v[146:147] op_sel_hi:[1,0,1]
	v_cvt_pk_f32_fp8_e32 v[188:189], v25
	v_cvt_pk_f32_fp8_sdwa v[190:191], v25 src0_sel:WORD_1
	v_pk_fma_f32 v[148:149], v[188:189], s[14:15], v[148:149] op_sel_hi:[1,0,1]
	v_pk_fma_f32 v[150:151], v[190:191], s[14:15], v[150:151] op_sel_hi:[1,0,1]
	v_cvt_pk_f32_fp8_e32 v[184:185], v26
	v_cvt_pk_f32_fp8_sdwa v[186:187], v26 src0_sel:WORD_1
	v_pk_fma_f32 v[152:153], v[184:185], s[14:15], v[152:153] op_sel_hi:[1,0,1]
	v_pk_fma_f32 v[154:155], v[186:187], s[14:15], v[154:155] op_sel_hi:[1,0,1]
	v_cvt_pk_f32_fp8_e32 v[188:189], v27
	v_cvt_pk_f32_fp8_sdwa v[190:191], v27 src0_sel:WORD_1
	v_pk_fma_f32 v[156:157], v[188:189], s[14:15], v[156:157] op_sel_hi:[1,0,1]
	v_pk_fma_f32 v[158:159], v[190:191], s[14:15], v[158:159] op_sel_hi:[1,0,1]
	v_readlane_b32 s14, v1, 56
	v_cvt_pk_f32_fp8_e32 v[184:185], v20
	v_cvt_pk_f32_fp8_sdwa v[186:187], v20 src0_sel:WORD_1
	v_pk_fma_f32 v[144:145], v[184:185], s[14:15], v[144:145] op_sel_hi:[1,0,1]
	v_pk_fma_f32 v[146:147], v[186:187], s[14:15], v[146:147] op_sel_hi:[1,0,1]
	v_cvt_pk_f32_fp8_e32 v[188:189], v21
	v_cvt_pk_f32_fp8_sdwa v[190:191], v21 src0_sel:WORD_1
	v_pk_fma_f32 v[148:149], v[188:189], s[14:15], v[148:149] op_sel_hi:[1,0,1]
	v_pk_fma_f32 v[150:151], v[190:191], s[14:15], v[150:151] op_sel_hi:[1,0,1]
	v_cvt_pk_f32_fp8_e32 v[184:185], v22
	v_cvt_pk_f32_fp8_sdwa v[186:187], v22 src0_sel:WORD_1
	v_pk_fma_f32 v[152:153], v[184:185], s[14:15], v[152:153] op_sel_hi:[1,0,1]
	v_pk_fma_f32 v[154:155], v[186:187], s[14:15], v[154:155] op_sel_hi:[1,0,1]
	v_cvt_pk_f32_fp8_e32 v[188:189], v23
	v_cvt_pk_f32_fp8_sdwa v[190:191], v23 src0_sel:WORD_1
	v_pk_fma_f32 v[156:157], v[188:189], s[14:15], v[156:157] op_sel_hi:[1,0,1]
	v_pk_fma_f32 v[158:159], v[190:191], s[14:15], v[158:159] op_sel_hi:[1,0,1]
	s_branch .Lp6c1_axdone
.Lp6c1_t5:
	v_readlane_b32 s14, v1, 0
	v_cvt_pk_f32_fp8_e32 v[184:185], v72
	v_cvt_pk_f32_fp8_sdwa v[186:187], v72 src0_sel:WORD_1
	v_pk_fma_f32 v[160:161], v[184:185], s[14:15], v[160:161] op_sel_hi:[1,0,1]
	v_pk_fma_f32 v[162:163], v[186:187], s[14:15], v[162:163] op_sel_hi:[1,0,1]
	v_cvt_pk_f32_fp8_e32 v[188:189], v73
	v_cvt_pk_f32_fp8_sdwa v[190:191], v73 src0_sel:WORD_1
	v_pk_fma_f32 v[164:165], v[188:189], s[14:15], v[164:165] op_sel_hi:[1,0,1]
	v_pk_fma_f32 v[166:167], v[190:191], s[14:15], v[166:167] op_sel_hi:[1,0,1]
	v_cvt_pk_f32_fp8_e32 v[184:185], v74
	v_cvt_pk_f32_fp8_sdwa v[186:187], v74 src0_sel:WORD_1
	v_pk_fma_f32 v[168:169], v[184:185], s[14:15], v[168:169] op_sel_hi:[1,0,1]
	v_pk_fma_f32 v[170:171], v[186:187], s[14:15], v[170:171] op_sel_hi:[1,0,1]
	v_cvt_pk_f32_fp8_e32 v[188:189], v75
	v_cvt_pk_f32_fp8_sdwa v[190:191], v75 src0_sel:WORD_1
	v_pk_fma_f32 v[172:173], v[188:189], s[14:15], v[172:173] op_sel_hi:[1,0,1]
	v_pk_fma_f32 v[174:175], v[190:191], s[14:15], v[174:175] op_sel_hi:[1,0,1]
	v_readlane_b32 s14, v1, 8
	v_cvt_pk_f32_fp8_e32 v[184:185], v52
	v_cvt_pk_f32_fp8_sdwa v[186:187], v52 src0_sel:WORD_1
	v_pk_fma_f32 v[160:161], v[184:185], s[14:15], v[160:161] op_sel_hi:[1,0,1]
	v_pk_fma_f32 v[162:163], v[186:187], s[14:15], v[162:163] op_sel_hi:[1,0,1]
	v_cvt_pk_f32_fp8_e32 v[188:189], v53
	v_cvt_pk_f32_fp8_sdwa v[190:191], v53 src0_sel:WORD_1
	v_pk_fma_f32 v[164:165], v[188:189], s[14:15], v[164:165] op_sel_hi:[1,0,1]
	v_pk_fma_f32 v[166:167], v[190:191], s[14:15], v[166:167] op_sel_hi:[1,0,1]
	v_cvt_pk_f32_fp8_e32 v[184:185], v54
	v_cvt_pk_f32_fp8_sdwa v[186:187], v54 src0_sel:WORD_1
	v_pk_fma_f32 v[168:169], v[184:185], s[14:15], v[168:169] op_sel_hi:[1,0,1]
	v_pk_fma_f32 v[170:171], v[186:187], s[14:15], v[170:171] op_sel_hi:[1,0,1]
	v_cvt_pk_f32_fp8_e32 v[188:189], v55
	v_cvt_pk_f32_fp8_sdwa v[190:191], v55 src0_sel:WORD_1
	v_pk_fma_f32 v[172:173], v[188:189], s[14:15], v[172:173] op_sel_hi:[1,0,1]
	v_pk_fma_f32 v[174:175], v[190:191], s[14:15], v[174:175] op_sel_hi:[1,0,1]
	s_cmp_le_u32 s36, 2
	s_cbranch_scc1 .Lp6c1_axdone
	v_readlane_b32 s14, v1, 16
	v_cvt_pk_f32_fp8_e32 v[184:185], v44
	v_cvt_pk_f32_fp8_sdwa v[186:187], v44 src0_sel:WORD_1
	v_pk_fma_f32 v[160:161], v[184:185], s[14:15], v[160:161] op_sel_hi:[1,0,1]
	v_pk_fma_f32 v[162:163], v[186:187], s[14:15], v[162:163] op_sel_hi:[1,0,1]
	v_cvt_pk_f32_fp8_e32 v[188:189], v45
	v_cvt_pk_f32_fp8_sdwa v[190:191], v45 src0_sel:WORD_1
	v_pk_fma_f32 v[164:165], v[188:189], s[14:15], v[164:165] op_sel_hi:[1,0,1]
	v_pk_fma_f32 v[166:167], v[190:191], s[14:15], v[166:167] op_sel_hi:[1,0,1]
	v_cvt_pk_f32_fp8_e32 v[184:185], v46
	v_cvt_pk_f32_fp8_sdwa v[186:187], v46 src0_sel:WORD_1
	v_pk_fma_f32 v[168:169], v[184:185], s[14:15], v[168:169] op_sel_hi:[1,0,1]
	v_pk_fma_f32 v[170:171], v[186:187], s[14:15], v[170:171] op_sel_hi:[1,0,1]
	v_cvt_pk_f32_fp8_e32 v[188:189], v47
	v_cvt_pk_f32_fp8_sdwa v[190:191], v47 src0_sel:WORD_1
	v_pk_fma_f32 v[172:173], v[188:189], s[14:15], v[172:173] op_sel_hi:[1,0,1]
	v_pk_fma_f32 v[174:175], v[190:191], s[14:15], v[174:175] op_sel_hi:[1,0,1]
	v_readlane_b32 s14, v1, 24
	v_cvt_pk_f32_fp8_e32 v[184:185], v40
	v_cvt_pk_f32_fp8_sdwa v[186:187], v40 src0_sel:WORD_1
	v_pk_fma_f32 v[160:161], v[184:185], s[14:15], v[160:161] op_sel_hi:[1,0,1]
	v_pk_fma_f32 v[162:163], v[186:187], s[14:15], v[162:163] op_sel_hi:[1,0,1]
	v_cvt_pk_f32_fp8_e32 v[188:189], v41
	v_cvt_pk_f32_fp8_sdwa v[190:191], v41 src0_sel:WORD_1
	v_pk_fma_f32 v[164:165], v[188:189], s[14:15], v[164:165] op_sel_hi:[1,0,1]
	v_pk_fma_f32 v[166:167], v[190:191], s[14:15], v[166:167] op_sel_hi:[1,0,1]
	v_cvt_pk_f32_fp8_e32 v[184:185], v42
	v_cvt_pk_f32_fp8_sdwa v[186:187], v42 src0_sel:WORD_1
	v_pk_fma_f32 v[168:169], v[184:185], s[14:15], v[168:169] op_sel_hi:[1,0,1]
	v_pk_fma_f32 v[170:171], v[186:187], s[14:15], v[170:171] op_sel_hi:[1,0,1]
	v_cvt_pk_f32_fp8_e32 v[188:189], v43
	v_cvt_pk_f32_fp8_sdwa v[190:191], v43 src0_sel:WORD_1
	v_pk_fma_f32 v[172:173], v[188:189], s[14:15], v[172:173] op_sel_hi:[1,0,1]
	v_pk_fma_f32 v[174:175], v[190:191], s[14:15], v[174:175] op_sel_hi:[1,0,1]
	s_cmp_le_u32 s36, 4
	s_cbranch_scc1 .Lp6c1_axdone
	v_readlane_b32 s14, v1, 32
	v_cvt_pk_f32_fp8_e32 v[184:185], v36
	v_cvt_pk_f32_fp8_sdwa v[186:187], v36 src0_sel:WORD_1
	v_pk_fma_f32 v[160:161], v[184:185], s[14:15], v[160:161] op_sel_hi:[1,0,1]
	v_pk_fma_f32 v[162:163], v[186:187], s[14:15], v[162:163] op_sel_hi:[1,0,1]
	v_cvt_pk_f32_fp8_e32 v[188:189], v37
	v_cvt_pk_f32_fp8_sdwa v[190:191], v37 src0_sel:WORD_1
	v_pk_fma_f32 v[164:165], v[188:189], s[14:15], v[164:165] op_sel_hi:[1,0,1]
	v_pk_fma_f32 v[166:167], v[190:191], s[14:15], v[166:167] op_sel_hi:[1,0,1]
	v_cvt_pk_f32_fp8_e32 v[184:185], v38
	v_cvt_pk_f32_fp8_sdwa v[186:187], v38 src0_sel:WORD_1
	v_pk_fma_f32 v[168:169], v[184:185], s[14:15], v[168:169] op_sel_hi:[1,0,1]
	v_pk_fma_f32 v[170:171], v[186:187], s[14:15], v[170:171] op_sel_hi:[1,0,1]
	v_cvt_pk_f32_fp8_e32 v[188:189], v39
	v_cvt_pk_f32_fp8_sdwa v[190:191], v39 src0_sel:WORD_1
	v_pk_fma_f32 v[172:173], v[188:189], s[14:15], v[172:173] op_sel_hi:[1,0,1]
	v_pk_fma_f32 v[174:175], v[190:191], s[14:15], v[174:175] op_sel_hi:[1,0,1]
	v_readlane_b32 s14, v1, 40
	v_cvt_pk_f32_fp8_e32 v[184:185], v28
	v_cvt_pk_f32_fp8_sdwa v[186:187], v28 src0_sel:WORD_1
	v_pk_fma_f32 v[160:161], v[184:185], s[14:15], v[160:161] op_sel_hi:[1,0,1]
	v_pk_fma_f32 v[162:163], v[186:187], s[14:15], v[162:163] op_sel_hi:[1,0,1]
	v_cvt_pk_f32_fp8_e32 v[188:189], v29
	v_cvt_pk_f32_fp8_sdwa v[190:191], v29 src0_sel:WORD_1
	v_pk_fma_f32 v[164:165], v[188:189], s[14:15], v[164:165] op_sel_hi:[1,0,1]
	v_pk_fma_f32 v[166:167], v[190:191], s[14:15], v[166:167] op_sel_hi:[1,0,1]
	v_cvt_pk_f32_fp8_e32 v[184:185], v30
	v_cvt_pk_f32_fp8_sdwa v[186:187], v30 src0_sel:WORD_1
	v_pk_fma_f32 v[168:169], v[184:185], s[14:15], v[168:169] op_sel_hi:[1,0,1]
	v_pk_fma_f32 v[170:171], v[186:187], s[14:15], v[170:171] op_sel_hi:[1,0,1]
	v_cvt_pk_f32_fp8_e32 v[188:189], v31
	v_cvt_pk_f32_fp8_sdwa v[190:191], v31 src0_sel:WORD_1
	v_pk_fma_f32 v[172:173], v[188:189], s[14:15], v[172:173] op_sel_hi:[1,0,1]
	v_pk_fma_f32 v[174:175], v[190:191], s[14:15], v[174:175] op_sel_hi:[1,0,1]
	s_cmp_le_u32 s36, 6
	s_cbranch_scc1 .Lp6c1_axdone
	v_readlane_b32 s14, v1, 48
	v_cvt_pk_f32_fp8_e32 v[184:185], v24
	v_cvt_pk_f32_fp8_sdwa v[186:187], v24 src0_sel:WORD_1
	v_pk_fma_f32 v[160:161], v[184:185], s[14:15], v[160:161] op_sel_hi:[1,0,1]
	v_pk_fma_f32 v[162:163], v[186:187], s[14:15], v[162:163] op_sel_hi:[1,0,1]
	v_cvt_pk_f32_fp8_e32 v[188:189], v25
	v_cvt_pk_f32_fp8_sdwa v[190:191], v25 src0_sel:WORD_1
	v_pk_fma_f32 v[164:165], v[188:189], s[14:15], v[164:165] op_sel_hi:[1,0,1]
	v_pk_fma_f32 v[166:167], v[190:191], s[14:15], v[166:167] op_sel_hi:[1,0,1]
	v_cvt_pk_f32_fp8_e32 v[184:185], v26
	v_cvt_pk_f32_fp8_sdwa v[186:187], v26 src0_sel:WORD_1
	v_pk_fma_f32 v[168:169], v[184:185], s[14:15], v[168:169] op_sel_hi:[1,0,1]
	v_pk_fma_f32 v[170:171], v[186:187], s[14:15], v[170:171] op_sel_hi:[1,0,1]
	v_cvt_pk_f32_fp8_e32 v[188:189], v27
	v_cvt_pk_f32_fp8_sdwa v[190:191], v27 src0_sel:WORD_1
	v_pk_fma_f32 v[172:173], v[188:189], s[14:15], v[172:173] op_sel_hi:[1,0,1]
	v_pk_fma_f32 v[174:175], v[190:191], s[14:15], v[174:175] op_sel_hi:[1,0,1]
	v_readlane_b32 s14, v1, 56
	v_cvt_pk_f32_fp8_e32 v[184:185], v20
	v_cvt_pk_f32_fp8_sdwa v[186:187], v20 src0_sel:WORD_1
	v_pk_fma_f32 v[160:161], v[184:185], s[14:15], v[160:161] op_sel_hi:[1,0,1]
	v_pk_fma_f32 v[162:163], v[186:187], s[14:15], v[162:163] op_sel_hi:[1,0,1]
	v_cvt_pk_f32_fp8_e32 v[188:189], v21
	v_cvt_pk_f32_fp8_sdwa v[190:191], v21 src0_sel:WORD_1
	v_pk_fma_f32 v[164:165], v[188:189], s[14:15], v[164:165] op_sel_hi:[1,0,1]
	v_pk_fma_f32 v[166:167], v[190:191], s[14:15], v[166:167] op_sel_hi:[1,0,1]
	v_cvt_pk_f32_fp8_e32 v[184:185], v22
	v_cvt_pk_f32_fp8_sdwa v[186:187], v22 src0_sel:WORD_1
	v_pk_fma_f32 v[168:169], v[184:185], s[14:15], v[168:169] op_sel_hi:[1,0,1]
	v_pk_fma_f32 v[170:171], v[186:187], s[14:15], v[170:171] op_sel_hi:[1,0,1]
	v_cvt_pk_f32_fp8_e32 v[188:189], v23
	v_cvt_pk_f32_fp8_sdwa v[190:191], v23 src0_sel:WORD_1
	v_pk_fma_f32 v[172:173], v[188:189], s[14:15], v[172:173] op_sel_hi:[1,0,1]
	v_pk_fma_f32 v[174:175], v[190:191], s[14:15], v[174:175] op_sel_hi:[1,0,1]
	s_branch .Lp6c1_axdone
.Lp6c1_t6:
	v_readlane_b32 s14, v1, 0
	v_cvt_pk_f32_fp8_e32 v[184:185], v72
	v_cvt_pk_f32_fp8_sdwa v[186:187], v72 src0_sel:WORD_1
	v_pk_fma_f32 v[224:225], v[184:185], s[14:15], v[224:225] op_sel_hi:[1,0,1]
	v_pk_fma_f32 v[226:227], v[186:187], s[14:15], v[226:227] op_sel_hi:[1,0,1]
	v_cvt_pk_f32_fp8_e32 v[188:189], v73
	v_cvt_pk_f32_fp8_sdwa v[190:191], v73 src0_sel:WORD_1
	v_pk_fma_f32 v[228:229], v[188:189], s[14:15], v[228:229] op_sel_hi:[1,0,1]
	v_pk_fma_f32 v[230:231], v[190:191], s[14:15], v[230:231] op_sel_hi:[1,0,1]
	v_cvt_pk_f32_fp8_e32 v[184:185], v74
	v_cvt_pk_f32_fp8_sdwa v[186:187], v74 src0_sel:WORD_1
	v_pk_fma_f32 v[232:233], v[184:185], s[14:15], v[232:233] op_sel_hi:[1,0,1]
	v_pk_fma_f32 v[234:235], v[186:187], s[14:15], v[234:235] op_sel_hi:[1,0,1]
	v_cvt_pk_f32_fp8_e32 v[188:189], v75
	v_cvt_pk_f32_fp8_sdwa v[190:191], v75 src0_sel:WORD_1
	v_pk_fma_f32 v[236:237], v[188:189], s[14:15], v[236:237] op_sel_hi:[1,0,1]
	v_pk_fma_f32 v[238:239], v[190:191], s[14:15], v[238:239] op_sel_hi:[1,0,1]
	v_readlane_b32 s14, v1, 8
	v_cvt_pk_f32_fp8_e32 v[184:185], v52
	v_cvt_pk_f32_fp8_sdwa v[186:187], v52 src0_sel:WORD_1
	v_pk_fma_f32 v[224:225], v[184:185], s[14:15], v[224:225] op_sel_hi:[1,0,1]
	v_pk_fma_f32 v[226:227], v[186:187], s[14:15], v[226:227] op_sel_hi:[1,0,1]
	v_cvt_pk_f32_fp8_e32 v[188:189], v53
	v_cvt_pk_f32_fp8_sdwa v[190:191], v53 src0_sel:WORD_1
	v_pk_fma_f32 v[228:229], v[188:189], s[14:15], v[228:229] op_sel_hi:[1,0,1]
	v_pk_fma_f32 v[230:231], v[190:191], s[14:15], v[230:231] op_sel_hi:[1,0,1]
	v_cvt_pk_f32_fp8_e32 v[184:185], v54
	v_cvt_pk_f32_fp8_sdwa v[186:187], v54 src0_sel:WORD_1
	v_pk_fma_f32 v[232:233], v[184:185], s[14:15], v[232:233] op_sel_hi:[1,0,1]
	v_pk_fma_f32 v[234:235], v[186:187], s[14:15], v[234:235] op_sel_hi:[1,0,1]
	v_cvt_pk_f32_fp8_e32 v[188:189], v55
	v_cvt_pk_f32_fp8_sdwa v[190:191], v55 src0_sel:WORD_1
	v_pk_fma_f32 v[236:237], v[188:189], s[14:15], v[236:237] op_sel_hi:[1,0,1]
	v_pk_fma_f32 v[238:239], v[190:191], s[14:15], v[238:239] op_sel_hi:[1,0,1]
	s_cmp_le_u32 s36, 2
	s_cbranch_scc1 .Lp6c1_axdone
	v_readlane_b32 s14, v1, 16
	v_cvt_pk_f32_fp8_e32 v[184:185], v44
	v_cvt_pk_f32_fp8_sdwa v[186:187], v44 src0_sel:WORD_1
	v_pk_fma_f32 v[224:225], v[184:185], s[14:15], v[224:225] op_sel_hi:[1,0,1]
	v_pk_fma_f32 v[226:227], v[186:187], s[14:15], v[226:227] op_sel_hi:[1,0,1]
	v_cvt_pk_f32_fp8_e32 v[188:189], v45
	v_cvt_pk_f32_fp8_sdwa v[190:191], v45 src0_sel:WORD_1
	v_pk_fma_f32 v[228:229], v[188:189], s[14:15], v[228:229] op_sel_hi:[1,0,1]
	v_pk_fma_f32 v[230:231], v[190:191], s[14:15], v[230:231] op_sel_hi:[1,0,1]
	v_cvt_pk_f32_fp8_e32 v[184:185], v46
	v_cvt_pk_f32_fp8_sdwa v[186:187], v46 src0_sel:WORD_1
	v_pk_fma_f32 v[232:233], v[184:185], s[14:15], v[232:233] op_sel_hi:[1,0,1]
	v_pk_fma_f32 v[234:235], v[186:187], s[14:15], v[234:235] op_sel_hi:[1,0,1]
	v_cvt_pk_f32_fp8_e32 v[188:189], v47
	v_cvt_pk_f32_fp8_sdwa v[190:191], v47 src0_sel:WORD_1
	v_pk_fma_f32 v[236:237], v[188:189], s[14:15], v[236:237] op_sel_hi:[1,0,1]
	v_pk_fma_f32 v[238:239], v[190:191], s[14:15], v[238:239] op_sel_hi:[1,0,1]
	v_readlane_b32 s14, v1, 24
	v_cvt_pk_f32_fp8_e32 v[184:185], v40
	v_cvt_pk_f32_fp8_sdwa v[186:187], v40 src0_sel:WORD_1
	v_pk_fma_f32 v[224:225], v[184:185], s[14:15], v[224:225] op_sel_hi:[1,0,1]
	v_pk_fma_f32 v[226:227], v[186:187], s[14:15], v[226:227] op_sel_hi:[1,0,1]
	v_cvt_pk_f32_fp8_e32 v[188:189], v41
	v_cvt_pk_f32_fp8_sdwa v[190:191], v41 src0_sel:WORD_1
	v_pk_fma_f32 v[228:229], v[188:189], s[14:15], v[228:229] op_sel_hi:[1,0,1]
	v_pk_fma_f32 v[230:231], v[190:191], s[14:15], v[230:231] op_sel_hi:[1,0,1]
	v_cvt_pk_f32_fp8_e32 v[184:185], v42
	v_cvt_pk_f32_fp8_sdwa v[186:187], v42 src0_sel:WORD_1
	v_pk_fma_f32 v[232:233], v[184:185], s[14:15], v[232:233] op_sel_hi:[1,0,1]
	v_pk_fma_f32 v[234:235], v[186:187], s[14:15], v[234:235] op_sel_hi:[1,0,1]
	v_cvt_pk_f32_fp8_e32 v[188:189], v43
	v_cvt_pk_f32_fp8_sdwa v[190:191], v43 src0_sel:WORD_1
	v_pk_fma_f32 v[236:237], v[188:189], s[14:15], v[236:237] op_sel_hi:[1,0,1]
	v_pk_fma_f32 v[238:239], v[190:191], s[14:15], v[238:239] op_sel_hi:[1,0,1]
	s_cmp_le_u32 s36, 4
	s_cbranch_scc1 .Lp6c1_axdone
	v_readlane_b32 s14, v1, 32
	v_cvt_pk_f32_fp8_e32 v[184:185], v36
	v_cvt_pk_f32_fp8_sdwa v[186:187], v36 src0_sel:WORD_1
	v_pk_fma_f32 v[224:225], v[184:185], s[14:15], v[224:225] op_sel_hi:[1,0,1]
	v_pk_fma_f32 v[226:227], v[186:187], s[14:15], v[226:227] op_sel_hi:[1,0,1]
	v_cvt_pk_f32_fp8_e32 v[188:189], v37
	v_cvt_pk_f32_fp8_sdwa v[190:191], v37 src0_sel:WORD_1
	v_pk_fma_f32 v[228:229], v[188:189], s[14:15], v[228:229] op_sel_hi:[1,0,1]
	v_pk_fma_f32 v[230:231], v[190:191], s[14:15], v[230:231] op_sel_hi:[1,0,1]
	v_cvt_pk_f32_fp8_e32 v[184:185], v38
	v_cvt_pk_f32_fp8_sdwa v[186:187], v38 src0_sel:WORD_1
	v_pk_fma_f32 v[232:233], v[184:185], s[14:15], v[232:233] op_sel_hi:[1,0,1]
	v_pk_fma_f32 v[234:235], v[186:187], s[14:15], v[234:235] op_sel_hi:[1,0,1]
	v_cvt_pk_f32_fp8_e32 v[188:189], v39
	v_cvt_pk_f32_fp8_sdwa v[190:191], v39 src0_sel:WORD_1
	v_pk_fma_f32 v[236:237], v[188:189], s[14:15], v[236:237] op_sel_hi:[1,0,1]
	v_pk_fma_f32 v[238:239], v[190:191], s[14:15], v[238:239] op_sel_hi:[1,0,1]
	v_readlane_b32 s14, v1, 40
	v_cvt_pk_f32_fp8_e32 v[184:185], v28
	v_cvt_pk_f32_fp8_sdwa v[186:187], v28 src0_sel:WORD_1
	v_pk_fma_f32 v[224:225], v[184:185], s[14:15], v[224:225] op_sel_hi:[1,0,1]
	v_pk_fma_f32 v[226:227], v[186:187], s[14:15], v[226:227] op_sel_hi:[1,0,1]
	v_cvt_pk_f32_fp8_e32 v[188:189], v29
	v_cvt_pk_f32_fp8_sdwa v[190:191], v29 src0_sel:WORD_1
	v_pk_fma_f32 v[228:229], v[188:189], s[14:15], v[228:229] op_sel_hi:[1,0,1]
	v_pk_fma_f32 v[230:231], v[190:191], s[14:15], v[230:231] op_sel_hi:[1,0,1]
	v_cvt_pk_f32_fp8_e32 v[184:185], v30
	v_cvt_pk_f32_fp8_sdwa v[186:187], v30 src0_sel:WORD_1
	v_pk_fma_f32 v[232:233], v[184:185], s[14:15], v[232:233] op_sel_hi:[1,0,1]
	v_pk_fma_f32 v[234:235], v[186:187], s[14:15], v[234:235] op_sel_hi:[1,0,1]
	v_cvt_pk_f32_fp8_e32 v[188:189], v31
	v_cvt_pk_f32_fp8_sdwa v[190:191], v31 src0_sel:WORD_1
	v_pk_fma_f32 v[236:237], v[188:189], s[14:15], v[236:237] op_sel_hi:[1,0,1]
	v_pk_fma_f32 v[238:239], v[190:191], s[14:15], v[238:239] op_sel_hi:[1,0,1]
	s_cmp_le_u32 s36, 6
	s_cbranch_scc1 .Lp6c1_axdone
	v_readlane_b32 s14, v1, 48
	v_cvt_pk_f32_fp8_e32 v[184:185], v24
	v_cvt_pk_f32_fp8_sdwa v[186:187], v24 src0_sel:WORD_1
	v_pk_fma_f32 v[224:225], v[184:185], s[14:15], v[224:225] op_sel_hi:[1,0,1]
	v_pk_fma_f32 v[226:227], v[186:187], s[14:15], v[226:227] op_sel_hi:[1,0,1]
	v_cvt_pk_f32_fp8_e32 v[188:189], v25
	v_cvt_pk_f32_fp8_sdwa v[190:191], v25 src0_sel:WORD_1
	v_pk_fma_f32 v[228:229], v[188:189], s[14:15], v[228:229] op_sel_hi:[1,0,1]
	v_pk_fma_f32 v[230:231], v[190:191], s[14:15], v[230:231] op_sel_hi:[1,0,1]
	v_cvt_pk_f32_fp8_e32 v[184:185], v26
	v_cvt_pk_f32_fp8_sdwa v[186:187], v26 src0_sel:WORD_1
	v_pk_fma_f32 v[232:233], v[184:185], s[14:15], v[232:233] op_sel_hi:[1,0,1]
	v_pk_fma_f32 v[234:235], v[186:187], s[14:15], v[234:235] op_sel_hi:[1,0,1]
	v_cvt_pk_f32_fp8_e32 v[188:189], v27
	v_cvt_pk_f32_fp8_sdwa v[190:191], v27 src0_sel:WORD_1
	v_pk_fma_f32 v[236:237], v[188:189], s[14:15], v[236:237] op_sel_hi:[1,0,1]
	v_pk_fma_f32 v[238:239], v[190:191], s[14:15], v[238:239] op_sel_hi:[1,0,1]
	v_readlane_b32 s14, v1, 56
	v_cvt_pk_f32_fp8_e32 v[184:185], v20
	v_cvt_pk_f32_fp8_sdwa v[186:187], v20 src0_sel:WORD_1
	v_pk_fma_f32 v[224:225], v[184:185], s[14:15], v[224:225] op_sel_hi:[1,0,1]
	v_pk_fma_f32 v[226:227], v[186:187], s[14:15], v[226:227] op_sel_hi:[1,0,1]
	v_cvt_pk_f32_fp8_e32 v[188:189], v21
	v_cvt_pk_f32_fp8_sdwa v[190:191], v21 src0_sel:WORD_1
	v_pk_fma_f32 v[228:229], v[188:189], s[14:15], v[228:229] op_sel_hi:[1,0,1]
	v_pk_fma_f32 v[230:231], v[190:191], s[14:15], v[230:231] op_sel_hi:[1,0,1]
	v_cvt_pk_f32_fp8_e32 v[184:185], v22
	v_cvt_pk_f32_fp8_sdwa v[186:187], v22 src0_sel:WORD_1
	v_pk_fma_f32 v[232:233], v[184:185], s[14:15], v[232:233] op_sel_hi:[1,0,1]
	v_pk_fma_f32 v[234:235], v[186:187], s[14:15], v[234:235] op_sel_hi:[1,0,1]
	v_cvt_pk_f32_fp8_e32 v[188:189], v23
	v_cvt_pk_f32_fp8_sdwa v[190:191], v23 src0_sel:WORD_1
	v_pk_fma_f32 v[236:237], v[188:189], s[14:15], v[236:237] op_sel_hi:[1,0,1]
	v_pk_fma_f32 v[238:239], v[190:191], s[14:15], v[238:239] op_sel_hi:[1,0,1]
	s_branch .Lp6c1_axdone
.Lp6c1_t7:
	v_readlane_b32 s14, v1, 0
	v_cvt_pk_f32_fp8_e32 v[184:185], v72
	v_cvt_pk_f32_fp8_sdwa v[186:187], v72 src0_sel:WORD_1
	v_pk_fma_f32 v[240:241], v[184:185], s[14:15], v[240:241] op_sel_hi:[1,0,1]
	v_pk_fma_f32 v[242:243], v[186:187], s[14:15], v[242:243] op_sel_hi:[1,0,1]
	v_cvt_pk_f32_fp8_e32 v[188:189], v73
	v_cvt_pk_f32_fp8_sdwa v[190:191], v73 src0_sel:WORD_1
	v_pk_fma_f32 v[244:245], v[188:189], s[14:15], v[244:245] op_sel_hi:[1,0,1]
	v_pk_fma_f32 v[246:247], v[190:191], s[14:15], v[246:247] op_sel_hi:[1,0,1]
	v_cvt_pk_f32_fp8_e32 v[184:185], v74
	v_cvt_pk_f32_fp8_sdwa v[186:187], v74 src0_sel:WORD_1
	v_pk_fma_f32 v[248:249], v[184:185], s[14:15], v[248:249] op_sel_hi:[1,0,1]
	v_pk_fma_f32 v[250:251], v[186:187], s[14:15], v[250:251] op_sel_hi:[1,0,1]
	v_cvt_pk_f32_fp8_e32 v[188:189], v75
	v_cvt_pk_f32_fp8_sdwa v[190:191], v75 src0_sel:WORD_1
	v_pk_fma_f32 v[216:217], v[188:189], s[14:15], v[216:217] op_sel_hi:[1,0,1]
	v_pk_fma_f32 v[218:219], v[190:191], s[14:15], v[218:219] op_sel_hi:[1,0,1]
	v_readlane_b32 s14, v1, 8
	v_cvt_pk_f32_fp8_e32 v[184:185], v52
	v_cvt_pk_f32_fp8_sdwa v[186:187], v52 src0_sel:WORD_1
	v_pk_fma_f32 v[240:241], v[184:185], s[14:15], v[240:241] op_sel_hi:[1,0,1]
	v_pk_fma_f32 v[242:243], v[186:187], s[14:15], v[242:243] op_sel_hi:[1,0,1]
	v_cvt_pk_f32_fp8_e32 v[188:189], v53
	v_cvt_pk_f32_fp8_sdwa v[190:191], v53 src0_sel:WORD_1
	v_pk_fma_f32 v[244:245], v[188:189], s[14:15], v[244:245] op_sel_hi:[1,0,1]
	v_pk_fma_f32 v[246:247], v[190:191], s[14:15], v[246:247] op_sel_hi:[1,0,1]
	v_cvt_pk_f32_fp8_e32 v[184:185], v54
	v_cvt_pk_f32_fp8_sdwa v[186:187], v54 src0_sel:WORD_1
	v_pk_fma_f32 v[248:249], v[184:185], s[14:15], v[248:249] op_sel_hi:[1,0,1]
	v_pk_fma_f32 v[250:251], v[186:187], s[14:15], v[250:251] op_sel_hi:[1,0,1]
	v_cvt_pk_f32_fp8_e32 v[188:189], v55
	v_cvt_pk_f32_fp8_sdwa v[190:191], v55 src0_sel:WORD_1
	v_pk_fma_f32 v[216:217], v[188:189], s[14:15], v[216:217] op_sel_hi:[1,0,1]
	v_pk_fma_f32 v[218:219], v[190:191], s[14:15], v[218:219] op_sel_hi:[1,0,1]
	s_cmp_le_u32 s36, 2
	s_cbranch_scc1 .Lp6c1_axdone
	v_readlane_b32 s14, v1, 16
	v_cvt_pk_f32_fp8_e32 v[184:185], v44
	v_cvt_pk_f32_fp8_sdwa v[186:187], v44 src0_sel:WORD_1
	v_pk_fma_f32 v[240:241], v[184:185], s[14:15], v[240:241] op_sel_hi:[1,0,1]
	v_pk_fma_f32 v[242:243], v[186:187], s[14:15], v[242:243] op_sel_hi:[1,0,1]
	v_cvt_pk_f32_fp8_e32 v[188:189], v45
	v_cvt_pk_f32_fp8_sdwa v[190:191], v45 src0_sel:WORD_1
	v_pk_fma_f32 v[244:245], v[188:189], s[14:15], v[244:245] op_sel_hi:[1,0,1]
	v_pk_fma_f32 v[246:247], v[190:191], s[14:15], v[246:247] op_sel_hi:[1,0,1]
	v_cvt_pk_f32_fp8_e32 v[184:185], v46
	v_cvt_pk_f32_fp8_sdwa v[186:187], v46 src0_sel:WORD_1
	v_pk_fma_f32 v[248:249], v[184:185], s[14:15], v[248:249] op_sel_hi:[1,0,1]
	v_pk_fma_f32 v[250:251], v[186:187], s[14:15], v[250:251] op_sel_hi:[1,0,1]
	v_cvt_pk_f32_fp8_e32 v[188:189], v47
	v_cvt_pk_f32_fp8_sdwa v[190:191], v47 src0_sel:WORD_1
	v_pk_fma_f32 v[216:217], v[188:189], s[14:15], v[216:217] op_sel_hi:[1,0,1]
	v_pk_fma_f32 v[218:219], v[190:191], s[14:15], v[218:219] op_sel_hi:[1,0,1]
	v_readlane_b32 s14, v1, 24
	v_cvt_pk_f32_fp8_e32 v[184:185], v40
	v_cvt_pk_f32_fp8_sdwa v[186:187], v40 src0_sel:WORD_1
	v_pk_fma_f32 v[240:241], v[184:185], s[14:15], v[240:241] op_sel_hi:[1,0,1]
	v_pk_fma_f32 v[242:243], v[186:187], s[14:15], v[242:243] op_sel_hi:[1,0,1]
	v_cvt_pk_f32_fp8_e32 v[188:189], v41
	v_cvt_pk_f32_fp8_sdwa v[190:191], v41 src0_sel:WORD_1
	v_pk_fma_f32 v[244:245], v[188:189], s[14:15], v[244:245] op_sel_hi:[1,0,1]
	v_pk_fma_f32 v[246:247], v[190:191], s[14:15], v[246:247] op_sel_hi:[1,0,1]
	v_cvt_pk_f32_fp8_e32 v[184:185], v42
	v_cvt_pk_f32_fp8_sdwa v[186:187], v42 src0_sel:WORD_1
	v_pk_fma_f32 v[248:249], v[184:185], s[14:15], v[248:249] op_sel_hi:[1,0,1]
	v_pk_fma_f32 v[250:251], v[186:187], s[14:15], v[250:251] op_sel_hi:[1,0,1]
	v_cvt_pk_f32_fp8_e32 v[188:189], v43
	v_cvt_pk_f32_fp8_sdwa v[190:191], v43 src0_sel:WORD_1
	v_pk_fma_f32 v[216:217], v[188:189], s[14:15], v[216:217] op_sel_hi:[1,0,1]
	v_pk_fma_f32 v[218:219], v[190:191], s[14:15], v[218:219] op_sel_hi:[1,0,1]
	s_cmp_le_u32 s36, 4
	s_cbranch_scc1 .Lp6c1_axdone
	v_readlane_b32 s14, v1, 32
	v_cvt_pk_f32_fp8_e32 v[184:185], v36
	v_cvt_pk_f32_fp8_sdwa v[186:187], v36 src0_sel:WORD_1
	v_pk_fma_f32 v[240:241], v[184:185], s[14:15], v[240:241] op_sel_hi:[1,0,1]
	v_pk_fma_f32 v[242:243], v[186:187], s[14:15], v[242:243] op_sel_hi:[1,0,1]
	v_cvt_pk_f32_fp8_e32 v[188:189], v37
	v_cvt_pk_f32_fp8_sdwa v[190:191], v37 src0_sel:WORD_1
	v_pk_fma_f32 v[244:245], v[188:189], s[14:15], v[244:245] op_sel_hi:[1,0,1]
	v_pk_fma_f32 v[246:247], v[190:191], s[14:15], v[246:247] op_sel_hi:[1,0,1]
	v_cvt_pk_f32_fp8_e32 v[184:185], v38
	v_cvt_pk_f32_fp8_sdwa v[186:187], v38 src0_sel:WORD_1
	v_pk_fma_f32 v[248:249], v[184:185], s[14:15], v[248:249] op_sel_hi:[1,0,1]
	v_pk_fma_f32 v[250:251], v[186:187], s[14:15], v[250:251] op_sel_hi:[1,0,1]
	v_cvt_pk_f32_fp8_e32 v[188:189], v39
	v_cvt_pk_f32_fp8_sdwa v[190:191], v39 src0_sel:WORD_1
	v_pk_fma_f32 v[216:217], v[188:189], s[14:15], v[216:217] op_sel_hi:[1,0,1]
	v_pk_fma_f32 v[218:219], v[190:191], s[14:15], v[218:219] op_sel_hi:[1,0,1]
	v_readlane_b32 s14, v1, 40
	v_cvt_pk_f32_fp8_e32 v[184:185], v28
	v_cvt_pk_f32_fp8_sdwa v[186:187], v28 src0_sel:WORD_1
	v_pk_fma_f32 v[240:241], v[184:185], s[14:15], v[240:241] op_sel_hi:[1,0,1]
	v_pk_fma_f32 v[242:243], v[186:187], s[14:15], v[242:243] op_sel_hi:[1,0,1]
	v_cvt_pk_f32_fp8_e32 v[188:189], v29
	v_cvt_pk_f32_fp8_sdwa v[190:191], v29 src0_sel:WORD_1
	v_pk_fma_f32 v[244:245], v[188:189], s[14:15], v[244:245] op_sel_hi:[1,0,1]
	v_pk_fma_f32 v[246:247], v[190:191], s[14:15], v[246:247] op_sel_hi:[1,0,1]
	v_cvt_pk_f32_fp8_e32 v[184:185], v30
	v_cvt_pk_f32_fp8_sdwa v[186:187], v30 src0_sel:WORD_1
	v_pk_fma_f32 v[248:249], v[184:185], s[14:15], v[248:249] op_sel_hi:[1,0,1]
	v_pk_fma_f32 v[250:251], v[186:187], s[14:15], v[250:251] op_sel_hi:[1,0,1]
	v_cvt_pk_f32_fp8_e32 v[188:189], v31
	v_cvt_pk_f32_fp8_sdwa v[190:191], v31 src0_sel:WORD_1
	v_pk_fma_f32 v[216:217], v[188:189], s[14:15], v[216:217] op_sel_hi:[1,0,1]
	v_pk_fma_f32 v[218:219], v[190:191], s[14:15], v[218:219] op_sel_hi:[1,0,1]
	s_cmp_le_u32 s36, 6
	s_cbranch_scc1 .Lp6c1_axdone
	v_readlane_b32 s14, v1, 48
	v_cvt_pk_f32_fp8_e32 v[184:185], v24
	v_cvt_pk_f32_fp8_sdwa v[186:187], v24 src0_sel:WORD_1
	v_pk_fma_f32 v[240:241], v[184:185], s[14:15], v[240:241] op_sel_hi:[1,0,1]
	v_pk_fma_f32 v[242:243], v[186:187], s[14:15], v[242:243] op_sel_hi:[1,0,1]
	v_cvt_pk_f32_fp8_e32 v[188:189], v25
	v_cvt_pk_f32_fp8_sdwa v[190:191], v25 src0_sel:WORD_1
	v_pk_fma_f32 v[244:245], v[188:189], s[14:15], v[244:245] op_sel_hi:[1,0,1]
	v_pk_fma_f32 v[246:247], v[190:191], s[14:15], v[246:247] op_sel_hi:[1,0,1]
	v_cvt_pk_f32_fp8_e32 v[184:185], v26
	v_cvt_pk_f32_fp8_sdwa v[186:187], v26 src0_sel:WORD_1
	v_pk_fma_f32 v[248:249], v[184:185], s[14:15], v[248:249] op_sel_hi:[1,0,1]
	v_pk_fma_f32 v[250:251], v[186:187], s[14:15], v[250:251] op_sel_hi:[1,0,1]
	v_cvt_pk_f32_fp8_e32 v[188:189], v27
	v_cvt_pk_f32_fp8_sdwa v[190:191], v27 src0_sel:WORD_1
	v_pk_fma_f32 v[216:217], v[188:189], s[14:15], v[216:217] op_sel_hi:[1,0,1]
	v_pk_fma_f32 v[218:219], v[190:191], s[14:15], v[218:219] op_sel_hi:[1,0,1]
	v_readlane_b32 s14, v1, 56
	v_cvt_pk_f32_fp8_e32 v[184:185], v20
	v_cvt_pk_f32_fp8_sdwa v[186:187], v20 src0_sel:WORD_1
	v_pk_fma_f32 v[240:241], v[184:185], s[14:15], v[240:241] op_sel_hi:[1,0,1]
	v_pk_fma_f32 v[242:243], v[186:187], s[14:15], v[242:243] op_sel_hi:[1,0,1]
	v_cvt_pk_f32_fp8_e32 v[188:189], v21
	v_cvt_pk_f32_fp8_sdwa v[190:191], v21 src0_sel:WORD_1
	v_pk_fma_f32 v[244:245], v[188:189], s[14:15], v[244:245] op_sel_hi:[1,0,1]
	v_pk_fma_f32 v[246:247], v[190:191], s[14:15], v[246:247] op_sel_hi:[1,0,1]
	v_cvt_pk_f32_fp8_e32 v[184:185], v22
	v_cvt_pk_f32_fp8_sdwa v[186:187], v22 src0_sel:WORD_1
	v_pk_fma_f32 v[248:249], v[184:185], s[14:15], v[248:249] op_sel_hi:[1,0,1]
	v_pk_fma_f32 v[250:251], v[186:187], s[14:15], v[250:251] op_sel_hi:[1,0,1]
	v_cvt_pk_f32_fp8_e32 v[188:189], v23
	v_cvt_pk_f32_fp8_sdwa v[190:191], v23 src0_sel:WORD_1
	v_pk_fma_f32 v[216:217], v[188:189], s[14:15], v[216:217] op_sel_hi:[1,0,1]
	v_pk_fma_f32 v[218:219], v[190:191], s[14:15], v[218:219] op_sel_hi:[1,0,1]
	s_branch .Lp6c1_axdone
.Lp6c1_axdone:
	s_nop 4
	buffer_load_dwordx4 v[72:75], v181, s[92:95], s44 offen
	buffer_load_dwordx4 v[52:55], v181, s[92:95], s45 offen
	buffer_load_dwordx4 v[44:47], v181, s[92:95], s46 offen
	buffer_load_dwordx4 v[40:43], v181, s[92:95], s47 offen
	buffer_load_dwordx4 v[36:39], v181, s[92:95], s48 offen
	buffer_load_dwordx4 v[28:31], v181, s[92:95], s49 offen
	buffer_load_dwordx4 v[24:27], v181, s[92:95], s50 offen
	buffer_load_dwordx4 v[20:23], v181, s[92:95], s51 offen
	s_mov_b32 s26, s86
	s_mov_b32 s86, s32
	s_mov_b32 s32, s37
	s_cmp_eq_u32 s22, s23
	s_cbranch_scc1 .Lp6_B8done
	s_branch .Lp6c0_top
.Lp6_B8done:
	s_mov_b32 s2, 0
	s_mov_b64 s[6:7], -1
	s_or_b32 s96, s2, s33
	s_ashr_i32 s97, s96, 31
	v_and_b32_e32 v183, 64, v178
	s_mov_b32 s86, 0x19000
	s_branch .LBB0_975

.LBB0_938:
	v_mov_b64_e32 v[126:127], v[144:145]
	v_mov_b64_e32 v[128:129], v[146:147]
	v_mov_b64_e32 v[130:131], v[148:149]
	v_mov_b64_e32 v[132:133], v[150:151]
	v_mov_b64_e32 v[134:135], v[152:153]
	v_mov_b64_e32 v[136:137], v[154:155]
	v_mov_b64_e32 v[138:139], v[156:157]
	v_mov_b64_e32 v[140:141], v[158:159]
	v_mov_b64_e32 v[110:111], v[160:161]
	v_mov_b64_e32 v[112:113], v[162:163]
	v_mov_b64_e32 v[114:115], v[164:165]
	v_mov_b64_e32 v[116:117], v[166:167]
	v_mov_b64_e32 v[118:119], v[168:169]
	v_mov_b64_e32 v[120:121], v[170:171]
	v_mov_b64_e32 v[122:123], v[172:173]
	v_mov_b64_e32 v[124:125], v[174:175]
	v_mov_b64_e32 v[94:95], v[224:225]
	v_mov_b64_e32 v[96:97], v[226:227]
	v_mov_b64_e32 v[98:99], v[228:229]
	v_mov_b64_e32 v[100:101], v[230:231]
	v_mov_b64_e32 v[102:103], v[232:233]
	v_mov_b64_e32 v[104:105], v[234:235]
	v_mov_b64_e32 v[106:107], v[236:237]
	v_mov_b64_e32 v[108:109], v[238:239]
	v_mov_b64_e32 v[78:79], v[240:241]
	v_mov_b64_e32 v[80:81], v[242:243]
	v_mov_b64_e32 v[82:83], v[244:245]
	v_mov_b64_e32 v[86:87], v[246:247]
	v_mov_b64_e32 v[88:89], v[248:249]
	v_mov_b64_e32 v[90:91], v[250:251]
	v_mov_b64_e32 v[92:93], v[216:217]
	v_mov_b64_e32 v[84:85], v[218:219]
	s_or_b32 s96, s2, s33
	s_ashr_i32 s97, s96, 31
	v_and_b32_e32 v183, 64, v178
	s_mov_b32 s86, 0x19000
	s_branch .LBB0_975
